# removed adjacent s_setprio 0 / s_setprio 1 pairs between the two MFMA clusters of each compute segment (48 sites)
# baseline (speedup 1.0000x reference)
; #define G_STAGE(bufoff, gbase, voff) do { _Pragma("unroll") for (int _i = 0; _i < 2; ++_i) \
;         __builtin_amdgcn_global_load_lds((const unsigned*)((const char*)(gbase) + (voff)[_i]), (LAS unsigned*)(lds + (bufoff) + ldsw + _i * 8192), 16, 0, 0); } while (0)
; #define G_LDA(dst, b, h) do { _Pragma("unroll") for (int m = 0; m < 4; ++m) G_LD8(dst[m], lds + G_SA(b, h) + aoff + m * 2048); } while (0)
; #define G_LDB(dst, b, h) do { _Pragma("unroll") for (int n = 0; n < 2; ++n) G_LD8(dst[n], lds + G_SB(b, h) + boff + n * 2048); } while (0)
; #define G_WAIT_V(n) asm volatile("s_waitcnt vmcnt(" #n ")" ::: "memory")
; #define G_WAIT_L(n) asm volatile("s_waitcnt lgkmcnt(" #n ")" ::: "memory")
; #define G_BAR __builtin_amdgcn_s_barrier()
; #define G_SCHED __builtin_amdgcn_sched_barrier(0)
;     __device__ __forceinline__ unsigned row_off(const Unit& u, int r, LAS unsigned char* lds) const { return (unsigned)((const LAS int*)(lds + LDS_STAGE + u.q * 4096))[r] * (unsigned)rowbytes; }
;     ...
;             const char* a11 = cur.a1 + (size_t)(t + 1) * kstep;
;             const char* a02 = last ? nxt.a0 : cur.a0 + (size_t)(t + 2) * kstep; const char* a12 = last ? nxt.a1 : cur.a1 + (size_t)(t + 2) * kstep;
;             const char* b02 = last ? nxt.b0 : cur.b0 + (size_t)(t + 2) * kstep; const char* b12 = last ? nxt.b1 : cur.b1 + (size_t)(t + 2) * kstep;
;             G_LDB(B0, 0, 0); G_LDB(B1, 0, 1); G_SCHED; G_LDA(At, 0, 0); G_STAGE(G_SA(1, 1), a11, vA1);
;             if constexpr (GATHER) { if (last) { int tz = tid; asm volatile("" : "+v"(tz));
; #pragma unroll
;                 for (int i = 0; i < 2; ++i) { int R, C; stage_rc(tz * 16 + i * 8192, R, C); gc0[i] = S.row_off(nxt, R, lds) + (unsigned)C * 2u; gc1[i] = S.row_off(nxt, 128 + R, lds) + (unsigned)C * 2u; } } }
;             G_WAIT_L(0); G_BAR; G_MMA(0, 0, At, B0); G_MMA(0, 1, At, B1); G_WAIT_V(8); G_BAR; G_SCHED;
;             G_LDA(At, 0, 1); G_STAGE(G_SB(0, 0), b02, voffB); G_STAGE(G_SB(0, 1), b12, voffB); G_STAGE(G_SA(0, 0), a02, vA0);
.LBB0_179:
	v_add_u32_e32 v144, s91, v163
	v_add_u32_e32 v170, s3, v163
	ds_read_b128 v[34:37], v144
	ds_read_b128 v[38:41], v144 offset:1024
	ds_read_b128 v[42:45], v144 offset:2048
	ds_read_b128 v[144:147], v144 offset:3072
	ds_read_b128 v[150:153], v170
	ds_read_b128 v[154:157], v170 offset:1024
	ds_read_b128 v[166:169], v170 offset:2048
	ds_read_b128 v[170:173], v170 offset:3072
	s_add_i32 s63, s59, 2
	s_add_u32 s73, s74, 0x80
	s_addc_u32 s76, s75, 0
	s_add_i32 s83, s91, s97
	s_add_i32 m0, s22, 0xc000
	s_add_i32 s82, s22, 0xe000
	s_add_i32 s89, s83, 0x2000
	s_cmp_eq_u32 s20, s59
	s_cselect_b32 s79, s65, s33
	s_cselect_b32 s78, s64, s19
	s_cselect_b32 s81, s69, s2
	s_cselect_b32 s80, s68, s0
	s_cselect_b32 s77, s67, s76
	s_cselect_b32 s76, s66, s73
	ds_read_b128 v[174:177], v164
	ds_read_b128 v[178:181], v164 offset:1024
	ds_read_b128 v[182:185], v164 offset:2048
	ds_read_b128 v[186:189], v164 offset:3072
	ds_read_b128 v[190:193], v164 offset:4096
	ds_read_b128 v[194:197], v164 offset:5120
	ds_read_b128 v[198:201], v164 offset:6144
	ds_read_b128 v[202:205], v164 offset:7168
	global_load_lds_dwordx4 v240, s[74:75]
	s_mov_b32 m0, s82
	s_nop 0
	global_load_lds_dwordx4 v242, s[74:75]
	s_waitcnt lgkmcnt(0)
	v_mov_b32_e32 v33, v149
	s_barrier
	s_setprio 1
	s_waitcnt lgkmcnt(0)
	v_mfma_i32_16x16x64_i8 v[140:143], v[34:37], v[174:177], v[140:143]
	v_mfma_i32_16x16x64_i8 v[132:135], v[42:45], v[174:177], v[132:135]
	v_mfma_i32_16x16x64_i8 v[124:127], v[34:37], v[182:185], v[124:127]
	v_mfma_i32_16x16x64_i8 v[116:119], v[42:45], v[182:185], v[116:119]
	v_mfma_i32_16x16x64_i8 v[108:111], v[34:37], v[190:193], v[108:111]
	v_mfma_i32_16x16x64_i8 v[100:103], v[42:45], v[190:193], v[100:103]
	v_mfma_i32_16x16x64_i8 v[92:95], v[34:37], v[198:201], v[92:95]
	v_mfma_i32_16x16x64_i8 v[84:87], v[42:45], v[198:201], v[84:87]
	v_mfma_i32_16x16x64_i8 v[140:143], v[38:41], v[178:181], v[140:143]
	v_mfma_i32_16x16x64_i8 v[132:135], v[144:147], v[178:181], v[132:135]
	v_mfma_i32_16x16x64_i8 v[124:127], v[38:41], v[186:189], v[124:127]
	v_mfma_i32_16x16x64_i8 v[116:119], v[144:147], v[186:189], v[116:119]
	v_mfma_i32_16x16x64_i8 v[108:111], v[38:41], v[194:197], v[108:111]
	v_mfma_i32_16x16x64_i8 v[100:103], v[144:147], v[194:197], v[100:103]
	v_mfma_i32_16x16x64_i8 v[92:95], v[38:41], v[202:205], v[92:95]
	v_mfma_i32_16x16x64_i8 v[84:87], v[144:147], v[202:205], v[84:87]
	v_mfma_i32_16x16x64_i8 v[136:139], v[150:153], v[174:177], v[136:139]
	v_mfma_i32_16x16x64_i8 v[128:131], v[166:169], v[174:177], v[128:131]
	v_mfma_i32_16x16x64_i8 v[120:123], v[150:153], v[182:185], v[120:123]
	v_mfma_i32_16x16x64_i8 v[112:115], v[166:169], v[182:185], v[112:115]
	v_mfma_i32_16x16x64_i8 v[104:107], v[150:153], v[190:193], v[104:107]
	v_mfma_i32_16x16x64_i8 v[96:99], v[166:169], v[190:193], v[96:99]
	v_mfma_i32_16x16x64_i8 v[88:91], v[150:153], v[198:201], v[88:91]
	v_mfma_i32_16x16x64_i8 v[80:83], v[166:169], v[198:201], v[80:83]
	v_mfma_i32_16x16x64_i8 v[136:139], v[154:157], v[178:181], v[136:139]
	v_mfma_i32_16x16x64_i8 v[128:131], v[170:173], v[178:181], v[128:131]
	v_mfma_i32_16x16x64_i8 v[120:123], v[154:157], v[186:189], v[120:123]
	v_mfma_i32_16x16x64_i8 v[112:115], v[170:173], v[186:189], v[112:115]
	v_mfma_i32_16x16x64_i8 v[104:107], v[154:157], v[194:197], v[104:107]
	v_mfma_i32_16x16x64_i8 v[96:99], v[170:173], v[194:197], v[96:99]
	v_mfma_i32_16x16x64_i8 v[88:91], v[154:157], v[202:205], v[88:91]
	v_mfma_i32_16x16x64_i8 v[80:83], v[170:173], v[202:205], v[80:83]
	s_setprio 0
	s_waitcnt vmcnt(8)
	s_barrier
	s_mov_b32 m0, s83
	ds_read_b128 v[174:177], v164 offset:16384
	ds_read_b128 v[178:181], v164 offset:17408
	ds_read_b128 v[182:185], v164 offset:18432
	ds_read_b128 v[186:189], v164 offset:19456
	ds_read_b128 v[190:193], v164 offset:20480
	ds_read_b128 v[194:197], v164 offset:21504
	ds_read_b128 v[198:201], v164 offset:22528
	ds_read_b128 v[202:205], v164 offset:23552
	v_mov_b32_e32 v47, v149
	global_load_lds_dwordx4 v244, s[80:81]
	v_mov_b32_e32 v159, v149
	s_mov_b32 m0, s89
	v_lshl_add_u64 v[206:207], s[80:81], 0, v[244:245]
	v_lshl_add_u64 v[208:209], s[80:81], 0, v[246:247]
	global_load_lds_dwordx4 v246, s[80:81]
	s_cselect_b32 s81, s71, s6
	s_cselect_b32 s80, s70, s5
	s_add_i32 s59, s3, s97
	s_mov_b32 m0, s59
	v_lshl_add_u64 v[210:211], s[80:81], 0, v[244:245]
	global_load_lds_dwordx4 v244, s[80:81]
	s_add_i32 m0, s59, 0x2000
	v_lshl_add_u64 v[212:213], s[80:81], 0, v[246:247]
	global_load_lds_dwordx4 v246, s[80:81]
	s_mov_b32 m0, s22
	v_lshl_add_u64 v[158:159], s[78:79], 0, v[240:241]
	global_load_lds_dwordx4 v240, s[78:79]
	s_mov_b32 m0, s23
	v_lshl_add_u64 v[214:215], s[78:79], 0, v[242:243]
	global_load_lds_dwordx4 v242, s[78:79]
	s_waitcnt lgkmcnt(0)
	s_barrier
; #define G_STAGE(bufoff, gbase, voff) do { _Pragma("unroll") for (int _i = 0; _i < 2; ++_i) \
;         __builtin_amdgcn_global_load_lds((const unsigned*)((const char*)(gbase) + (voff)[_i]), (LAS unsigned*)(lds + (bufoff) + ldsw + _i * 8192), 16, 0, 0); } while (0)
; #define G_LDA(dst, b, h) do { _Pragma("unroll") for (int m = 0; m < 4; ++m) G_LD8(dst[m], lds + G_SA(b, h) + aoff + m * 2048); } while (0)
; #define G_LDB(dst, b, h) do { _Pragma("unroll") for (int n = 0; n < 2; ++n) G_LD8(dst[n], lds + G_SB(b, h) + boff + n * 2048); } while (0)
; #define G_WAIT_V(n) asm volatile("s_waitcnt vmcnt(" #n ")" ::: "memory")
; #define G_WAIT_L(n) asm volatile("s_waitcnt lgkmcnt(" #n ")" ::: "memory")
; #define G_BAR __builtin_amdgcn_s_barrier()
; #define G_SCHED __builtin_amdgcn_sched_barrier(0)
;     ...
;             G_WAIT_L(0); G_BAR; G_MMA(1, 0, At, B0); G_MMA(1, 1, At, B1); G_WAIT_V(8); G_BAR; G_SCHED;
;             G_LDB(B0, 1, 0); G_LDB(B1, 1, 1); G_SCHED; G_LDA(At, 1, 0); G_STAGE(G_SA(0, 1), a12, vA1);
;             G_WAIT_L(0); G_BAR; G_MMA(0, 0, At, B0); G_MMA(0, 1, At, B1); G_WAIT_V(8); G_BAR; G_SCHED;
	s_setprio 1
	s_waitcnt lgkmcnt(0)
	v_mfma_i32_16x16x64_i8 v[76:79], v[34:37], v[174:177], v[76:79]
	v_mfma_i32_16x16x64_i8 v[68:71], v[42:45], v[174:177], v[68:71]
	v_mfma_i32_16x16x64_i8 v[60:63], v[34:37], v[182:185], v[60:63]
	v_mfma_i32_16x16x64_i8 v[52:55], v[42:45], v[182:185], v[52:55]
	v_mfma_i32_16x16x64_i8 v[28:31], v[34:37], v[190:193], v[28:31]
	v_mfma_i32_16x16x64_i8 v[20:23], v[42:45], v[190:193], v[20:23]
	v_mfma_i32_16x16x64_i8 v[12:15], v[34:37], v[198:201], v[12:15]
	v_mfma_i32_16x16x64_i8 v[4:7], v[42:45], v[198:201], v[4:7]
	v_mfma_i32_16x16x64_i8 v[76:79], v[38:41], v[178:181], v[76:79]
	v_mfma_i32_16x16x64_i8 v[68:71], v[144:147], v[178:181], v[68:71]
	v_mfma_i32_16x16x64_i8 v[60:63], v[38:41], v[186:189], v[60:63]
	v_mfma_i32_16x16x64_i8 v[52:55], v[144:147], v[186:189], v[52:55]
	v_mfma_i32_16x16x64_i8 v[28:31], v[38:41], v[194:197], v[28:31]
	v_mfma_i32_16x16x64_i8 v[20:23], v[144:147], v[194:197], v[20:23]
	v_mfma_i32_16x16x64_i8 v[12:15], v[38:41], v[202:205], v[12:15]
	v_mfma_i32_16x16x64_i8 v[4:7], v[144:147], v[202:205], v[4:7]
	v_mfma_i32_16x16x64_i8 v[46:49], v[166:169], v[182:185], v[48:51]
	v_mfma_i32_16x16x64_i8 v[24:27], v[150:153], v[190:193], v[24:27]
	v_mfma_i32_16x16x64_i8 v[16:19], v[166:169], v[190:193], v[16:19]
	v_mfma_i32_16x16x64_i8 v[8:11], v[150:153], v[198:201], v[8:11]
	v_mfma_i32_16x16x64_i8 v[0:3], v[166:169], v[198:201], v[0:3]
	v_mfma_i32_16x16x64_i8 v[34:37], v[150:153], v[174:177], v[72:75]
	v_mfma_i32_16x16x64_i8 v[38:41], v[166:169], v[174:177], v[64:67]
	v_mfma_i32_16x16x64_i8 v[42:45], v[150:153], v[182:185], v[56:59]
	v_mfma_i32_16x16x64_i8 v[46:49], v[170:173], v[186:189], v[46:49]
	v_mfma_i32_16x16x64_i8 v[24:27], v[154:157], v[194:197], v[24:27]
	v_mfma_i32_16x16x64_i8 v[16:19], v[170:173], v[194:197], v[16:19]
	v_mfma_i32_16x16x64_i8 v[8:11], v[154:157], v[202:205], v[8:11]
	v_mfma_i32_16x16x64_i8 v[0:3], v[170:173], v[202:205], v[0:3]
	v_mfma_i32_16x16x64_i8 v[34:37], v[154:157], v[178:181], v[34:37]
	v_mfma_i32_16x16x64_i8 v[38:41], v[170:173], v[178:181], v[38:41]
	v_mfma_i32_16x16x64_i8 v[42:45], v[154:157], v[186:189], v[42:45]
	s_setprio 0
	s_waitcnt vmcnt(8)
	s_barrier
	s_add_i32 s59, 0, 0x18000
	v_add_u32_e32 v33, s59, v163
	s_add_i32 s73, 0, 0x1c000
	ds_read_b128 v[56:59], v33
	ds_read_b128 v[64:67], v33 offset:1024
	ds_read_b128 v[72:75], v33 offset:2048
	ds_read_b128 v[144:147], v33 offset:3072
	v_add_u32_e32 v33, s73, v163
	ds_read_b128 v[150:153], v33
	ds_read_b128 v[154:157], v33 offset:1024
	ds_read_b128 v[166:169], v33 offset:2048
	ds_read_b128 v[170:173], v33 offset:3072
	s_mov_b32 m0, s55
	ds_read_b128 v[174:177], v164 offset:32768
	ds_read_b128 v[178:181], v164 offset:33792
	ds_read_b128 v[182:185], v164 offset:34816
	ds_read_b128 v[186:189], v164 offset:35840
	ds_read_b128 v[190:193], v164 offset:36864
	ds_read_b128 v[194:197], v164 offset:37888
	ds_read_b128 v[198:201], v164 offset:38912
	ds_read_b128 v[202:205], v164 offset:39936
	global_load_lds_dwordx4 v240, s[76:77]
	s_mov_b32 m0, s84
	s_nop 0
	global_load_lds_dwordx4 v242, s[76:77]
	s_waitcnt lgkmcnt(0)
	s_barrier
	s_setprio 1
	s_waitcnt lgkmcnt(0)
	v_mfma_i32_16x16x64_i8 v[140:143], v[56:59], v[174:177], v[140:143]
	v_mfma_i32_16x16x64_i8 v[132:135], v[72:75], v[174:177], v[132:135]
	v_mfma_i32_16x16x64_i8 v[124:127], v[56:59], v[182:185], v[124:127]
	v_mfma_i32_16x16x64_i8 v[116:119], v[72:75], v[182:185], v[116:119]
	v_mfma_i32_16x16x64_i8 v[108:111], v[56:59], v[190:193], v[108:111]
	v_mfma_i32_16x16x64_i8 v[100:103], v[72:75], v[190:193], v[100:103]
	v_mfma_i32_16x16x64_i8 v[92:95], v[56:59], v[198:201], v[92:95]
	v_mfma_i32_16x16x64_i8 v[84:87], v[72:75], v[198:201], v[84:87]
	v_mfma_i32_16x16x64_i8 v[140:143], v[64:67], v[178:181], v[140:143]
	v_mfma_i32_16x16x64_i8 v[132:135], v[144:147], v[178:181], v[132:135]
	v_mfma_i32_16x16x64_i8 v[124:127], v[64:67], v[186:189], v[124:127]
	v_mfma_i32_16x16x64_i8 v[116:119], v[144:147], v[186:189], v[116:119]
	v_mfma_i32_16x16x64_i8 v[108:111], v[64:67], v[194:197], v[108:111]
	v_mfma_i32_16x16x64_i8 v[100:103], v[144:147], v[194:197], v[100:103]
	v_mfma_i32_16x16x64_i8 v[92:95], v[64:67], v[202:205], v[92:95]
	v_mfma_i32_16x16x64_i8 v[84:87], v[144:147], v[202:205], v[84:87]
	v_mfma_i32_16x16x64_i8 v[136:139], v[150:153], v[174:177], v[136:139]
	v_mfma_i32_16x16x64_i8 v[128:131], v[166:169], v[174:177], v[128:131]
	v_mfma_i32_16x16x64_i8 v[120:123], v[150:153], v[182:185], v[120:123]
	v_mfma_i32_16x16x64_i8 v[112:115], v[166:169], v[182:185], v[112:115]
	v_mfma_i32_16x16x64_i8 v[104:107], v[150:153], v[190:193], v[104:107]
	v_mfma_i32_16x16x64_i8 v[96:99], v[166:169], v[190:193], v[96:99]
	v_mfma_i32_16x16x64_i8 v[88:91], v[150:153], v[198:201], v[88:91]
	v_mfma_i32_16x16x64_i8 v[80:83], v[166:169], v[198:201], v[80:83]
	v_mfma_i32_16x16x64_i8 v[136:139], v[154:157], v[178:181], v[136:139]
	v_mfma_i32_16x16x64_i8 v[128:131], v[170:173], v[178:181], v[128:131]
	v_mfma_i32_16x16x64_i8 v[120:123], v[154:157], v[186:189], v[120:123]
	v_mfma_i32_16x16x64_i8 v[112:115], v[170:173], v[186:189], v[112:115]
	v_mfma_i32_16x16x64_i8 v[104:107], v[154:157], v[194:197], v[104:107]
	v_mfma_i32_16x16x64_i8 v[96:99], v[170:173], v[194:197], v[96:99]
	v_mfma_i32_16x16x64_i8 v[88:91], v[154:157], v[202:205], v[88:91]
	v_mfma_i32_16x16x64_i8 v[80:83], v[170:173], v[202:205], v[80:83]
	s_setprio 0
	s_waitcnt vmcnt(8)
	s_barrier
; #define G_STAGE(bufoff, gbase, voff) do { _Pragma("unroll") for (int _i = 0; _i < 2; ++_i) \
;         __builtin_amdgcn_global_load_lds((const unsigned*)((const char*)(gbase) + (voff)[_i]), (LAS unsigned*)(lds + (bufoff) + ldsw + _i * 8192), 16, 0, 0); } while (0)
; #define G_LDA(dst, b, h) do { _Pragma("unroll") for (int m = 0; m < 4; ++m) G_LD8(dst[m], lds + G_SA(b, h) + aoff + m * 2048); } while (0)
; #define G_WAIT_V(n) asm volatile("s_waitcnt vmcnt(" #n ")" ::: "memory")
; #define G_WAIT_L(n) asm volatile("s_waitcnt lgkmcnt(" #n ")" ::: "memory")
; #define G_BAR __builtin_amdgcn_s_barrier()
; #define G_SCHED __builtin_amdgcn_sched_barrier(0)
;     ...
;             G_LDA(At, 1, 1); G_STAGE(G_SB(1, 0), b02 + kstep, voffB); G_STAGE(G_SB(1, 1), b12 + kstep, voffB); G_STAGE(G_SA(1, 0), a02 + kstep, vA0);
;             G_WAIT_L(0); G_BAR; G_MMA(1, 0, At, B0); G_MMA(1, 1, At, B1); G_WAIT_V(8); G_BAR; G_SCHED;
;         }
	s_add_i32 s59, s59, s97
	v_lshl_add_u64 v[32:33], v[206:207], 0, s[46:47]
	s_mov_b32 m0, s59
	ds_read_b128 v[174:177], v164 offset:49152
	ds_read_b128 v[178:181], v164 offset:50176
	ds_read_b128 v[182:185], v164 offset:51200
	ds_read_b128 v[186:189], v164 offset:52224
	ds_read_b128 v[190:193], v164 offset:53248
	ds_read_b128 v[194:197], v164 offset:54272
	ds_read_b128 v[198:201], v164 offset:55296
	ds_read_b128 v[202:205], v164 offset:56320
	global_load_lds_dwordx4 v[32:33], off
	v_lshl_add_u64 v[32:33], v[208:209], 0, s[46:47]
	s_add_i32 m0, s59, 0x2000
	s_add_i32 s59, s73, s97
	global_load_lds_dwordx4 v[32:33], off
	v_lshl_add_u64 v[32:33], v[210:211], 0, s[46:47]
	s_mov_b32 m0, s59
	s_nop 0
	global_load_lds_dwordx4 v[32:33], off
	v_lshl_add_u64 v[32:33], v[212:213], 0, s[46:47]
	s_add_i32 m0, s59, 0x2000
	s_nop 0
	global_load_lds_dwordx4 v[32:33], off
	v_lshl_add_u64 v[32:33], v[158:159], 0, s[46:47]
	s_mov_b32 m0, s86
	s_nop 0
	global_load_lds_dwordx4 v[32:33], off
	v_lshl_add_u64 v[32:33], v[214:215], 0, s[46:47]
	s_mov_b32 m0, s87
	s_nop 0
	global_load_lds_dwordx4 v[32:33], off
	s_waitcnt lgkmcnt(0)
	s_barrier
	s_setprio 1
	s_waitcnt lgkmcnt(0)
	v_mfma_i32_16x16x64_i8 v[76:79], v[56:59], v[174:177], v[76:79]
	v_mfma_i32_16x16x64_i8 v[68:71], v[72:75], v[174:177], v[68:71]
	v_mfma_i32_16x16x64_i8 v[60:63], v[56:59], v[182:185], v[60:63]
	v_mfma_i32_16x16x64_i8 v[50:53], v[72:75], v[182:185], v[52:55]
	v_mfma_i32_16x16x64_i8 v[28:31], v[56:59], v[190:193], v[28:31]
	v_mfma_i32_16x16x64_i8 v[20:23], v[72:75], v[190:193], v[20:23]
	v_mfma_i32_16x16x64_i8 v[12:15], v[56:59], v[198:201], v[12:15]
	v_mfma_i32_16x16x64_i8 v[4:7], v[72:75], v[198:201], v[4:7]
	v_mfma_i32_16x16x64_i8 v[76:79], v[64:67], v[178:181], v[76:79]
	v_mfma_i32_16x16x64_i8 v[68:71], v[144:147], v[178:181], v[68:71]
	v_mfma_i32_16x16x64_i8 v[60:63], v[64:67], v[186:189], v[60:63]
	v_mfma_i32_16x16x64_i8 v[52:55], v[144:147], v[186:189], v[50:53]
	v_mfma_i32_16x16x64_i8 v[28:31], v[64:67], v[194:197], v[28:31]
	v_mfma_i32_16x16x64_i8 v[20:23], v[144:147], v[194:197], v[20:23]
	v_mfma_i32_16x16x64_i8 v[12:15], v[64:67], v[202:205], v[12:15]
	v_mfma_i32_16x16x64_i8 v[4:7], v[144:147], v[202:205], v[4:7]
	v_mfma_i32_16x16x64_i8 v[32:35], v[150:153], v[174:177], v[34:37]
	v_mfma_i32_16x16x64_i8 v[72:75], v[154:157], v[178:181], v[32:35]
	v_mfma_i32_16x16x64_i8 v[32:35], v[166:169], v[174:177], v[38:41]
	v_mfma_i32_16x16x64_i8 v[64:67], v[170:173], v[178:181], v[32:35]
	v_mfma_i32_16x16x64_i8 v[32:35], v[150:153], v[182:185], v[42:45]
	v_mfma_i32_16x16x64_i8 v[56:59], v[154:157], v[186:189], v[32:35]
	v_mfma_i32_16x16x64_i8 v[32:35], v[166:169], v[182:185], v[46:49]
	v_mfma_i32_16x16x64_i8 v[24:27], v[150:153], v[190:193], v[24:27]
	v_mfma_i32_16x16x64_i8 v[16:19], v[166:169], v[190:193], v[16:19]
	v_mfma_i32_16x16x64_i8 v[8:11], v[150:153], v[198:201], v[8:11]
	v_mfma_i32_16x16x64_i8 v[0:3], v[166:169], v[198:201], v[0:3]
	v_mfma_i32_16x16x64_i8 v[48:51], v[170:173], v[186:189], v[32:35]
	v_mfma_i32_16x16x64_i8 v[24:27], v[154:157], v[194:197], v[24:27]
	v_mfma_i32_16x16x64_i8 v[16:19], v[170:173], v[194:197], v[16:19]
	v_mfma_i32_16x16x64_i8 v[8:11], v[154:157], v[202:205], v[8:11]
	v_mfma_i32_16x16x64_i8 v[0:3], v[170:173], v[202:205], v[0:3]
	s_setprio 0
	s_waitcnt vmcnt(8)
	s_barrier
	s_add_u32 s0, s0, 0x100
	s_addc_u32 s2, s2, 0
	s_add_u32 s5, s5, 0x100
	s_addc_u32 s6, s6, 0
	s_add_u32 s19, s19, 0x100
	s_addc_u32 s33, s33, 0
	s_add_u32 s74, s74, 0x100
	s_addc_u32 s75, s75, 0
	s_cmp_ge_i32 s63, s25
	s_mov_b32 s59, s63
	s_cbranch_scc0 .LBB0_179
	s_and_b64 vcc, exec, s[50:51]
	s_cbranch_vccz .LBB0_182

; #define G_STAGE(bufoff, gbase, voff) do { _Pragma("unroll") for (int _i = 0; _i < 2; ++_i) \
;         __builtin_amdgcn_global_load_lds((const unsigned*)((const char*)(gbase) + (voff)[_i]), (LAS unsigned*)(lds + (bufoff) + ldsw + _i * 8192), 16, 0, 0); } while (0)
; #define G_LDA(dst, b, h) do { _Pragma("unroll") for (int m = 0; m < 4; ++m) G_LD8(dst[m], lds + G_SA(b, h) + aoff + m * 2048); } while (0)
; #define G_LDB(dst, b, h) do { _Pragma("unroll") for (int n = 0; n < 2; ++n) G_LD8(dst[n], lds + G_SB(b, h) + boff + n * 2048); } while (0)
; #define G_WAIT_V(n) asm volatile("s_waitcnt vmcnt(" #n ")" ::: "memory")
; #define G_WAIT_L(n) asm volatile("s_waitcnt lgkmcnt(" #n ")" ::: "memory")
; #define G_BAR __builtin_amdgcn_s_barrier()
; #define G_SCHED __builtin_amdgcn_sched_barrier(0)
;     __device__ __forceinline__ unsigned row_off(const Unit& u, int r, LAS unsigned char* lds) const { return (unsigned)((const LAS int*)(lds + LDS_STAGE + u.q * 4096))[r] * (unsigned)rowbytes; }
;     ...
;             const char* a11 = cur.a1 + (size_t)(t + 1) * kstep;
;             const char* a02 = last ? nxt.a0 : cur.a0 + (size_t)(t + 2) * kstep; const char* a12 = last ? nxt.a1 : cur.a1 + (size_t)(t + 2) * kstep;
;             const char* b02 = last ? nxt.b0 : cur.b0 + (size_t)(t + 2) * kstep; const char* b12 = last ? nxt.b1 : cur.b1 + (size_t)(t + 2) * kstep;
;             G_LDB(B0, 0, 0); G_LDB(B1, 0, 1); G_SCHED; G_LDA(At, 0, 0); G_STAGE(G_SA(1, 1), a11, vA1);
;             if constexpr (GATHER) { if (last) { int tz = tid; asm volatile("" : "+v"(tz));
; #pragma unroll
;                 for (int i = 0; i < 2; ++i) { int R, C; stage_rc(tz * 16 + i * 8192, R, C); gc0[i] = S.row_off(nxt, R, lds) + (unsigned)C * 2u; gc1[i] = S.row_off(nxt, 128 + R, lds) + (unsigned)C * 2u; } } }
;             G_WAIT_L(0); G_BAR; G_MMA(0, 0, At, B0); G_MMA(0, 1, At, B1); G_WAIT_V(8); G_BAR; G_SCHED;
;             G_LDA(At, 0, 1); G_STAGE(G_SB(0, 0), b02, voffB); G_STAGE(G_SB(0, 1), b12, voffB); G_STAGE(G_SA(0, 0), a02, vA0);
.LBB0_249:
	v_add_u32_e32 v144, s23, v151
	v_add_u32_e32 v166, s24, v151
	ds_read_b128 v[132:135], v144
	ds_read_b128 v[136:139], v144 offset:1024
	ds_read_b128 v[140:143], v144 offset:2048
	ds_read_b128 v[144:147], v144 offset:3072
	ds_read_b128 v[154:157], v166
	ds_read_b128 v[158:161], v166 offset:1024
	ds_read_b128 v[162:165], v166 offset:2048
	ds_read_b128 v[166:169], v166 offset:3072
	s_add_i32 s68, s58, 2
	s_add_u32 s69, s56, 0x80
	s_addc_u32 s59, s57, 0
	s_add_i32 s71, s23, s97
	s_add_i32 m0, s2, 0xc000
	s_add_i32 s70, s2, 0xe000
	s_add_i32 s72, s71, 0x2000
	s_cmp_eq_u32 s22, s58
	s_cselect_b32 s58, s46, s69
	s_cselect_b32 s61, s45, s67
	s_cselect_b32 s60, s44, s66
	s_cselect_b32 s63, s49, s55
	s_cselect_b32 s62, s48, s43
	s_cselect_b32 s59, s47, s59
	ds_read_b128 v[170:173], v152
	ds_read_b128 v[174:177], v152 offset:1024
	ds_read_b128 v[178:181], v152 offset:2048
	ds_read_b128 v[182:185], v152 offset:3072
	ds_read_b128 v[186:189], v152 offset:4096
	ds_read_b128 v[190:193], v152 offset:5120
	ds_read_b128 v[194:197], v152 offset:6144
	ds_read_b128 v[198:201], v152 offset:7168
	global_load_lds_dwordx4 v240, s[56:57]
	s_mov_b32 m0, s70
	s_nop 0
	global_load_lds_dwordx4 v242, s[56:57]
	s_waitcnt lgkmcnt(0)
	v_mov_b32_e32 v131, v129
	s_barrier
	s_setprio 1
	s_waitcnt lgkmcnt(0)
	v_mfma_i32_16x16x64_i8 v[124:127], v[132:135], v[170:173], v[124:127]
	v_mfma_i32_16x16x64_i8 v[120:123], v[140:143], v[170:173], v[120:123]
	v_mfma_i32_16x16x64_i8 v[108:111], v[132:135], v[178:181], v[108:111]
	v_mfma_i32_16x16x64_i8 v[104:107], v[140:143], v[178:181], v[104:107]
	v_mfma_i32_16x16x64_i8 v[92:95], v[132:135], v[186:189], v[92:95]
	v_mfma_i32_16x16x64_i8 v[88:91], v[140:143], v[186:189], v[88:91]
	v_mfma_i32_16x16x64_i8 v[76:79], v[132:135], v[194:197], v[76:79]
	v_mfma_i32_16x16x64_i8 v[72:75], v[140:143], v[194:197], v[72:75]
	v_mfma_i32_16x16x64_i8 v[124:127], v[136:139], v[174:177], v[124:127]
	v_mfma_i32_16x16x64_i8 v[120:123], v[144:147], v[174:177], v[120:123]
	v_mfma_i32_16x16x64_i8 v[108:111], v[136:139], v[182:185], v[108:111]
	v_mfma_i32_16x16x64_i8 v[104:107], v[144:147], v[182:185], v[104:107]
	v_mfma_i32_16x16x64_i8 v[92:95], v[136:139], v[190:193], v[92:95]
	v_mfma_i32_16x16x64_i8 v[88:91], v[144:147], v[190:193], v[88:91]
	v_mfma_i32_16x16x64_i8 v[76:79], v[136:139], v[198:201], v[76:79]
	v_mfma_i32_16x16x64_i8 v[72:75], v[144:147], v[198:201], v[72:75]
	v_mfma_i32_16x16x64_i8 v[116:119], v[154:157], v[170:173], v[116:119]
	v_mfma_i32_16x16x64_i8 v[112:115], v[162:165], v[170:173], v[112:115]
	v_mfma_i32_16x16x64_i8 v[100:103], v[154:157], v[178:181], v[100:103]
	v_mfma_i32_16x16x64_i8 v[96:99], v[162:165], v[178:181], v[96:99]
	v_mfma_i32_16x16x64_i8 v[84:87], v[154:157], v[186:189], v[84:87]
	v_mfma_i32_16x16x64_i8 v[80:83], v[162:165], v[186:189], v[80:83]
	v_mfma_i32_16x16x64_i8 v[68:71], v[154:157], v[194:197], v[68:71]
	v_mfma_i32_16x16x64_i8 v[64:67], v[162:165], v[194:197], v[64:67]
	v_mfma_i32_16x16x64_i8 v[116:119], v[158:161], v[174:177], v[116:119]
	v_mfma_i32_16x16x64_i8 v[112:115], v[166:169], v[174:177], v[112:115]
	v_mfma_i32_16x16x64_i8 v[100:103], v[158:161], v[182:185], v[100:103]
	v_mfma_i32_16x16x64_i8 v[96:99], v[166:169], v[182:185], v[96:99]
	v_mfma_i32_16x16x64_i8 v[84:87], v[158:161], v[190:193], v[84:87]
	v_mfma_i32_16x16x64_i8 v[80:83], v[166:169], v[190:193], v[80:83]
	v_mfma_i32_16x16x64_i8 v[68:71], v[158:161], v[198:201], v[68:71]
	v_mfma_i32_16x16x64_i8 v[64:67], v[166:169], v[198:201], v[64:67]
	s_setprio 0
	s_waitcnt vmcnt(8)
	s_barrier
	s_mov_b32 m0, s71
	ds_read_b128 v[170:173], v152 offset:16384
	ds_read_b128 v[174:177], v152 offset:17408
	ds_read_b128 v[178:181], v152 offset:18432
	ds_read_b128 v[182:185], v152 offset:19456
	ds_read_b128 v[186:189], v152 offset:20480
	ds_read_b128 v[190:193], v152 offset:21504
	ds_read_b128 v[194:197], v152 offset:22528
	ds_read_b128 v[198:201], v152 offset:23552
	v_mov_b32_e32 v203, v129
	global_load_lds_dwordx4 v244, s[62:63]
	v_mov_b32_e32 v205, v129
	s_mov_b32 m0, s72
	v_lshl_add_u64 v[206:207], s[62:63], 0, v[244:245]
	v_lshl_add_u64 v[208:209], s[62:63], 0, v[246:247]
	global_load_lds_dwordx4 v246, s[62:63]
	s_cselect_b32 s63, s51, s65
	s_cselect_b32 s62, s50, s64
	s_add_i32 s69, s24, s97
	s_mov_b32 m0, s69
	v_lshl_add_u64 v[210:211], s[62:63], 0, v[244:245]
	global_load_lds_dwordx4 v244, s[62:63]
	s_add_i32 m0, s69, 0x2000
	v_lshl_add_u64 v[202:203], s[62:63], 0, v[246:247]
	global_load_lds_dwordx4 v246, s[62:63]
	s_mov_b32 m0, s2
	v_lshl_add_u64 v[204:205], s[60:61], 0, v[240:241]
	global_load_lds_dwordx4 v240, s[60:61]
	s_mov_b32 m0, s10
	v_lshl_add_u64 v[212:213], s[60:61], 0, v[242:243]
	global_load_lds_dwordx4 v242, s[60:61]
	s_waitcnt lgkmcnt(0)
	s_barrier
; #define G_STAGE(bufoff, gbase, voff) do { _Pragma("unroll") for (int _i = 0; _i < 2; ++_i) \
;         __builtin_amdgcn_global_load_lds((const unsigned*)((const char*)(gbase) + (voff)[_i]), (LAS unsigned*)(lds + (bufoff) + ldsw + _i * 8192), 16, 0, 0); } while (0)
; #define G_LDA(dst, b, h) do { _Pragma("unroll") for (int m = 0; m < 4; ++m) G_LD8(dst[m], lds + G_SA(b, h) + aoff + m * 2048); } while (0)
; #define G_LDB(dst, b, h) do { _Pragma("unroll") for (int n = 0; n < 2; ++n) G_LD8(dst[n], lds + G_SB(b, h) + boff + n * 2048); } while (0)
; #define G_WAIT_V(n) asm volatile("s_waitcnt vmcnt(" #n ")" ::: "memory")
; #define G_WAIT_L(n) asm volatile("s_waitcnt lgkmcnt(" #n ")" ::: "memory")
; #define G_BAR __builtin_amdgcn_s_barrier()
; #define G_SCHED __builtin_amdgcn_sched_barrier(0)
;     ...
;             G_WAIT_L(0); G_BAR; G_MMA(1, 0, At, B0); G_MMA(1, 1, At, B1); G_WAIT_V(8); G_BAR; G_SCHED;
;             G_LDB(B0, 1, 0); G_LDB(B1, 1, 1); G_SCHED; G_LDA(At, 1, 0); G_STAGE(G_SA(0, 1), a12, vA1);
;             G_WAIT_L(0); G_BAR; G_MMA(0, 0, At, B0); G_MMA(0, 1, At, B1); G_WAIT_V(8); G_BAR; G_SCHED;
	s_setprio 1
	s_waitcnt lgkmcnt(0)
	v_mfma_i32_16x16x64_i8 v[60:63], v[132:135], v[170:173], v[60:63]
	v_mfma_i32_16x16x64_i8 v[56:59], v[140:143], v[170:173], v[56:59]
	v_mfma_i32_16x16x64_i8 v[44:47], v[132:135], v[178:181], v[44:47]
	v_mfma_i32_16x16x64_i8 v[40:43], v[140:143], v[178:181], v[40:43]
	v_mfma_i32_16x16x64_i8 v[28:31], v[132:135], v[186:189], v[28:31]
	v_mfma_i32_16x16x64_i8 v[24:27], v[140:143], v[186:189], v[24:27]
	v_mfma_i32_16x16x64_i8 v[12:15], v[132:135], v[194:197], v[12:15]
	v_mfma_i32_16x16x64_i8 v[8:11], v[140:143], v[194:197], v[8:11]
	v_mfma_i32_16x16x64_i8 v[60:63], v[136:139], v[174:177], v[60:63]
	v_mfma_i32_16x16x64_i8 v[56:59], v[144:147], v[174:177], v[56:59]
	v_mfma_i32_16x16x64_i8 v[44:47], v[136:139], v[182:185], v[44:47]
	v_mfma_i32_16x16x64_i8 v[40:43], v[144:147], v[182:185], v[40:43]
	v_mfma_i32_16x16x64_i8 v[28:31], v[136:139], v[190:193], v[28:31]
	v_mfma_i32_16x16x64_i8 v[24:27], v[144:147], v[190:193], v[24:27]
	v_mfma_i32_16x16x64_i8 v[12:15], v[136:139], v[198:201], v[12:15]
	v_mfma_i32_16x16x64_i8 v[8:11], v[144:147], v[198:201], v[8:11]
	v_mfma_i32_16x16x64_i8 v[52:55], v[154:157], v[170:173], v[52:55]
	v_mfma_i32_16x16x64_i8 v[48:51], v[162:165], v[170:173], v[48:51]
	v_mfma_i32_16x16x64_i8 v[36:39], v[154:157], v[178:181], v[36:39]
	v_mfma_i32_16x16x64_i8 v[32:35], v[162:165], v[178:181], v[32:35]
	v_mfma_i32_16x16x64_i8 v[20:23], v[154:157], v[186:189], v[20:23]
	v_mfma_i32_16x16x64_i8 v[16:19], v[162:165], v[186:189], v[16:19]
	v_mfma_i32_16x16x64_i8 v[4:7], v[154:157], v[194:197], v[4:7]
	v_mfma_i32_16x16x64_i8 v[0:3], v[162:165], v[194:197], v[0:3]
	v_mfma_i32_16x16x64_i8 v[52:55], v[158:161], v[174:177], v[52:55]
	v_mfma_i32_16x16x64_i8 v[48:51], v[166:169], v[174:177], v[48:51]
	v_mfma_i32_16x16x64_i8 v[36:39], v[158:161], v[182:185], v[36:39]
	v_mfma_i32_16x16x64_i8 v[32:35], v[166:169], v[182:185], v[32:35]
	v_mfma_i32_16x16x64_i8 v[20:23], v[158:161], v[190:193], v[20:23]
	v_mfma_i32_16x16x64_i8 v[16:19], v[166:169], v[190:193], v[16:19]
	v_mfma_i32_16x16x64_i8 v[4:7], v[158:161], v[198:201], v[4:7]
	v_mfma_i32_16x16x64_i8 v[0:3], v[166:169], v[198:201], v[0:3]
	s_setprio 0
	s_waitcnt vmcnt(8)
	s_barrier
	s_add_i32 s60, 0, 0x18000
	v_add_u32_e32 v131, s60, v151
	s_add_i32 s61, 0, 0x1c000
	ds_read_b128 v[132:135], v131
	ds_read_b128 v[136:139], v131 offset:1024
	ds_read_b128 v[140:143], v131 offset:2048
	ds_read_b128 v[144:147], v131 offset:3072
	v_add_u32_e32 v131, s61, v151
	ds_read_b128 v[154:157], v131
	ds_read_b128 v[158:161], v131 offset:1024
	ds_read_b128 v[162:165], v131 offset:2048
	ds_read_b128 v[166:169], v131 offset:3072
	s_mov_b32 m0, s11
	ds_read_b128 v[170:173], v152 offset:32768
	ds_read_b128 v[174:177], v152 offset:33792
	ds_read_b128 v[178:181], v152 offset:34816
	ds_read_b128 v[182:185], v152 offset:35840
	ds_read_b128 v[186:189], v152 offset:36864
	ds_read_b128 v[190:193], v152 offset:37888
	ds_read_b128 v[194:197], v152 offset:38912
	ds_read_b128 v[198:201], v152 offset:39936
	global_load_lds_dwordx4 v240, s[58:59]
	s_mov_b32 m0, s18
	s_nop 0
	global_load_lds_dwordx4 v242, s[58:59]
	s_waitcnt lgkmcnt(0)
	s_barrier
	s_setprio 1
	s_waitcnt lgkmcnt(0)
	v_mfma_i32_16x16x64_i8 v[124:127], v[132:135], v[170:173], v[124:127]
	v_mfma_i32_16x16x64_i8 v[120:123], v[140:143], v[170:173], v[120:123]
	v_mfma_i32_16x16x64_i8 v[108:111], v[132:135], v[178:181], v[108:111]
	v_mfma_i32_16x16x64_i8 v[104:107], v[140:143], v[178:181], v[104:107]
	v_mfma_i32_16x16x64_i8 v[92:95], v[132:135], v[186:189], v[92:95]
	v_mfma_i32_16x16x64_i8 v[88:91], v[140:143], v[186:189], v[88:91]
	v_mfma_i32_16x16x64_i8 v[76:79], v[132:135], v[194:197], v[76:79]
	v_mfma_i32_16x16x64_i8 v[72:75], v[140:143], v[194:197], v[72:75]
	v_mfma_i32_16x16x64_i8 v[124:127], v[136:139], v[174:177], v[124:127]
	v_mfma_i32_16x16x64_i8 v[120:123], v[144:147], v[174:177], v[120:123]
	v_mfma_i32_16x16x64_i8 v[108:111], v[136:139], v[182:185], v[108:111]
	v_mfma_i32_16x16x64_i8 v[104:107], v[144:147], v[182:185], v[104:107]
	v_mfma_i32_16x16x64_i8 v[92:95], v[136:139], v[190:193], v[92:95]
	v_mfma_i32_16x16x64_i8 v[88:91], v[144:147], v[190:193], v[88:91]
	v_mfma_i32_16x16x64_i8 v[76:79], v[136:139], v[198:201], v[76:79]
	v_mfma_i32_16x16x64_i8 v[72:75], v[144:147], v[198:201], v[72:75]
	v_mfma_i32_16x16x64_i8 v[116:119], v[154:157], v[170:173], v[116:119]
	v_mfma_i32_16x16x64_i8 v[112:115], v[162:165], v[170:173], v[112:115]
	v_mfma_i32_16x16x64_i8 v[100:103], v[154:157], v[178:181], v[100:103]
	v_mfma_i32_16x16x64_i8 v[96:99], v[162:165], v[178:181], v[96:99]
	v_mfma_i32_16x16x64_i8 v[84:87], v[154:157], v[186:189], v[84:87]
	v_mfma_i32_16x16x64_i8 v[80:83], v[162:165], v[186:189], v[80:83]
	v_mfma_i32_16x16x64_i8 v[68:71], v[154:157], v[194:197], v[68:71]
	v_mfma_i32_16x16x64_i8 v[64:67], v[162:165], v[194:197], v[64:67]
	v_mfma_i32_16x16x64_i8 v[116:119], v[158:161], v[174:177], v[116:119]
	v_mfma_i32_16x16x64_i8 v[112:115], v[166:169], v[174:177], v[112:115]
	v_mfma_i32_16x16x64_i8 v[100:103], v[158:161], v[182:185], v[100:103]
	v_mfma_i32_16x16x64_i8 v[96:99], v[166:169], v[182:185], v[96:99]
	v_mfma_i32_16x16x64_i8 v[84:87], v[158:161], v[190:193], v[84:87]
	v_mfma_i32_16x16x64_i8 v[80:83], v[166:169], v[190:193], v[80:83]
	v_mfma_i32_16x16x64_i8 v[68:71], v[158:161], v[198:201], v[68:71]
	v_mfma_i32_16x16x64_i8 v[64:67], v[166:169], v[198:201], v[64:67]
	s_setprio 0
	s_waitcnt vmcnt(8)
	s_barrier
; #define G_STAGE(bufoff, gbase, voff) do { _Pragma("unroll") for (int _i = 0; _i < 2; ++_i) \
;         __builtin_amdgcn_global_load_lds((const unsigned*)((const char*)(gbase) + (voff)[_i]), (LAS unsigned*)(lds + (bufoff) + ldsw + _i * 8192), 16, 0, 0); } while (0)
; #define G_LDA(dst, b, h) do { _Pragma("unroll") for (int m = 0; m < 4; ++m) G_LD8(dst[m], lds + G_SA(b, h) + aoff + m * 2048); } while (0)
; #define G_WAIT_V(n) asm volatile("s_waitcnt vmcnt(" #n ")" ::: "memory")
; #define G_WAIT_L(n) asm volatile("s_waitcnt lgkmcnt(" #n ")" ::: "memory")
; #define G_BAR __builtin_amdgcn_s_barrier()
; #define G_SCHED __builtin_amdgcn_sched_barrier(0)
;     ...
;             G_LDA(At, 1, 1); G_STAGE(G_SB(1, 0), b02 + kstep, voffB); G_STAGE(G_SB(1, 1), b12 + kstep, voffB); G_STAGE(G_SA(1, 0), a02 + kstep, vA0);
;             G_WAIT_L(0); G_BAR; G_MMA(1, 0, At, B0); G_MMA(1, 1, At, B1); G_WAIT_V(8); G_BAR; G_SCHED;
;         }
	s_add_i32 s58, s60, s97
	v_lshl_add_u64 v[130:131], v[206:207], 0, s[8:9]
	s_mov_b32 m0, s58
	ds_read_b128 v[170:173], v152 offset:49152
	ds_read_b128 v[174:177], v152 offset:50176
	ds_read_b128 v[178:181], v152 offset:51200
	ds_read_b128 v[182:185], v152 offset:52224
	ds_read_b128 v[186:189], v152 offset:53248
	ds_read_b128 v[190:193], v152 offset:54272
	ds_read_b128 v[194:197], v152 offset:55296
	ds_read_b128 v[198:201], v152 offset:56320
	global_load_lds_dwordx4 v[130:131], off
	v_lshl_add_u64 v[130:131], v[208:209], 0, s[8:9]
	s_add_i32 m0, s58, 0x2000
	s_add_i32 s58, s61, s97
	global_load_lds_dwordx4 v[130:131], off
	v_lshl_add_u64 v[130:131], v[210:211], 0, s[8:9]
	s_mov_b32 m0, s58
	s_nop 0
	global_load_lds_dwordx4 v[130:131], off
	v_lshl_add_u64 v[130:131], v[202:203], 0, s[8:9]
	s_add_i32 m0, s58, 0x2000
	s_nop 0
	global_load_lds_dwordx4 v[130:131], off
	v_lshl_add_u64 v[130:131], v[204:205], 0, s[8:9]
	s_mov_b32 m0, s20
	s_nop 0
	global_load_lds_dwordx4 v[130:131], off
	v_lshl_add_u64 v[130:131], v[212:213], 0, s[8:9]
	s_mov_b32 m0, s21
	s_nop 0
	global_load_lds_dwordx4 v[130:131], off
	s_waitcnt lgkmcnt(0)
	s_barrier
	s_setprio 1
	s_waitcnt lgkmcnt(0)
	v_mfma_i32_16x16x64_i8 v[60:63], v[132:135], v[170:173], v[60:63]
	v_mfma_i32_16x16x64_i8 v[56:59], v[140:143], v[170:173], v[56:59]
	v_mfma_i32_16x16x64_i8 v[44:47], v[132:135], v[178:181], v[44:47]
	v_mfma_i32_16x16x64_i8 v[40:43], v[140:143], v[178:181], v[40:43]
	v_mfma_i32_16x16x64_i8 v[28:31], v[132:135], v[186:189], v[28:31]
	v_mfma_i32_16x16x64_i8 v[24:27], v[140:143], v[186:189], v[24:27]
	v_mfma_i32_16x16x64_i8 v[12:15], v[132:135], v[194:197], v[12:15]
	v_mfma_i32_16x16x64_i8 v[8:11], v[140:143], v[194:197], v[8:11]
	v_mfma_i32_16x16x64_i8 v[60:63], v[136:139], v[174:177], v[60:63]
	v_mfma_i32_16x16x64_i8 v[56:59], v[144:147], v[174:177], v[56:59]
	v_mfma_i32_16x16x64_i8 v[44:47], v[136:139], v[182:185], v[44:47]
	v_mfma_i32_16x16x64_i8 v[40:43], v[144:147], v[182:185], v[40:43]
	v_mfma_i32_16x16x64_i8 v[28:31], v[136:139], v[190:193], v[28:31]
	v_mfma_i32_16x16x64_i8 v[24:27], v[144:147], v[190:193], v[24:27]
	v_mfma_i32_16x16x64_i8 v[12:15], v[136:139], v[198:201], v[12:15]
	v_mfma_i32_16x16x64_i8 v[8:11], v[144:147], v[198:201], v[8:11]
	v_mfma_i32_16x16x64_i8 v[52:55], v[154:157], v[170:173], v[52:55]
	v_mfma_i32_16x16x64_i8 v[48:51], v[162:165], v[170:173], v[48:51]
	v_mfma_i32_16x16x64_i8 v[36:39], v[154:157], v[178:181], v[36:39]
	v_mfma_i32_16x16x64_i8 v[32:35], v[162:165], v[178:181], v[32:35]
	v_mfma_i32_16x16x64_i8 v[20:23], v[154:157], v[186:189], v[20:23]
	v_mfma_i32_16x16x64_i8 v[16:19], v[162:165], v[186:189], v[16:19]
	v_mfma_i32_16x16x64_i8 v[4:7], v[154:157], v[194:197], v[4:7]
	v_mfma_i32_16x16x64_i8 v[0:3], v[162:165], v[194:197], v[0:3]
	v_mfma_i32_16x16x64_i8 v[52:55], v[158:161], v[174:177], v[52:55]
	v_mfma_i32_16x16x64_i8 v[48:51], v[166:169], v[174:177], v[48:51]
	v_mfma_i32_16x16x64_i8 v[36:39], v[158:161], v[182:185], v[36:39]
	v_mfma_i32_16x16x64_i8 v[32:35], v[166:169], v[182:185], v[32:35]
	v_mfma_i32_16x16x64_i8 v[20:23], v[158:161], v[190:193], v[20:23]
	v_mfma_i32_16x16x64_i8 v[16:19], v[166:169], v[190:193], v[16:19]
	v_mfma_i32_16x16x64_i8 v[4:7], v[158:161], v[198:201], v[4:7]
	v_mfma_i32_16x16x64_i8 v[0:3], v[166:169], v[198:201], v[0:3]
	s_setprio 0
	s_waitcnt vmcnt(8)
	s_barrier
	s_add_u32 s43, s43, 0x100
	s_addc_u32 s55, s55, 0
	s_add_u32 s64, s64, 0x100
	s_addc_u32 s65, s65, 0
	s_add_u32 s66, s66, 0x100
	s_addc_u32 s67, s67, 0
	s_add_u32 s56, s56, 0x100
	s_addc_u32 s57, s57, 0
	s_cmp_ge_i32 s68, s0
	s_mov_b32 s58, s68
	s_cbranch_scc0 .LBB0_249
	s_and_b64 vcc, exec, s[40:41]
	s_cbranch_vccz .LBB0_252

; #define G_STAGE(bufoff, gbase, voff) do { _Pragma("unroll") for (int _i = 0; _i < 2; ++_i) \
;         __builtin_amdgcn_global_load_lds((const unsigned*)((const char*)(gbase) + (voff)[_i]), (LAS unsigned*)(lds + (bufoff) + ldsw + _i * 8192), 16, 0, 0); } while (0)
; #define G_LDA(dst, b, h) do { _Pragma("unroll") for (int m = 0; m < 4; ++m) G_LD8(dst[m], lds + G_SA(b, h) + aoff + m * 2048); } while (0)
; #define G_LDB(dst, b, h) do { _Pragma("unroll") for (int n = 0; n < 2; ++n) G_LD8(dst[n], lds + G_SB(b, h) + boff + n * 2048); } while (0)
; #define G_WAIT_V(n) asm volatile("s_waitcnt vmcnt(" #n ")" ::: "memory")
; #define G_WAIT_L(n) asm volatile("s_waitcnt lgkmcnt(" #n ")" ::: "memory")
; #define G_BAR __builtin_amdgcn_s_barrier()
; #define G_SCHED __builtin_amdgcn_sched_barrier(0)
;     __device__ __forceinline__ unsigned row_off(const Unit& u, int r, LAS unsigned char* lds) const { return (unsigned)((const LAS int*)(lds + LDS_STAGE + u.q * 4096))[r] * (unsigned)rowbytes; }
;     ...
;             const char* a11 = cur.a1 + (size_t)(t + 1) * kstep;
;             const char* a02 = last ? nxt.a0 : cur.a0 + (size_t)(t + 2) * kstep; const char* a12 = last ? nxt.a1 : cur.a1 + (size_t)(t + 2) * kstep;
;             const char* b02 = last ? nxt.b0 : cur.b0 + (size_t)(t + 2) * kstep; const char* b12 = last ? nxt.b1 : cur.b1 + (size_t)(t + 2) * kstep;
;             G_LDB(B0, 0, 0); G_LDB(B1, 0, 1); G_SCHED; G_LDA(At, 0, 0); G_STAGE(G_SA(1, 1), a11, vA1);
;             if constexpr (GATHER) { if (last) { int tz = tid; asm volatile("" : "+v"(tz));
; #pragma unroll
;                 for (int i = 0; i < 2; ++i) { int R, C; stage_rc(tz * 16 + i * 8192, R, C); gc0[i] = S.row_off(nxt, R, lds) + (unsigned)C * 2u; gc1[i] = S.row_off(nxt, 128 + R, lds) + (unsigned)C * 2u; } } }
;             G_WAIT_L(0); G_BAR; G_MMA(0, 0, At, B0); G_MMA(0, 1, At, B1); G_WAIT_V(8); G_BAR; G_SCHED;
;             G_LDA(At, 0, 1); G_STAGE(G_SB(0, 0), b02, voffB); G_STAGE(G_SB(0, 1), b12, voffB); G_STAGE(G_SA(0, 0), a02, vA0);
.LBB0_284:
	v_add_u32_e32 v144, s24, v157
	v_add_u32_e32 v168, s25, v157
	ds_read_b128 v[100:103], v144
	ds_read_b128 v[112:115], v144 offset:1024
	ds_read_b128 v[120:123], v144 offset:2048
	ds_read_b128 v[144:147], v144 offset:3072
	ds_read_b128 v[150:153], v168
	ds_read_b128 v[160:163], v168 offset:1024
	ds_read_b128 v[164:167], v168 offset:2048
	ds_read_b128 v[168:171], v168 offset:3072
	s_add_i32 s76, s64, 2
	s_add_u32 s77, s62, 0x80
	s_addc_u32 s65, s63, 0
	s_add_i32 s79, s24, s97
	s_add_i32 m0, s0, 0xc000
	s_add_i32 s78, s0, 0xe000
	s_add_i32 s80, s79, 0x2000
	s_cmp_eq_u32 s23, s64
	s_cselect_b32 s64, s50, s77
	s_cselect_b32 s67, s49, s75
	s_cselect_b32 s66, s48, s71
	s_cselect_b32 s69, s53, s59
	s_cselect_b32 s68, s52, s45
	s_cselect_b32 s65, s51, s65
	ds_read_b128 v[172:175], v158
	ds_read_b128 v[176:179], v158 offset:1024
	ds_read_b128 v[180:183], v158 offset:2048
	ds_read_b128 v[184:187], v158 offset:3072
	ds_read_b128 v[188:191], v158 offset:4096
	ds_read_b128 v[192:195], v158 offset:5120
	ds_read_b128 v[196:199], v158 offset:6144
	ds_read_b128 v[200:203], v158 offset:7168
	global_load_lds_dwordx4 v240, s[62:63]
	s_mov_b32 m0, s78
	s_nop 0
	global_load_lds_dwordx4 v242, s[62:63]
	s_waitcnt lgkmcnt(0)
	v_mov_b32_e32 v93, v149
	s_barrier
	s_setprio 1
	s_waitcnt lgkmcnt(0)
	v_mfma_i32_16x16x64_i8 v[140:143], v[100:103], v[172:175], v[140:143]
	v_mfma_i32_16x16x64_i8 v[132:135], v[120:123], v[172:175], v[132:135]
	v_mfma_i32_16x16x64_i8 v[94:97], v[100:103], v[180:183], v[96:99]
	v_mfma_i32_16x16x64_i8 v[88:91], v[120:123], v[180:183], v[88:91]
	v_mfma_i32_16x16x64_i8 v[60:63], v[100:103], v[188:191], v[60:63]
	v_mfma_i32_16x16x64_i8 v[56:59], v[120:123], v[188:191], v[56:59]
	v_mfma_i32_16x16x64_i8 v[28:31], v[100:103], v[196:199], v[28:31]
	v_mfma_i32_16x16x64_i8 v[24:27], v[120:123], v[196:199], v[24:27]
	v_mfma_i32_16x16x64_i8 v[140:143], v[112:115], v[176:179], v[140:143]
	v_mfma_i32_16x16x64_i8 v[132:135], v[144:147], v[176:179], v[132:135]
	v_mfma_i32_16x16x64_i8 v[94:97], v[112:115], v[184:187], v[94:97]
	v_mfma_i32_16x16x64_i8 v[88:91], v[144:147], v[184:187], v[88:91]
	v_mfma_i32_16x16x64_i8 v[60:63], v[112:115], v[192:195], v[60:63]
	v_mfma_i32_16x16x64_i8 v[56:59], v[144:147], v[192:195], v[56:59]
	v_mfma_i32_16x16x64_i8 v[28:31], v[112:115], v[200:203], v[28:31]
	v_mfma_i32_16x16x64_i8 v[24:27], v[144:147], v[200:203], v[24:27]
	v_mfma_i32_16x16x64_i8 v[124:127], v[150:153], v[172:175], v[124:127]
	v_mfma_i32_16x16x64_i8 v[108:111], v[164:167], v[172:175], v[108:111]
	v_mfma_i32_16x16x64_i8 v[76:79], v[150:153], v[180:183], v[76:79]
	v_mfma_i32_16x16x64_i8 v[72:75], v[164:167], v[180:183], v[72:75]
	v_mfma_i32_16x16x64_i8 v[44:47], v[150:153], v[188:191], v[44:47]
	v_mfma_i32_16x16x64_i8 v[40:43], v[164:167], v[188:191], v[40:43]
	v_mfma_i32_16x16x64_i8 v[12:15], v[150:153], v[196:199], v[12:15]
	v_mfma_i32_16x16x64_i8 v[8:11], v[164:167], v[196:199], v[8:11]
	v_mfma_i32_16x16x64_i8 v[124:127], v[160:163], v[176:179], v[124:127]
	v_mfma_i32_16x16x64_i8 v[108:111], v[168:171], v[176:179], v[108:111]
	v_mfma_i32_16x16x64_i8 v[76:79], v[160:163], v[184:187], v[76:79]
	v_mfma_i32_16x16x64_i8 v[72:75], v[168:171], v[184:187], v[72:75]
	v_mfma_i32_16x16x64_i8 v[44:47], v[160:163], v[192:195], v[44:47]
	v_mfma_i32_16x16x64_i8 v[40:43], v[168:171], v[192:195], v[40:43]
	v_mfma_i32_16x16x64_i8 v[12:15], v[160:163], v[200:203], v[12:15]
	v_mfma_i32_16x16x64_i8 v[8:11], v[168:171], v[200:203], v[8:11]
	s_setprio 0
	s_waitcnt vmcnt(8)
	s_barrier
	s_mov_b32 m0, s79
	ds_read_b128 v[172:175], v158 offset:16384
	ds_read_b128 v[176:179], v158 offset:17408
	ds_read_b128 v[180:183], v158 offset:18432
	ds_read_b128 v[184:187], v158 offset:19456
	ds_read_b128 v[188:191], v158 offset:20480
	ds_read_b128 v[192:195], v158 offset:21504
	ds_read_b128 v[196:199], v158 offset:22528
	ds_read_b128 v[200:203], v158 offset:23552
	v_mov_b32_e32 v205, v149
	global_load_lds_dwordx4 v244, s[68:69]
	v_mov_b32_e32 v207, v149
	s_mov_b32 m0, s80
	v_lshl_add_u64 v[208:209], s[68:69], 0, v[244:245]
	v_lshl_add_u64 v[210:211], s[68:69], 0, v[246:247]
	global_load_lds_dwordx4 v246, s[68:69]
	s_cselect_b32 s69, s55, s70
	s_cselect_b32 s68, s54, s61
	s_add_i32 s77, s25, s97
	s_mov_b32 m0, s77
	v_lshl_add_u64 v[212:213], s[68:69], 0, v[244:245]
	global_load_lds_dwordx4 v244, s[68:69]
	s_add_i32 m0, s77, 0x2000
	v_lshl_add_u64 v[204:205], s[68:69], 0, v[246:247]
	global_load_lds_dwordx4 v246, s[68:69]
	s_mov_b32 m0, s0
	v_lshl_add_u64 v[206:207], s[66:67], 0, v[240:241]
	global_load_lds_dwordx4 v240, s[66:67]
	s_mov_b32 m0, s11
	v_lshl_add_u64 v[214:215], s[66:67], 0, v[242:243]
	global_load_lds_dwordx4 v242, s[66:67]
	s_waitcnt lgkmcnt(0)
	s_barrier
; #define G_STAGE(bufoff, gbase, voff) do { _Pragma("unroll") for (int _i = 0; _i < 2; ++_i) \
;         __builtin_amdgcn_global_load_lds((const unsigned*)((const char*)(gbase) + (voff)[_i]), (LAS unsigned*)(lds + (bufoff) + ldsw + _i * 8192), 16, 0, 0); } while (0)
; #define G_LDA(dst, b, h) do { _Pragma("unroll") for (int m = 0; m < 4; ++m) G_LD8(dst[m], lds + G_SA(b, h) + aoff + m * 2048); } while (0)
; #define G_LDB(dst, b, h) do { _Pragma("unroll") for (int n = 0; n < 2; ++n) G_LD8(dst[n], lds + G_SB(b, h) + boff + n * 2048); } while (0)
; #define G_WAIT_V(n) asm volatile("s_waitcnt vmcnt(" #n ")" ::: "memory")
; #define G_WAIT_L(n) asm volatile("s_waitcnt lgkmcnt(" #n ")" ::: "memory")
; #define G_BAR __builtin_amdgcn_s_barrier()
; #define G_SCHED __builtin_amdgcn_sched_barrier(0)
;     ...
;             G_WAIT_L(0); G_BAR; G_MMA(1, 0, At, B0); G_MMA(1, 1, At, B1); G_WAIT_V(8); G_BAR; G_SCHED;
;             G_LDB(B0, 1, 0); G_LDB(B1, 1, 1); G_SCHED; G_LDA(At, 1, 0); G_STAGE(G_SA(0, 1), a12, vA1);
;             G_WAIT_L(0); G_BAR; G_MMA(0, 0, At, B0); G_MMA(0, 1, At, B1); G_WAIT_V(8); G_BAR; G_SCHED;
	s_setprio 1
	s_waitcnt lgkmcnt(0)
	v_mfma_i32_16x16x64_i8 v[136:139], v[100:103], v[172:175], v[136:139]
	v_mfma_i32_16x16x64_i8 v[128:131], v[120:123], v[172:175], v[128:131]
	v_mfma_i32_16x16x64_i8 v[84:87], v[100:103], v[180:183], v[84:87]
	v_mfma_i32_16x16x64_i8 v[80:83], v[120:123], v[180:183], v[80:83]
	v_mfma_i32_16x16x64_i8 v[52:55], v[100:103], v[188:191], v[52:55]
	v_mfma_i32_16x16x64_i8 v[48:51], v[120:123], v[188:191], v[48:51]
	v_mfma_i32_16x16x64_i8 v[20:23], v[100:103], v[196:199], v[20:23]
	v_mfma_i32_16x16x64_i8 v[16:19], v[120:123], v[196:199], v[16:19]
	v_mfma_i32_16x16x64_i8 v[136:139], v[112:115], v[176:179], v[136:139]
	v_mfma_i32_16x16x64_i8 v[128:131], v[144:147], v[176:179], v[128:131]
	v_mfma_i32_16x16x64_i8 v[84:87], v[112:115], v[184:187], v[84:87]
	v_mfma_i32_16x16x64_i8 v[80:83], v[144:147], v[184:187], v[80:83]
	v_mfma_i32_16x16x64_i8 v[52:55], v[112:115], v[192:195], v[52:55]
	v_mfma_i32_16x16x64_i8 v[48:51], v[144:147], v[192:195], v[48:51]
	v_mfma_i32_16x16x64_i8 v[20:23], v[112:115], v[200:203], v[20:23]
	v_mfma_i32_16x16x64_i8 v[16:19], v[144:147], v[200:203], v[16:19]
	v_mfma_i32_16x16x64_i8 v[104:107], v[164:167], v[172:175], v[104:107]
	v_mfma_i32_16x16x64_i8 v[68:71], v[150:153], v[180:183], v[68:71]
	v_mfma_i32_16x16x64_i8 v[64:67], v[164:167], v[180:183], v[64:67]
	v_mfma_i32_16x16x64_i8 v[36:39], v[150:153], v[188:191], v[36:39]
	v_mfma_i32_16x16x64_i8 v[32:35], v[164:167], v[188:191], v[32:35]
	v_mfma_i32_16x16x64_i8 v[4:7], v[150:153], v[196:199], v[4:7]
	v_mfma_i32_16x16x64_i8 v[0:3], v[164:167], v[196:199], v[0:3]
	v_mfma_i32_16x16x64_i8 v[98:101], v[150:153], v[172:175], v[116:119]
	v_mfma_i32_16x16x64_i8 v[104:107], v[168:171], v[176:179], v[104:107]
	v_mfma_i32_16x16x64_i8 v[68:71], v[160:163], v[184:187], v[68:71]
	v_mfma_i32_16x16x64_i8 v[64:67], v[168:171], v[184:187], v[64:67]
	v_mfma_i32_16x16x64_i8 v[36:39], v[160:163], v[192:195], v[36:39]
	v_mfma_i32_16x16x64_i8 v[32:35], v[168:171], v[192:195], v[32:35]
	v_mfma_i32_16x16x64_i8 v[4:7], v[160:163], v[200:203], v[4:7]
	v_mfma_i32_16x16x64_i8 v[0:3], v[168:171], v[200:203], v[0:3]
	v_mfma_i32_16x16x64_i8 v[100:103], v[160:163], v[176:179], v[98:101]
	s_setprio 0
	s_waitcnt vmcnt(8)
	s_barrier
	s_add_i32 s66, 0, 0x18000
	v_add_u32_e32 v93, s66, v157
	s_add_i32 s67, 0, 0x1c000
	ds_read_b128 v[112:115], v93
	ds_read_b128 v[116:119], v93 offset:1024
	ds_read_b128 v[120:123], v93 offset:2048
	ds_read_b128 v[144:147], v93 offset:3072
	v_add_u32_e32 v93, s67, v157
	ds_read_b128 v[150:153], v93
	ds_read_b128 v[160:163], v93 offset:1024
	ds_read_b128 v[164:167], v93 offset:2048
	ds_read_b128 v[168:171], v93 offset:3072
	s_mov_b32 m0, s18
	ds_read_b128 v[172:175], v158 offset:32768
	ds_read_b128 v[176:179], v158 offset:33792
	ds_read_b128 v[180:183], v158 offset:34816
	ds_read_b128 v[184:187], v158 offset:35840
	ds_read_b128 v[188:191], v158 offset:36864
	ds_read_b128 v[192:195], v158 offset:37888
	ds_read_b128 v[196:199], v158 offset:38912
	ds_read_b128 v[200:203], v158 offset:39936
	global_load_lds_dwordx4 v240, s[64:65]
	s_mov_b32 m0, s19
	s_nop 0
	global_load_lds_dwordx4 v242, s[64:65]
	s_waitcnt lgkmcnt(0)
	s_barrier
	s_setprio 1
	s_waitcnt lgkmcnt(0)
	v_mfma_i32_16x16x64_i8 v[140:143], v[112:115], v[172:175], v[140:143]
	v_mfma_i32_16x16x64_i8 v[132:135], v[120:123], v[172:175], v[132:135]
	v_mfma_i32_16x16x64_i8 v[92:95], v[112:115], v[180:183], v[94:97]
	v_mfma_i32_16x16x64_i8 v[88:91], v[120:123], v[180:183], v[88:91]
	v_mfma_i32_16x16x64_i8 v[60:63], v[112:115], v[188:191], v[60:63]
	v_mfma_i32_16x16x64_i8 v[56:59], v[120:123], v[188:191], v[56:59]
	v_mfma_i32_16x16x64_i8 v[28:31], v[112:115], v[196:199], v[28:31]
	v_mfma_i32_16x16x64_i8 v[24:27], v[120:123], v[196:199], v[24:27]
	v_mfma_i32_16x16x64_i8 v[140:143], v[116:119], v[176:179], v[140:143]
	v_mfma_i32_16x16x64_i8 v[132:135], v[144:147], v[176:179], v[132:135]
	v_mfma_i32_16x16x64_i8 v[96:99], v[116:119], v[184:187], v[92:95]
	v_mfma_i32_16x16x64_i8 v[88:91], v[144:147], v[184:187], v[88:91]
	v_mfma_i32_16x16x64_i8 v[60:63], v[116:119], v[192:195], v[60:63]
	v_mfma_i32_16x16x64_i8 v[56:59], v[144:147], v[192:195], v[56:59]
	v_mfma_i32_16x16x64_i8 v[28:31], v[116:119], v[200:203], v[28:31]
	v_mfma_i32_16x16x64_i8 v[24:27], v[144:147], v[200:203], v[24:27]
	v_mfma_i32_16x16x64_i8 v[92:95], v[150:153], v[172:175], v[124:127]
	v_mfma_i32_16x16x64_i8 v[124:127], v[160:163], v[176:179], v[92:95]
	v_mfma_i32_16x16x64_i8 v[92:95], v[164:167], v[172:175], v[108:111]
	v_mfma_i32_16x16x64_i8 v[76:79], v[150:153], v[180:183], v[76:79]
	v_mfma_i32_16x16x64_i8 v[72:75], v[164:167], v[180:183], v[72:75]
	v_mfma_i32_16x16x64_i8 v[44:47], v[150:153], v[188:191], v[44:47]
	v_mfma_i32_16x16x64_i8 v[40:43], v[164:167], v[188:191], v[40:43]
	v_mfma_i32_16x16x64_i8 v[12:15], v[150:153], v[196:199], v[12:15]
	v_mfma_i32_16x16x64_i8 v[8:11], v[164:167], v[196:199], v[8:11]
	v_mfma_i32_16x16x64_i8 v[108:111], v[168:171], v[176:179], v[92:95]
	v_mfma_i32_16x16x64_i8 v[76:79], v[160:163], v[184:187], v[76:79]
	v_mfma_i32_16x16x64_i8 v[72:75], v[168:171], v[184:187], v[72:75]
	v_mfma_i32_16x16x64_i8 v[44:47], v[160:163], v[192:195], v[44:47]
	v_mfma_i32_16x16x64_i8 v[40:43], v[168:171], v[192:195], v[40:43]
	v_mfma_i32_16x16x64_i8 v[12:15], v[160:163], v[200:203], v[12:15]
	v_mfma_i32_16x16x64_i8 v[8:11], v[168:171], v[200:203], v[8:11]
	s_setprio 0
	s_waitcnt vmcnt(8)
	s_barrier
; #define G_STAGE(bufoff, gbase, voff) do { _Pragma("unroll") for (int _i = 0; _i < 2; ++_i) \
;         __builtin_amdgcn_global_load_lds((const unsigned*)((const char*)(gbase) + (voff)[_i]), (LAS unsigned*)(lds + (bufoff) + ldsw + _i * 8192), 16, 0, 0); } while (0)
; #define G_LDA(dst, b, h) do { _Pragma("unroll") for (int m = 0; m < 4; ++m) G_LD8(dst[m], lds + G_SA(b, h) + aoff + m * 2048); } while (0)
; #define G_WAIT_V(n) asm volatile("s_waitcnt vmcnt(" #n ")" ::: "memory")
; #define G_WAIT_L(n) asm volatile("s_waitcnt lgkmcnt(" #n ")" ::: "memory")
; #define G_BAR __builtin_amdgcn_s_barrier()
; #define G_SCHED __builtin_amdgcn_sched_barrier(0)
;     ...
;             G_LDA(At, 1, 1); G_STAGE(G_SB(1, 0), b02 + kstep, voffB); G_STAGE(G_SB(1, 1), b12 + kstep, voffB); G_STAGE(G_SA(1, 0), a02 + kstep, vA0);
;             G_WAIT_L(0); G_BAR; G_MMA(1, 0, At, B0); G_MMA(1, 1, At, B1); G_WAIT_V(8); G_BAR; G_SCHED;
;         }
	s_add_i32 s64, s66, s97
	v_lshl_add_u64 v[200:201], v[208:209], 0, s[38:39]
	s_mov_b32 m0, s64
	ds_read_b128 v[92:95], v158 offset:49152
	ds_read_b128 v[172:175], v158 offset:50176
	ds_read_b128 v[176:179], v158 offset:51200
	ds_read_b128 v[180:183], v158 offset:52224
	ds_read_b128 v[184:187], v158 offset:53248
	ds_read_b128 v[188:191], v158 offset:54272
	ds_read_b128 v[192:195], v158 offset:55296
	ds_read_b128 v[196:199], v158 offset:56320
	global_load_lds_dwordx4 v[200:201], off
	v_lshl_add_u64 v[200:201], v[210:211], 0, s[38:39]
	s_add_i32 m0, s64, 0x2000
	s_add_i32 s64, s67, s97
	global_load_lds_dwordx4 v[200:201], off
	v_lshl_add_u64 v[200:201], v[212:213], 0, s[38:39]
	s_mov_b32 m0, s64
	s_nop 0
	global_load_lds_dwordx4 v[200:201], off
	v_lshl_add_u64 v[200:201], v[204:205], 0, s[38:39]
	s_add_i32 m0, s64, 0x2000
	s_nop 0
	global_load_lds_dwordx4 v[200:201], off
	v_lshl_add_u64 v[200:201], v[206:207], 0, s[38:39]
	s_mov_b32 m0, s21
	s_nop 0
	global_load_lds_dwordx4 v[200:201], off
	v_lshl_add_u64 v[200:201], v[214:215], 0, s[38:39]
	s_mov_b32 m0, s22
	s_nop 0
	global_load_lds_dwordx4 v[200:201], off
	s_waitcnt lgkmcnt(0)
	s_barrier
	s_setprio 1
	s_waitcnt lgkmcnt(0)
	v_mfma_i32_16x16x64_i8 v[136:139], v[112:115], v[92:95], v[136:139]
	v_mfma_i32_16x16x64_i8 v[128:131], v[120:123], v[92:95], v[128:131]
	v_mfma_i32_16x16x64_i8 v[84:87], v[112:115], v[176:179], v[84:87]
	v_mfma_i32_16x16x64_i8 v[80:83], v[120:123], v[176:179], v[80:83]
	v_mfma_i32_16x16x64_i8 v[52:55], v[112:115], v[184:187], v[52:55]
	v_mfma_i32_16x16x64_i8 v[48:51], v[120:123], v[184:187], v[48:51]
	v_mfma_i32_16x16x64_i8 v[20:23], v[112:115], v[192:195], v[20:23]
	v_mfma_i32_16x16x64_i8 v[16:19], v[120:123], v[192:195], v[16:19]
	v_mfma_i32_16x16x64_i8 v[136:139], v[116:119], v[172:175], v[136:139]
	v_mfma_i32_16x16x64_i8 v[128:131], v[144:147], v[172:175], v[128:131]
	v_mfma_i32_16x16x64_i8 v[84:87], v[116:119], v[180:183], v[84:87]
	v_mfma_i32_16x16x64_i8 v[80:83], v[144:147], v[180:183], v[80:83]
	v_mfma_i32_16x16x64_i8 v[52:55], v[116:119], v[188:191], v[52:55]
	v_mfma_i32_16x16x64_i8 v[48:51], v[144:147], v[188:191], v[48:51]
	v_mfma_i32_16x16x64_i8 v[20:23], v[116:119], v[196:199], v[20:23]
	v_mfma_i32_16x16x64_i8 v[16:19], v[144:147], v[196:199], v[16:19]
	v_mfma_i32_16x16x64_i8 v[100:103], v[150:153], v[92:95], v[100:103]
	v_mfma_i32_16x16x64_i8 v[92:95], v[164:167], v[92:95], v[104:107]
	v_mfma_i32_16x16x64_i8 v[68:71], v[150:153], v[176:179], v[68:71]
	v_mfma_i32_16x16x64_i8 v[64:67], v[164:167], v[176:179], v[64:67]
	v_mfma_i32_16x16x64_i8 v[36:39], v[150:153], v[184:187], v[36:39]
	v_mfma_i32_16x16x64_i8 v[32:35], v[164:167], v[184:187], v[32:35]
	v_mfma_i32_16x16x64_i8 v[4:7], v[150:153], v[192:195], v[4:7]
	v_mfma_i32_16x16x64_i8 v[0:3], v[164:167], v[192:195], v[0:3]
	v_mfma_i32_16x16x64_i8 v[116:119], v[160:163], v[172:175], v[100:103]
	v_mfma_i32_16x16x64_i8 v[104:107], v[168:171], v[172:175], v[92:95]
	v_mfma_i32_16x16x64_i8 v[68:71], v[160:163], v[180:183], v[68:71]
	v_mfma_i32_16x16x64_i8 v[64:67], v[168:171], v[180:183], v[64:67]
	v_mfma_i32_16x16x64_i8 v[36:39], v[160:163], v[188:191], v[36:39]
	v_mfma_i32_16x16x64_i8 v[32:35], v[168:171], v[188:191], v[32:35]
	v_mfma_i32_16x16x64_i8 v[4:7], v[160:163], v[196:199], v[4:7]
	v_mfma_i32_16x16x64_i8 v[0:3], v[168:171], v[196:199], v[0:3]
	s_setprio 0
	s_waitcnt vmcnt(8)
	s_barrier
	s_add_u32 s45, s45, 0x100
	s_addc_u32 s59, s59, 0
	s_add_u32 s61, s61, 0x100
	s_addc_u32 s70, s70, 0
	s_add_u32 s71, s71, 0x100
	s_addc_u32 s75, s75, 0
	s_add_u32 s62, s62, 0x100
	s_addc_u32 s63, s63, 0
	s_cmp_ge_i32 s76, s3
	s_mov_b32 s64, s76
	s_cbranch_scc0 .LBB0_284
	v_readlane_b32 s78, v255, 11
	v_readlane_b32 s79, v255, 13
	s_branch .LBB0_289

; #define G_STAGE(bufoff, gbase, voff) do { _Pragma("unroll") for (int _i = 0; _i < 2; ++_i) \
;         __builtin_amdgcn_global_load_lds((const unsigned*)((const char*)(gbase) + (voff)[_i]), (LAS unsigned*)(lds + (bufoff) + ldsw + _i * 8192), 16, 0, 0); } while (0)
; #define G_LDA(dst, b, h) do { _Pragma("unroll") for (int m = 0; m < 4; ++m) G_LD8(dst[m], lds + G_SA(b, h) + aoff + m * 2048); } while (0)
; #define G_LDB(dst, b, h) do { _Pragma("unroll") for (int n = 0; n < 2; ++n) G_LD8(dst[n], lds + G_SB(b, h) + boff + n * 2048); } while (0)
; #define G_WAIT_V(n) asm volatile("s_waitcnt vmcnt(" #n ")" ::: "memory")
; #define G_WAIT_L(n) asm volatile("s_waitcnt lgkmcnt(" #n ")" ::: "memory")
; #define G_BAR __builtin_amdgcn_s_barrier()
; #define G_SCHED __builtin_amdgcn_sched_barrier(0)
;     __device__ __forceinline__ unsigned row_off(const Unit& u, int r, LAS unsigned char* lds) const { return (unsigned)((const LAS int*)(lds + LDS_STAGE + u.q * 4096))[r] * (unsigned)rowbytes; }
;     ...
;             const char* a11 = cur.a1 + (size_t)(t + 1) * kstep;
;             const char* a02 = last ? nxt.a0 : cur.a0 + (size_t)(t + 2) * kstep; const char* a12 = last ? nxt.a1 : cur.a1 + (size_t)(t + 2) * kstep;
;             const char* b02 = last ? nxt.b0 : cur.b0 + (size_t)(t + 2) * kstep; const char* b12 = last ? nxt.b1 : cur.b1 + (size_t)(t + 2) * kstep;
;             G_LDB(B0, 0, 0); G_LDB(B1, 0, 1); G_SCHED; G_LDA(At, 0, 0); G_STAGE(G_SA(1, 1), a11, vA1);
;             if constexpr (GATHER) { if (last) { int tz = tid; asm volatile("" : "+v"(tz));
; #pragma unroll
;                 for (int i = 0; i < 2; ++i) { int R, C; stage_rc(tz * 16 + i * 8192, R, C); gc0[i] = S.row_off(nxt, R, lds) + (unsigned)C * 2u; gc1[i] = S.row_off(nxt, 128 + R, lds) + (unsigned)C * 2u; } } }
;             G_WAIT_L(0); G_BAR; G_MMA(0, 0, At, B0); G_MMA(0, 1, At, B1); G_WAIT_V(8); G_BAR; G_SCHED;
;             G_LDA(At, 0, 1); G_STAGE(G_SB(0, 0), b02, voffB); G_STAGE(G_SB(0, 1), b12, voffB); G_STAGE(G_SA(0, 0), a02, vA0);
.LBB0_522:
	s_add_i32 s79, s56, 2
	ds_read_b128 v[142:145], v138
	ds_read_b128 v[146:149], v138 offset:1024
	ds_read_b128 v[150:153], v138 offset:2048
	ds_read_b128 v[154:157], v138 offset:3072
	ds_read_b128 v[158:161], v139
	ds_read_b128 v[162:165], v139 offset:1024
	ds_read_b128 v[166:169], v139 offset:2048
	ds_read_b128 v[170:173], v139 offset:3072
	s_add_u32 s80, s54, 0x80
	s_addc_u32 s57, s55, 0
	s_add_i32 s82, s72, s20
	s_add_i32 m0, s27, 0xc000
	s_add_i32 s81, s27, 0xe000
	s_add_i32 s83, s82, 0x2000
	s_cmp_eq_u32 s71, s56
	s_cselect_b32 s56, s48, s80
	s_cselect_b32 s59, s51, s78
	s_cselect_b32 s58, s50, s77
	s_cselect_b32 s61, s45, s63
	s_cselect_b32 s60, s44, s62
	s_cselect_b32 s57, s49, s57
	ds_read_b128 v[174:177], v140
	ds_read_b128 v[178:181], v140 offset:1024
	ds_read_b128 v[182:185], v140 offset:2048
	ds_read_b128 v[186:189], v140 offset:3072
	ds_read_b128 v[190:193], v140 offset:4096
	ds_read_b128 v[194:197], v140 offset:5120
	ds_read_b128 v[198:201], v140 offset:6144
	ds_read_b128 v[202:205], v140 offset:7168
	global_load_lds_dwordx4 v240, s[54:55]
	s_mov_b32 m0, s81
	s_nop 0
	global_load_lds_dwordx4 v242, s[54:55]
	s_waitcnt lgkmcnt(0)
	v_mov_b32_e32 v131, v129
	s_barrier
	s_setprio 1
	s_waitcnt lgkmcnt(0)
	v_mfma_f32_16x16x32_bf16 v[124:127], v[142:145], v[174:177], v[124:127]
	v_mfma_f32_16x16x32_bf16 v[120:123], v[150:153], v[174:177], v[120:123]
	v_mfma_f32_16x16x32_bf16 v[92:95], v[142:145], v[182:185], v[92:95]
	v_mfma_f32_16x16x32_bf16 v[88:91], v[150:153], v[182:185], v[88:91]
	v_mfma_f32_16x16x32_bf16 v[60:63], v[142:145], v[190:193], v[60:63]
	v_mfma_f32_16x16x32_bf16 v[56:59], v[150:153], v[190:193], v[56:59]
	v_mfma_f32_16x16x32_bf16 v[28:31], v[142:145], v[198:201], v[28:31]
	v_mfma_f32_16x16x32_bf16 v[24:27], v[150:153], v[198:201], v[24:27]
	v_mfma_f32_16x16x32_bf16 v[124:127], v[146:149], v[178:181], v[124:127]
	v_mfma_f32_16x16x32_bf16 v[120:123], v[154:157], v[178:181], v[120:123]
	v_mfma_f32_16x16x32_bf16 v[92:95], v[146:149], v[186:189], v[92:95]
	v_mfma_f32_16x16x32_bf16 v[88:91], v[154:157], v[186:189], v[88:91]
	v_mfma_f32_16x16x32_bf16 v[60:63], v[146:149], v[194:197], v[60:63]
	v_mfma_f32_16x16x32_bf16 v[56:59], v[154:157], v[194:197], v[56:59]
	v_mfma_f32_16x16x32_bf16 v[28:31], v[146:149], v[202:205], v[28:31]
	v_mfma_f32_16x16x32_bf16 v[24:27], v[154:157], v[202:205], v[24:27]
	v_mfma_f32_16x16x32_bf16 v[112:115], v[158:161], v[174:177], v[112:115]
	v_mfma_f32_16x16x32_bf16 v[104:107], v[166:169], v[174:177], v[104:107]
	v_mfma_f32_16x16x32_bf16 v[80:83], v[158:161], v[182:185], v[80:83]
	v_mfma_f32_16x16x32_bf16 v[72:75], v[166:169], v[182:185], v[72:75]
	v_mfma_f32_16x16x32_bf16 v[48:51], v[158:161], v[190:193], v[48:51]
	v_mfma_f32_16x16x32_bf16 v[40:43], v[166:169], v[190:193], v[40:43]
	v_mfma_f32_16x16x32_bf16 v[16:19], v[158:161], v[198:201], v[16:19]
	v_mfma_f32_16x16x32_bf16 v[8:11], v[166:169], v[198:201], v[8:11]
	v_mfma_f32_16x16x32_bf16 v[112:115], v[162:165], v[178:181], v[112:115]
	v_mfma_f32_16x16x32_bf16 v[104:107], v[170:173], v[178:181], v[104:107]
	v_mfma_f32_16x16x32_bf16 v[80:83], v[162:165], v[186:189], v[80:83]
	v_mfma_f32_16x16x32_bf16 v[72:75], v[170:173], v[186:189], v[72:75]
	v_mfma_f32_16x16x32_bf16 v[48:51], v[162:165], v[194:197], v[48:51]
	v_mfma_f32_16x16x32_bf16 v[40:43], v[170:173], v[194:197], v[40:43]
	v_mfma_f32_16x16x32_bf16 v[16:19], v[162:165], v[202:205], v[16:19]
	v_mfma_f32_16x16x32_bf16 v[8:11], v[170:173], v[202:205], v[8:11]
	s_setprio 0
	s_waitcnt vmcnt(8)
	s_barrier
	s_mov_b32 m0, s82
	ds_read_b128 v[174:177], v140 offset:16384
	ds_read_b128 v[178:181], v140 offset:17408
	ds_read_b128 v[182:185], v140 offset:18432
	ds_read_b128 v[186:189], v140 offset:19456
	ds_read_b128 v[190:193], v140 offset:20480
	ds_read_b128 v[194:197], v140 offset:21504
	ds_read_b128 v[198:201], v140 offset:22528
	ds_read_b128 v[202:205], v140 offset:23552
	v_mov_b32_e32 v133, v129
	global_load_lds_dwordx4 v244, s[60:61]
	v_mov_b32_e32 v207, v129
	s_mov_b32 m0, s83
	v_lshl_add_u64 v[208:209], s[60:61], 0, v[244:245]
	v_lshl_add_u64 v[210:211], s[60:61], 0, v[246:247]
	global_load_lds_dwordx4 v246, s[60:61]
	s_cselect_b32 s61, s47, s75
	s_cselect_b32 s60, s46, s64
	s_add_i32 s80, s73, s20
	s_mov_b32 m0, s80
	v_lshl_add_u64 v[212:213], s[60:61], 0, v[244:245]
	global_load_lds_dwordx4 v244, s[60:61]
	s_add_i32 m0, s80, 0x2000
	v_lshl_add_u64 v[214:215], s[60:61], 0, v[246:247]
	global_load_lds_dwordx4 v246, s[60:61]
	s_mov_b32 m0, s27
	v_lshl_add_u64 v[206:207], s[58:59], 0, v[240:241]
	global_load_lds_dwordx4 v240, s[58:59]
	s_mov_b32 m0, s33
	v_lshl_add_u64 v[216:217], s[58:59], 0, v[242:243]
	global_load_lds_dwordx4 v242, s[58:59]
	s_waitcnt lgkmcnt(0)
	s_barrier
; #define G_STAGE(bufoff, gbase, voff) do { _Pragma("unroll") for (int _i = 0; _i < 2; ++_i) \
;         __builtin_amdgcn_global_load_lds((const unsigned*)((const char*)(gbase) + (voff)[_i]), (LAS unsigned*)(lds + (bufoff) + ldsw + _i * 8192), 16, 0, 0); } while (0)
; #define G_LDA(dst, b, h) do { _Pragma("unroll") for (int m = 0; m < 4; ++m) G_LD8(dst[m], lds + G_SA(b, h) + aoff + m * 2048); } while (0)
; #define G_LDB(dst, b, h) do { _Pragma("unroll") for (int n = 0; n < 2; ++n) G_LD8(dst[n], lds + G_SB(b, h) + boff + n * 2048); } while (0)
; #define G_WAIT_V(n) asm volatile("s_waitcnt vmcnt(" #n ")" ::: "memory")
; #define G_WAIT_L(n) asm volatile("s_waitcnt lgkmcnt(" #n ")" ::: "memory")
; #define G_BAR __builtin_amdgcn_s_barrier()
; #define G_SCHED __builtin_amdgcn_sched_barrier(0)
;     ...
;             G_WAIT_L(0); G_BAR; G_MMA(1, 0, At, B0); G_MMA(1, 1, At, B1); G_WAIT_V(8); G_BAR; G_SCHED;
;             G_LDB(B0, 1, 0); G_LDB(B1, 1, 1); G_SCHED; G_LDA(At, 1, 0); G_STAGE(G_SA(0, 1), a12, vA1);
;             G_WAIT_L(0); G_BAR; G_MMA(0, 0, At, B0); G_MMA(0, 1, At, B1); G_WAIT_V(8); G_BAR; G_SCHED;
	s_setprio 1
	s_waitcnt lgkmcnt(0)
	v_mfma_f32_16x16x32_bf16 v[116:119], v[142:145], v[174:177], v[116:119]
	v_mfma_f32_16x16x32_bf16 v[108:111], v[150:153], v[174:177], v[108:111]
	v_mfma_f32_16x16x32_bf16 v[84:87], v[142:145], v[182:185], v[84:87]
	v_mfma_f32_16x16x32_bf16 v[76:79], v[150:153], v[182:185], v[76:79]
	v_mfma_f32_16x16x32_bf16 v[52:55], v[142:145], v[190:193], v[52:55]
	v_mfma_f32_16x16x32_bf16 v[44:47], v[150:153], v[190:193], v[44:47]
	v_mfma_f32_16x16x32_bf16 v[20:23], v[142:145], v[198:201], v[20:23]
	v_mfma_f32_16x16x32_bf16 v[12:15], v[150:153], v[198:201], v[12:15]
	v_mfma_f32_16x16x32_bf16 v[116:119], v[146:149], v[178:181], v[116:119]
	v_mfma_f32_16x16x32_bf16 v[108:111], v[154:157], v[178:181], v[108:111]
	v_mfma_f32_16x16x32_bf16 v[84:87], v[146:149], v[186:189], v[84:87]
	v_mfma_f32_16x16x32_bf16 v[76:79], v[154:157], v[186:189], v[76:79]
	v_mfma_f32_16x16x32_bf16 v[52:55], v[146:149], v[194:197], v[52:55]
	v_mfma_f32_16x16x32_bf16 v[44:47], v[154:157], v[194:197], v[44:47]
	v_mfma_f32_16x16x32_bf16 v[20:23], v[146:149], v[202:205], v[20:23]
	v_mfma_f32_16x16x32_bf16 v[12:15], v[154:157], v[202:205], v[12:15]
	v_mfma_f32_16x16x32_bf16 v[100:103], v[158:161], v[174:177], v[100:103]
	v_mfma_f32_16x16x32_bf16 v[96:99], v[166:169], v[174:177], v[96:99]
	v_mfma_f32_16x16x32_bf16 v[68:71], v[158:161], v[182:185], v[68:71]
	v_mfma_f32_16x16x32_bf16 v[64:67], v[166:169], v[182:185], v[64:67]
	v_mfma_f32_16x16x32_bf16 v[36:39], v[158:161], v[190:193], v[36:39]
	v_mfma_f32_16x16x32_bf16 v[32:35], v[166:169], v[190:193], v[32:35]
	v_mfma_f32_16x16x32_bf16 v[4:7], v[158:161], v[198:201], v[4:7]
	v_mfma_f32_16x16x32_bf16 v[0:3], v[166:169], v[198:201], v[0:3]
	v_mfma_f32_16x16x32_bf16 v[100:103], v[162:165], v[178:181], v[100:103]
	v_mfma_f32_16x16x32_bf16 v[96:99], v[170:173], v[178:181], v[96:99]
	v_mfma_f32_16x16x32_bf16 v[68:71], v[162:165], v[186:189], v[68:71]
	v_mfma_f32_16x16x32_bf16 v[64:67], v[170:173], v[186:189], v[64:67]
	v_mfma_f32_16x16x32_bf16 v[36:39], v[162:165], v[194:197], v[36:39]
	v_mfma_f32_16x16x32_bf16 v[32:35], v[170:173], v[194:197], v[32:35]
	v_mfma_f32_16x16x32_bf16 v[4:7], v[162:165], v[202:205], v[4:7]
	v_mfma_f32_16x16x32_bf16 v[0:3], v[170:173], v[202:205], v[0:3]
	s_setprio 0
	s_waitcnt vmcnt(8)
	s_barrier
	s_add_i32 s58, 0, 0x18000
	v_add_u32_e32 v131, s58, v137
	s_add_i32 s59, 0, 0x1c000
	ds_read_b128 v[142:145], v131
	ds_read_b128 v[146:149], v131 offset:1024
	ds_read_b128 v[150:153], v131 offset:2048
	ds_read_b128 v[154:157], v131 offset:3072
	v_add_u32_e32 v131, s59, v137
	ds_read_b128 v[158:161], v131
	ds_read_b128 v[162:165], v131 offset:1024
	ds_read_b128 v[166:169], v131 offset:2048
	ds_read_b128 v[170:173], v131 offset:3072
	s_mov_b32 m0, s66
	ds_read_b128 v[174:177], v140 offset:32768
	ds_read_b128 v[178:181], v140 offset:33792
	ds_read_b128 v[182:185], v140 offset:34816
	ds_read_b128 v[186:189], v140 offset:35840
	ds_read_b128 v[190:193], v140 offset:36864
	ds_read_b128 v[194:197], v140 offset:37888
	ds_read_b128 v[198:201], v140 offset:38912
	ds_read_b128 v[202:205], v140 offset:39936
	global_load_lds_dwordx4 v240, s[56:57]
	s_mov_b32 m0, s67
	s_nop 0
	global_load_lds_dwordx4 v242, s[56:57]
	s_waitcnt lgkmcnt(0)
	s_barrier
	s_setprio 1
	s_waitcnt lgkmcnt(0)
	v_mfma_f32_16x16x32_bf16 v[124:127], v[142:145], v[174:177], v[124:127]
	v_mfma_f32_16x16x32_bf16 v[120:123], v[150:153], v[174:177], v[120:123]
	v_mfma_f32_16x16x32_bf16 v[92:95], v[142:145], v[182:185], v[92:95]
	v_mfma_f32_16x16x32_bf16 v[88:91], v[150:153], v[182:185], v[88:91]
	v_mfma_f32_16x16x32_bf16 v[60:63], v[142:145], v[190:193], v[60:63]
	v_mfma_f32_16x16x32_bf16 v[56:59], v[150:153], v[190:193], v[56:59]
	v_mfma_f32_16x16x32_bf16 v[28:31], v[142:145], v[198:201], v[28:31]
	v_mfma_f32_16x16x32_bf16 v[24:27], v[150:153], v[198:201], v[24:27]
	v_mfma_f32_16x16x32_bf16 v[124:127], v[146:149], v[178:181], v[124:127]
	v_mfma_f32_16x16x32_bf16 v[120:123], v[154:157], v[178:181], v[120:123]
	v_mfma_f32_16x16x32_bf16 v[92:95], v[146:149], v[186:189], v[92:95]
	v_mfma_f32_16x16x32_bf16 v[88:91], v[154:157], v[186:189], v[88:91]
	v_mfma_f32_16x16x32_bf16 v[60:63], v[146:149], v[194:197], v[60:63]
	v_mfma_f32_16x16x32_bf16 v[56:59], v[154:157], v[194:197], v[56:59]
	v_mfma_f32_16x16x32_bf16 v[28:31], v[146:149], v[202:205], v[28:31]
	v_mfma_f32_16x16x32_bf16 v[24:27], v[154:157], v[202:205], v[24:27]
	v_mfma_f32_16x16x32_bf16 v[112:115], v[158:161], v[174:177], v[112:115]
	v_mfma_f32_16x16x32_bf16 v[104:107], v[166:169], v[174:177], v[104:107]
	v_mfma_f32_16x16x32_bf16 v[80:83], v[158:161], v[182:185], v[80:83]
	v_mfma_f32_16x16x32_bf16 v[72:75], v[166:169], v[182:185], v[72:75]
	v_mfma_f32_16x16x32_bf16 v[48:51], v[158:161], v[190:193], v[48:51]
	v_mfma_f32_16x16x32_bf16 v[40:43], v[166:169], v[190:193], v[40:43]
	v_mfma_f32_16x16x32_bf16 v[16:19], v[158:161], v[198:201], v[16:19]
	v_mfma_f32_16x16x32_bf16 v[8:11], v[166:169], v[198:201], v[8:11]
	v_mfma_f32_16x16x32_bf16 v[112:115], v[162:165], v[178:181], v[112:115]
	v_mfma_f32_16x16x32_bf16 v[104:107], v[170:173], v[178:181], v[104:107]
	v_mfma_f32_16x16x32_bf16 v[80:83], v[162:165], v[186:189], v[80:83]
	v_mfma_f32_16x16x32_bf16 v[72:75], v[170:173], v[186:189], v[72:75]
	v_mfma_f32_16x16x32_bf16 v[48:51], v[162:165], v[194:197], v[48:51]
	v_mfma_f32_16x16x32_bf16 v[40:43], v[170:173], v[194:197], v[40:43]
	v_mfma_f32_16x16x32_bf16 v[16:19], v[162:165], v[202:205], v[16:19]
	v_mfma_f32_16x16x32_bf16 v[8:11], v[170:173], v[202:205], v[8:11]
	s_setprio 0
	s_waitcnt vmcnt(8)
	s_barrier
; #define G_STAGE(bufoff, gbase, voff) do { _Pragma("unroll") for (int _i = 0; _i < 2; ++_i) \
;         __builtin_amdgcn_global_load_lds((const unsigned*)((const char*)(gbase) + (voff)[_i]), (LAS unsigned*)(lds + (bufoff) + ldsw + _i * 8192), 16, 0, 0); } while (0)
; #define G_LDA(dst, b, h) do { _Pragma("unroll") for (int m = 0; m < 4; ++m) G_LD8(dst[m], lds + G_SA(b, h) + aoff + m * 2048); } while (0)
; #define G_WAIT_V(n) asm volatile("s_waitcnt vmcnt(" #n ")" ::: "memory")
; #define G_WAIT_L(n) asm volatile("s_waitcnt lgkmcnt(" #n ")" ::: "memory")
; #define G_BAR __builtin_amdgcn_s_barrier()
; #define G_SCHED __builtin_amdgcn_sched_barrier(0)
;     ...
;             G_LDA(At, 1, 1); G_STAGE(G_SB(1, 0), b02 + kstep, voffB); G_STAGE(G_SB(1, 1), b12 + kstep, voffB); G_STAGE(G_SA(1, 0), a02 + kstep, vA0);
;             G_WAIT_L(0); G_BAR; G_MMA(1, 0, At, B0); G_MMA(1, 1, At, B1); G_WAIT_V(8); G_BAR; G_SCHED;
;         }
	s_add_i32 s56, s58, s20
	v_lshl_add_u64 v[202:203], v[208:209], 0, s[40:41]
	s_mov_b32 m0, s56
	ds_read_b128 v[130:133], v140 offset:49152
	ds_read_b128 v[174:177], v140 offset:50176
	ds_read_b128 v[178:181], v140 offset:51200
	ds_read_b128 v[182:185], v140 offset:52224
	ds_read_b128 v[186:189], v140 offset:53248
	ds_read_b128 v[190:193], v140 offset:54272
	ds_read_b128 v[194:197], v140 offset:55296
	ds_read_b128 v[198:201], v140 offset:56320
	global_load_lds_dwordx4 v[202:203], off
	v_lshl_add_u64 v[202:203], v[210:211], 0, s[40:41]
	s_add_i32 m0, s56, 0x2000
	s_add_i32 s56, s59, s20
	global_load_lds_dwordx4 v[202:203], off
	v_lshl_add_u64 v[202:203], v[212:213], 0, s[40:41]
	s_mov_b32 m0, s56
	s_nop 0
	global_load_lds_dwordx4 v[202:203], off
	v_lshl_add_u64 v[202:203], v[214:215], 0, s[40:41]
	s_add_i32 m0, s56, 0x2000
	s_nop 0
	global_load_lds_dwordx4 v[202:203], off
	v_lshl_add_u64 v[202:203], v[206:207], 0, s[40:41]
	s_mov_b32 m0, s69
	s_nop 0
	global_load_lds_dwordx4 v[202:203], off
	v_lshl_add_u64 v[202:203], v[216:217], 0, s[40:41]
	s_mov_b32 m0, s70
	s_nop 0
	global_load_lds_dwordx4 v[202:203], off
	s_waitcnt lgkmcnt(0)
	s_barrier
	s_setprio 1
	s_waitcnt lgkmcnt(0)
	v_mfma_f32_16x16x32_bf16 v[116:119], v[142:145], v[130:133], v[116:119]
	v_mfma_f32_16x16x32_bf16 v[108:111], v[150:153], v[130:133], v[108:111]
	v_mfma_f32_16x16x32_bf16 v[84:87], v[142:145], v[178:181], v[84:87]
	v_mfma_f32_16x16x32_bf16 v[76:79], v[150:153], v[178:181], v[76:79]
	v_mfma_f32_16x16x32_bf16 v[52:55], v[142:145], v[186:189], v[52:55]
	v_mfma_f32_16x16x32_bf16 v[44:47], v[150:153], v[186:189], v[44:47]
	v_mfma_f32_16x16x32_bf16 v[20:23], v[142:145], v[194:197], v[20:23]
	v_mfma_f32_16x16x32_bf16 v[12:15], v[150:153], v[194:197], v[12:15]
	v_mfma_f32_16x16x32_bf16 v[116:119], v[146:149], v[174:177], v[116:119]
	v_mfma_f32_16x16x32_bf16 v[108:111], v[154:157], v[174:177], v[108:111]
	v_mfma_f32_16x16x32_bf16 v[84:87], v[146:149], v[182:185], v[84:87]
	v_mfma_f32_16x16x32_bf16 v[76:79], v[154:157], v[182:185], v[76:79]
	v_mfma_f32_16x16x32_bf16 v[52:55], v[146:149], v[190:193], v[52:55]
	v_mfma_f32_16x16x32_bf16 v[44:47], v[154:157], v[190:193], v[44:47]
	v_mfma_f32_16x16x32_bf16 v[20:23], v[146:149], v[198:201], v[20:23]
	v_mfma_f32_16x16x32_bf16 v[12:15], v[154:157], v[198:201], v[12:15]
	v_mfma_f32_16x16x32_bf16 v[100:103], v[158:161], v[130:133], v[100:103]
	v_mfma_f32_16x16x32_bf16 v[96:99], v[166:169], v[130:133], v[96:99]
	v_mfma_f32_16x16x32_bf16 v[68:71], v[158:161], v[178:181], v[68:71]
	v_mfma_f32_16x16x32_bf16 v[64:67], v[166:169], v[178:181], v[64:67]
	v_mfma_f32_16x16x32_bf16 v[36:39], v[158:161], v[186:189], v[36:39]
	v_mfma_f32_16x16x32_bf16 v[32:35], v[166:169], v[186:189], v[32:35]
	v_mfma_f32_16x16x32_bf16 v[4:7], v[158:161], v[194:197], v[4:7]
	v_mfma_f32_16x16x32_bf16 v[0:3], v[166:169], v[194:197], v[0:3]
	v_mfma_f32_16x16x32_bf16 v[100:103], v[162:165], v[174:177], v[100:103]
	v_mfma_f32_16x16x32_bf16 v[96:99], v[170:173], v[174:177], v[96:99]
	v_mfma_f32_16x16x32_bf16 v[68:71], v[162:165], v[182:185], v[68:71]
	v_mfma_f32_16x16x32_bf16 v[64:67], v[170:173], v[182:185], v[64:67]
	v_mfma_f32_16x16x32_bf16 v[36:39], v[162:165], v[190:193], v[36:39]
	v_mfma_f32_16x16x32_bf16 v[32:35], v[170:173], v[190:193], v[32:35]
	v_mfma_f32_16x16x32_bf16 v[4:7], v[162:165], v[198:201], v[4:7]
	v_mfma_f32_16x16x32_bf16 v[0:3], v[170:173], v[198:201], v[0:3]
	s_setprio 0
	s_waitcnt vmcnt(8)
	s_barrier
	s_add_u32 s62, s62, 0x100
	s_addc_u32 s63, s63, 0
	s_add_u32 s64, s64, 0x100
	s_addc_u32 s75, s75, 0
	s_add_u32 s77, s77, 0x100
	s_addc_u32 s78, s78, 0
	s_add_u32 s54, s54, 0x100
	s_addc_u32 s55, s55, 0
	s_cmp_ge_i32 s79, s0
	s_mov_b32 s56, s79
	s_cbranch_scc0 .LBB0_522
	v_readlane_b32 s78, v255, 11
	v_readlane_b32 s79, v255, 13
	s_and_b64 vcc, exec, s[42:43]
	s_cbranch_vccz .LBB0_525

; __device__ __forceinline__ int lane_id() { int l; asm volatile("v_mbcnt_lo_u32_b32 %0, -1, 0\n\tv_mbcnt_hi_u32_b32 %0, -1, %0" : "=v"(l)); return l; }
; #define G_STAGE(bufoff, gbase, voff) do { _Pragma("unroll") for (int _i = 0; _i < 2; ++_i) \
;         __builtin_amdgcn_global_load_lds((const unsigned*)((const char*)(gbase) + (voff)[_i]), (LAS unsigned*)(lds + (bufoff) + ldsw + _i * 8192), 16, 0, 0); } while (0)
; #define G_LDA(dst, b, h) do { _Pragma("unroll") for (int m = 0; m < 4; ++m) G_LD8(dst[m], lds + G_SA(b, h) + aoff + m * 2048); } while (0)
; #define G_BAR __builtin_amdgcn_s_barrier()
;     ...
;         for (int t = 0; t < nt; t += 2) {
;             const bool last = (t == nt - 2);
;             { const int tz_ = wid * 64 + lane_id();
; #pragma unroll
;               for (int i = 0; i < 2; ++i) { int R, C; stage_rc(tz_ * 16 + i * 8192, R, C); const int Rb = Epi::PERM ? ((R & ~31) + perm32(R & 31)) : R;
;                   voffA[i] = (unsigned)(R * S.multA * S.pitchA + C) * 2u; voffB[i] = (unsigned)(Rb * S.multB * S.pitchB + C) * 2u; } }
;             if constexpr (GATHER) asm volatile("" : "+v"(gc0[0]), "+v"(gc0[1]), "+v"(gc1[0]), "+v"(gc1[1]));
;             if constexpr (PREF) { if (t == nt - 4) S.prefetch(nxt, lds); }
;             const char* a11 = cur.a1 + (size_t)(t + 1) * kstep;
;             const char* a02 = last ? nxt.a0 : cur.a0 + (size_t)(t + 2) * kstep; const char* a12 = last ? nxt.a1 : cur.a1 + (size_t)(t + 2) * kstep;
;             const char* b02 = last ? nxt.b0 : cur.b0 + (size_t)(t + 2) * kstep; const char* b12 = last ? nxt.b1 : cur.b1 + (size_t)(t + 2) * kstep;
;             G_LDB(B0, 0, 0); G_LDB(B1, 0, 1); G_SCHED; G_LDA(At, 0, 0); G_STAGE(G_SA(1, 1), a11, vA1);
;             if constexpr (GATHER) { if (last) { int tz = tid; asm volatile("" : "+v"(tz));
; #pragma unroll
;                 for (int i = 0; i < 2; ++i) { int R, C; stage_rc(tz * 16 + i * 8192, R, C); gc0[i] = S.row_off(nxt, R, lds) + (unsigned)C * 2u; gc1[i] = S.row_off(nxt, 128 + R, lds) + (unsigned)C * 2u; } } }
;             G_WAIT_L(0); G_BAR; G_MMA(0, 0, At, B0); G_MMA(0, 1, At, B1); G_WAIT_V(8); G_BAR; G_SCHED;
;             G_LDA(At, 0, 1); G_STAGE(G_SB(0, 0), b02, voffB); G_STAGE(G_SB(0, 1), b12, voffB); G_STAGE(G_SA(0, 0), a02, vA0);
;             G_WAIT_L(0); G_BAR; G_MMA(1, 0, At, B0); G_MMA(1, 1, At, B1); G_WAIT_V(8); G_BAR; G_SCHED;
.LBB0_549:
	s_add_i32 s80, s58, 2
	ds_read_b128 v[130:133], v138
	ds_read_b128 v[142:145], v138 offset:1024
	ds_read_b128 v[146:149], v138 offset:2048
	ds_read_b128 v[150:153], v138 offset:3072
	ds_read_b128 v[154:157], v139
	ds_read_b128 v[158:161], v139 offset:1024
	ds_read_b128 v[162:165], v139 offset:2048
	ds_read_b128 v[166:169], v139 offset:3072
	s_add_u32 s81, s56, 0x80
	s_addc_u32 s59, s57, 0
	s_add_i32 s83, s75, s20
	s_add_i32 m0, s67, 0xc000
	s_add_i32 s82, s67, 0xe000
	s_add_i32 s84, s83, 0x2000
	s_cmp_eq_u32 s74, s58
	s_cselect_b32 s58, s44, s81
	s_cselect_b32 s61, s43, s79
	s_cselect_b32 s60, s42, s65
	s_cselect_b32 s63, s47, s53
	s_cselect_b32 s62, s46, s41
	s_cselect_b32 s59, s45, s59
	ds_read_b128 v[170:173], v140
	ds_read_b128 v[174:177], v140 offset:1024
	ds_read_b128 v[178:181], v140 offset:2048
	ds_read_b128 v[182:185], v140 offset:3072
	ds_read_b128 v[186:189], v140 offset:4096
	ds_read_b128 v[190:193], v140 offset:5120
	ds_read_b128 v[194:197], v140 offset:6144
	ds_read_b128 v[198:201], v140 offset:7168
	global_load_lds_dwordx4 v240, s[56:57]
	s_mov_b32 m0, s82
	v_mov_b32_e32 v205, v129
	global_load_lds_dwordx4 v242, s[56:57]
	s_waitcnt lgkmcnt(0)
	s_barrier
	s_setprio 1
	s_waitcnt lgkmcnt(0)
	v_mfma_f32_16x16x32_bf16 v[124:127], v[130:133], v[170:173], v[124:127]
	v_mfma_f32_16x16x32_bf16 v[120:123], v[146:149], v[170:173], v[120:123]
	v_mfma_f32_16x16x32_bf16 v[108:111], v[130:133], v[178:181], v[108:111]
	v_mfma_f32_16x16x32_bf16 v[104:107], v[146:149], v[178:181], v[104:107]
	v_mfma_f32_16x16x32_bf16 v[92:95], v[130:133], v[186:189], v[92:95]
	v_mfma_f32_16x16x32_bf16 v[88:91], v[146:149], v[186:189], v[88:91]
	v_mfma_f32_16x16x32_bf16 v[76:79], v[130:133], v[194:197], v[76:79]
	v_mfma_f32_16x16x32_bf16 v[72:75], v[146:149], v[194:197], v[72:75]
	v_mfma_f32_16x16x32_bf16 v[124:127], v[142:145], v[174:177], v[124:127]
	v_mfma_f32_16x16x32_bf16 v[120:123], v[150:153], v[174:177], v[120:123]
	v_mfma_f32_16x16x32_bf16 v[108:111], v[142:145], v[182:185], v[108:111]
	v_mfma_f32_16x16x32_bf16 v[104:107], v[150:153], v[182:185], v[104:107]
	v_mfma_f32_16x16x32_bf16 v[92:95], v[142:145], v[190:193], v[92:95]
	v_mfma_f32_16x16x32_bf16 v[88:91], v[150:153], v[190:193], v[88:91]
	v_mfma_f32_16x16x32_bf16 v[76:79], v[142:145], v[198:201], v[76:79]
	v_mfma_f32_16x16x32_bf16 v[72:75], v[150:153], v[198:201], v[72:75]
	v_mfma_f32_16x16x32_bf16 v[116:119], v[154:157], v[170:173], v[116:119]
	v_mfma_f32_16x16x32_bf16 v[112:115], v[162:165], v[170:173], v[112:115]
	v_mfma_f32_16x16x32_bf16 v[100:103], v[154:157], v[178:181], v[100:103]
	v_mfma_f32_16x16x32_bf16 v[96:99], v[162:165], v[178:181], v[96:99]
	v_mfma_f32_16x16x32_bf16 v[84:87], v[154:157], v[186:189], v[84:87]
	v_mfma_f32_16x16x32_bf16 v[80:83], v[162:165], v[186:189], v[80:83]
	v_mfma_f32_16x16x32_bf16 v[68:71], v[154:157], v[194:197], v[68:71]
	v_mfma_f32_16x16x32_bf16 v[64:67], v[162:165], v[194:197], v[64:67]
	v_mfma_f32_16x16x32_bf16 v[116:119], v[158:161], v[174:177], v[116:119]
	v_mfma_f32_16x16x32_bf16 v[112:115], v[166:169], v[174:177], v[112:115]
	v_mfma_f32_16x16x32_bf16 v[100:103], v[158:161], v[182:185], v[100:103]
	v_mfma_f32_16x16x32_bf16 v[96:99], v[166:169], v[182:185], v[96:99]
	v_mfma_f32_16x16x32_bf16 v[84:87], v[158:161], v[190:193], v[84:87]
	v_mfma_f32_16x16x32_bf16 v[80:83], v[166:169], v[190:193], v[80:83]
	v_mfma_f32_16x16x32_bf16 v[68:71], v[158:161], v[198:201], v[68:71]
	v_mfma_f32_16x16x32_bf16 v[64:67], v[166:169], v[198:201], v[64:67]
	s_setprio 0
	s_waitcnt vmcnt(8)
	s_barrier
	s_mov_b32 m0, s83
	ds_read_b128 v[170:173], v140 offset:16384
	ds_read_b128 v[174:177], v140 offset:17408
	ds_read_b128 v[178:181], v140 offset:18432
	ds_read_b128 v[182:185], v140 offset:19456
	ds_read_b128 v[186:189], v140 offset:20480
	ds_read_b128 v[190:193], v140 offset:21504
	ds_read_b128 v[194:197], v140 offset:22528
	ds_read_b128 v[198:201], v140 offset:23552
	global_load_lds_dwordx4 v244, s[62:63]
	s_mov_b32 m0, s84
	s_cselect_b32 s83, s49, s64
	s_cselect_b32 s82, s48, s55
	s_add_i32 s81, s76, s20
	global_load_lds_dwordx4 v246, s[62:63]
	s_mov_b32 m0, s81
	v_mov_b32_e32 v203, v129
	global_load_lds_dwordx4 v244, s[82:83]
	s_add_i32 m0, s81, 0x2000
	v_mov_b32_e32 v207, v129
	global_load_lds_dwordx4 v246, s[82:83]
	s_mov_b32 m0, s67
	v_lshl_add_u64 v[208:209], s[62:63], 0, v[244:245]
	global_load_lds_dwordx4 v240, s[60:61]
	s_mov_b32 m0, s68
	v_lshl_add_u64 v[210:211], s[62:63], 0, v[246:247]
	global_load_lds_dwordx4 v242, s[60:61]
	s_waitcnt lgkmcnt(0)
	v_lshl_add_u64 v[202:203], s[82:83], 0, v[244:245]
	v_lshl_add_u64 v[206:207], s[82:83], 0, v[246:247]
	v_lshl_add_u64 v[212:213], s[60:61], 0, v[240:241]
	v_lshl_add_u64 v[214:215], s[60:61], 0, v[242:243]
	s_barrier
; #define G_STAGE(bufoff, gbase, voff) do { _Pragma("unroll") for (int _i = 0; _i < 2; ++_i) \
;         __builtin_amdgcn_global_load_lds((const unsigned*)((const char*)(gbase) + (voff)[_i]), (LAS unsigned*)(lds + (bufoff) + ldsw + _i * 8192), 16, 0, 0); } while (0)
; #define G_LDA(dst, b, h) do { _Pragma("unroll") for (int m = 0; m < 4; ++m) G_LD8(dst[m], lds + G_SA(b, h) + aoff + m * 2048); } while (0)
; #define G_LDB(dst, b, h) do { _Pragma("unroll") for (int n = 0; n < 2; ++n) G_LD8(dst[n], lds + G_SB(b, h) + boff + n * 2048); } while (0)
; #define G_WAIT_V(n) asm volatile("s_waitcnt vmcnt(" #n ")" ::: "memory")
; #define G_WAIT_L(n) asm volatile("s_waitcnt lgkmcnt(" #n ")" ::: "memory")
; #define G_BAR __builtin_amdgcn_s_barrier()
; #define G_SCHED __builtin_amdgcn_sched_barrier(0)
;     ...
;             G_WAIT_L(0); G_BAR; G_MMA(1, 0, At, B0); G_MMA(1, 1, At, B1); G_WAIT_V(8); G_BAR; G_SCHED;
;             G_LDB(B0, 1, 0); G_LDB(B1, 1, 1); G_SCHED; G_LDA(At, 1, 0); G_STAGE(G_SA(0, 1), a12, vA1);
;             G_WAIT_L(0); G_BAR; G_MMA(0, 0, At, B0); G_MMA(0, 1, At, B1); G_WAIT_V(8); G_BAR; G_SCHED;
	s_setprio 1
	s_waitcnt lgkmcnt(0)
	v_mfma_f32_16x16x32_bf16 v[60:63], v[130:133], v[170:173], v[60:63]
	v_mfma_f32_16x16x32_bf16 v[56:59], v[146:149], v[170:173], v[56:59]
	v_mfma_f32_16x16x32_bf16 v[44:47], v[130:133], v[178:181], v[44:47]
	v_mfma_f32_16x16x32_bf16 v[40:43], v[146:149], v[178:181], v[40:43]
	v_mfma_f32_16x16x32_bf16 v[28:31], v[130:133], v[186:189], v[28:31]
	v_mfma_f32_16x16x32_bf16 v[24:27], v[146:149], v[186:189], v[24:27]
	v_mfma_f32_16x16x32_bf16 v[12:15], v[130:133], v[194:197], v[12:15]
	v_mfma_f32_16x16x32_bf16 v[8:11], v[146:149], v[194:197], v[8:11]
	v_mfma_f32_16x16x32_bf16 v[60:63], v[142:145], v[174:177], v[60:63]
	v_mfma_f32_16x16x32_bf16 v[56:59], v[150:153], v[174:177], v[56:59]
	v_mfma_f32_16x16x32_bf16 v[44:47], v[142:145], v[182:185], v[44:47]
	v_mfma_f32_16x16x32_bf16 v[40:43], v[150:153], v[182:185], v[40:43]
	v_mfma_f32_16x16x32_bf16 v[28:31], v[142:145], v[190:193], v[28:31]
	v_mfma_f32_16x16x32_bf16 v[24:27], v[150:153], v[190:193], v[24:27]
	v_mfma_f32_16x16x32_bf16 v[12:15], v[142:145], v[198:201], v[12:15]
	v_mfma_f32_16x16x32_bf16 v[8:11], v[150:153], v[198:201], v[8:11]
	v_mfma_f32_16x16x32_bf16 v[52:55], v[154:157], v[170:173], v[52:55]
	v_mfma_f32_16x16x32_bf16 v[48:51], v[162:165], v[170:173], v[48:51]
	v_mfma_f32_16x16x32_bf16 v[36:39], v[154:157], v[178:181], v[36:39]
	v_mfma_f32_16x16x32_bf16 v[32:35], v[162:165], v[178:181], v[32:35]
	v_mfma_f32_16x16x32_bf16 v[20:23], v[154:157], v[186:189], v[20:23]
	v_mfma_f32_16x16x32_bf16 v[16:19], v[162:165], v[186:189], v[16:19]
	v_mfma_f32_16x16x32_bf16 v[4:7], v[154:157], v[194:197], v[4:7]
	v_mfma_f32_16x16x32_bf16 v[0:3], v[162:165], v[194:197], v[0:3]
	v_mfma_f32_16x16x32_bf16 v[52:55], v[158:161], v[174:177], v[52:55]
	v_mfma_f32_16x16x32_bf16 v[48:51], v[166:169], v[174:177], v[48:51]
	v_mfma_f32_16x16x32_bf16 v[36:39], v[158:161], v[182:185], v[36:39]
	v_mfma_f32_16x16x32_bf16 v[32:35], v[166:169], v[182:185], v[32:35]
	v_mfma_f32_16x16x32_bf16 v[20:23], v[158:161], v[190:193], v[20:23]
	v_mfma_f32_16x16x32_bf16 v[16:19], v[166:169], v[190:193], v[16:19]
	v_mfma_f32_16x16x32_bf16 v[4:7], v[158:161], v[198:201], v[4:7]
	v_mfma_f32_16x16x32_bf16 v[0:3], v[166:169], v[198:201], v[0:3]
	s_setprio 0
	s_waitcnt vmcnt(8)
	s_barrier
	s_add_i32 s60, 0, 0x18000
	v_add_u32_e32 v141, s60, v137
	s_add_i32 s61, 0, 0x1c000
	ds_read_b128 v[130:133], v141
	ds_read_b128 v[142:145], v141 offset:1024
	ds_read_b128 v[146:149], v141 offset:2048
	ds_read_b128 v[150:153], v141 offset:3072
	v_add_u32_e32 v141, s61, v137
	ds_read_b128 v[154:157], v141
	ds_read_b128 v[158:161], v141 offset:1024
	ds_read_b128 v[162:165], v141 offset:2048
	ds_read_b128 v[166:169], v141 offset:3072
	s_mov_b32 m0, s69
	ds_read_b128 v[170:173], v140 offset:32768
	ds_read_b128 v[174:177], v140 offset:33792
	ds_read_b128 v[178:181], v140 offset:34816
	ds_read_b128 v[182:185], v140 offset:35840
	ds_read_b128 v[186:189], v140 offset:36864
	ds_read_b128 v[190:193], v140 offset:37888
	ds_read_b128 v[194:197], v140 offset:38912
	ds_read_b128 v[198:201], v140 offset:39936
	global_load_lds_dwordx4 v240, s[58:59]
	s_mov_b32 m0, s70
	s_nop 0
	global_load_lds_dwordx4 v242, s[58:59]
	s_waitcnt lgkmcnt(0)
	s_barrier
	s_setprio 1
	s_waitcnt lgkmcnt(0)
	v_mfma_f32_16x16x32_bf16 v[124:127], v[130:133], v[170:173], v[124:127]
	v_mfma_f32_16x16x32_bf16 v[120:123], v[146:149], v[170:173], v[120:123]
	v_mfma_f32_16x16x32_bf16 v[108:111], v[130:133], v[178:181], v[108:111]
	v_mfma_f32_16x16x32_bf16 v[104:107], v[146:149], v[178:181], v[104:107]
	v_mfma_f32_16x16x32_bf16 v[92:95], v[130:133], v[186:189], v[92:95]
	v_mfma_f32_16x16x32_bf16 v[88:91], v[146:149], v[186:189], v[88:91]
	v_mfma_f32_16x16x32_bf16 v[76:79], v[130:133], v[194:197], v[76:79]
	v_mfma_f32_16x16x32_bf16 v[72:75], v[146:149], v[194:197], v[72:75]
	v_mfma_f32_16x16x32_bf16 v[124:127], v[142:145], v[174:177], v[124:127]
	v_mfma_f32_16x16x32_bf16 v[120:123], v[150:153], v[174:177], v[120:123]
	v_mfma_f32_16x16x32_bf16 v[108:111], v[142:145], v[182:185], v[108:111]
	v_mfma_f32_16x16x32_bf16 v[104:107], v[150:153], v[182:185], v[104:107]
	v_mfma_f32_16x16x32_bf16 v[92:95], v[142:145], v[190:193], v[92:95]
	v_mfma_f32_16x16x32_bf16 v[88:91], v[150:153], v[190:193], v[88:91]
	v_mfma_f32_16x16x32_bf16 v[76:79], v[142:145], v[198:201], v[76:79]
	v_mfma_f32_16x16x32_bf16 v[72:75], v[150:153], v[198:201], v[72:75]
	v_mfma_f32_16x16x32_bf16 v[116:119], v[154:157], v[170:173], v[116:119]
	v_mfma_f32_16x16x32_bf16 v[112:115], v[162:165], v[170:173], v[112:115]
	v_mfma_f32_16x16x32_bf16 v[100:103], v[154:157], v[178:181], v[100:103]
	v_mfma_f32_16x16x32_bf16 v[96:99], v[162:165], v[178:181], v[96:99]
	v_mfma_f32_16x16x32_bf16 v[84:87], v[154:157], v[186:189], v[84:87]
	v_mfma_f32_16x16x32_bf16 v[80:83], v[162:165], v[186:189], v[80:83]
	v_mfma_f32_16x16x32_bf16 v[68:71], v[154:157], v[194:197], v[68:71]
	v_mfma_f32_16x16x32_bf16 v[64:67], v[162:165], v[194:197], v[64:67]
	v_mfma_f32_16x16x32_bf16 v[116:119], v[158:161], v[174:177], v[116:119]
	v_mfma_f32_16x16x32_bf16 v[112:115], v[166:169], v[174:177], v[112:115]
	v_mfma_f32_16x16x32_bf16 v[100:103], v[158:161], v[182:185], v[100:103]
	v_mfma_f32_16x16x32_bf16 v[96:99], v[166:169], v[182:185], v[96:99]
	v_mfma_f32_16x16x32_bf16 v[84:87], v[158:161], v[190:193], v[84:87]
	v_mfma_f32_16x16x32_bf16 v[80:83], v[166:169], v[190:193], v[80:83]
	v_mfma_f32_16x16x32_bf16 v[68:71], v[158:161], v[198:201], v[68:71]
	v_mfma_f32_16x16x32_bf16 v[64:67], v[166:169], v[198:201], v[64:67]
	s_setprio 0
	s_waitcnt vmcnt(8)
	s_barrier
; #define G_STAGE(bufoff, gbase, voff) do { _Pragma("unroll") for (int _i = 0; _i < 2; ++_i) \
;         __builtin_amdgcn_global_load_lds((const unsigned*)((const char*)(gbase) + (voff)[_i]), (LAS unsigned*)(lds + (bufoff) + ldsw + _i * 8192), 16, 0, 0); } while (0)
; #define G_LDA(dst, b, h) do { _Pragma("unroll") for (int m = 0; m < 4; ++m) G_LD8(dst[m], lds + G_SA(b, h) + aoff + m * 2048); } while (0)
; #define G_WAIT_V(n) asm volatile("s_waitcnt vmcnt(" #n ")" ::: "memory")
; #define G_WAIT_L(n) asm volatile("s_waitcnt lgkmcnt(" #n ")" ::: "memory")
; #define G_BAR __builtin_amdgcn_s_barrier()
; #define G_SCHED __builtin_amdgcn_sched_barrier(0)
;     ...
;             G_LDA(At, 1, 1); G_STAGE(G_SB(1, 0), b02 + kstep, voffB); G_STAGE(G_SB(1, 1), b12 + kstep, voffB); G_STAGE(G_SA(1, 0), a02 + kstep, vA0);
;             G_WAIT_L(0); G_BAR; G_MMA(1, 0, At, B0); G_MMA(1, 1, At, B1); G_WAIT_V(8); G_BAR; G_SCHED;
;         }
	s_add_i32 s58, s60, s20
	v_lshl_add_u64 v[204:205], v[208:209], 0, s[8:9]
	s_mov_b32 m0, s58
	ds_read_b128 v[170:173], v140 offset:49152
	ds_read_b128 v[174:177], v140 offset:50176
	ds_read_b128 v[178:181], v140 offset:51200
	ds_read_b128 v[182:185], v140 offset:52224
	ds_read_b128 v[186:189], v140 offset:53248
	ds_read_b128 v[190:193], v140 offset:54272
	ds_read_b128 v[194:197], v140 offset:55296
	ds_read_b128 v[198:201], v140 offset:56320
	global_load_lds_dwordx4 v[204:205], off
	v_lshl_add_u64 v[204:205], v[210:211], 0, s[8:9]
	s_add_i32 m0, s58, 0x2000
	s_add_i32 s58, s61, s20
	global_load_lds_dwordx4 v[204:205], off
	v_lshl_add_u64 v[202:203], v[202:203], 0, s[8:9]
	s_mov_b32 m0, s58
	s_nop 0
	global_load_lds_dwordx4 v[202:203], off
	v_lshl_add_u64 v[202:203], v[206:207], 0, s[8:9]
	s_add_i32 m0, s58, 0x2000
	s_nop 0
	global_load_lds_dwordx4 v[202:203], off
	v_lshl_add_u64 v[202:203], v[212:213], 0, s[8:9]
	s_mov_b32 m0, s72
	s_nop 0
	global_load_lds_dwordx4 v[202:203], off
	v_lshl_add_u64 v[202:203], v[214:215], 0, s[8:9]
	s_mov_b32 m0, s73
	s_nop 0
	global_load_lds_dwordx4 v[202:203], off
	s_waitcnt lgkmcnt(0)
	s_barrier
	s_setprio 1
	s_waitcnt lgkmcnt(0)
	v_mfma_f32_16x16x32_bf16 v[60:63], v[130:133], v[170:173], v[60:63]
	v_mfma_f32_16x16x32_bf16 v[56:59], v[146:149], v[170:173], v[56:59]
	v_mfma_f32_16x16x32_bf16 v[44:47], v[130:133], v[178:181], v[44:47]
	v_mfma_f32_16x16x32_bf16 v[40:43], v[146:149], v[178:181], v[40:43]
	v_mfma_f32_16x16x32_bf16 v[28:31], v[130:133], v[186:189], v[28:31]
	v_mfma_f32_16x16x32_bf16 v[24:27], v[146:149], v[186:189], v[24:27]
	v_mfma_f32_16x16x32_bf16 v[12:15], v[130:133], v[194:197], v[12:15]
	v_mfma_f32_16x16x32_bf16 v[8:11], v[146:149], v[194:197], v[8:11]
	v_mfma_f32_16x16x32_bf16 v[60:63], v[142:145], v[174:177], v[60:63]
	v_mfma_f32_16x16x32_bf16 v[56:59], v[150:153], v[174:177], v[56:59]
	v_mfma_f32_16x16x32_bf16 v[44:47], v[142:145], v[182:185], v[44:47]
	v_mfma_f32_16x16x32_bf16 v[40:43], v[150:153], v[182:185], v[40:43]
	v_mfma_f32_16x16x32_bf16 v[28:31], v[142:145], v[190:193], v[28:31]
	v_mfma_f32_16x16x32_bf16 v[24:27], v[150:153], v[190:193], v[24:27]
	v_mfma_f32_16x16x32_bf16 v[12:15], v[142:145], v[198:201], v[12:15]
	v_mfma_f32_16x16x32_bf16 v[8:11], v[150:153], v[198:201], v[8:11]
	v_mfma_f32_16x16x32_bf16 v[52:55], v[154:157], v[170:173], v[52:55]
	v_mfma_f32_16x16x32_bf16 v[48:51], v[162:165], v[170:173], v[48:51]
	v_mfma_f32_16x16x32_bf16 v[36:39], v[154:157], v[178:181], v[36:39]
	v_mfma_f32_16x16x32_bf16 v[32:35], v[162:165], v[178:181], v[32:35]
	v_mfma_f32_16x16x32_bf16 v[20:23], v[154:157], v[186:189], v[20:23]
	v_mfma_f32_16x16x32_bf16 v[16:19], v[162:165], v[186:189], v[16:19]
	v_mfma_f32_16x16x32_bf16 v[4:7], v[154:157], v[194:197], v[4:7]
	v_mfma_f32_16x16x32_bf16 v[0:3], v[162:165], v[194:197], v[0:3]
	v_mfma_f32_16x16x32_bf16 v[52:55], v[158:161], v[174:177], v[52:55]
	v_mfma_f32_16x16x32_bf16 v[48:51], v[166:169], v[174:177], v[48:51]
	v_mfma_f32_16x16x32_bf16 v[36:39], v[158:161], v[182:185], v[36:39]
	v_mfma_f32_16x16x32_bf16 v[32:35], v[166:169], v[182:185], v[32:35]
	v_mfma_f32_16x16x32_bf16 v[20:23], v[158:161], v[190:193], v[20:23]
	v_mfma_f32_16x16x32_bf16 v[16:19], v[166:169], v[190:193], v[16:19]
	v_mfma_f32_16x16x32_bf16 v[4:7], v[158:161], v[198:201], v[4:7]
	v_mfma_f32_16x16x32_bf16 v[0:3], v[166:169], v[198:201], v[0:3]
	s_setprio 0
	s_waitcnt vmcnt(8)
	s_barrier
	s_add_u32 s41, s41, 0x100
	s_addc_u32 s53, s53, 0
	s_add_u32 s55, s55, 0x100
	s_addc_u32 s64, s64, 0
	s_add_u32 s65, s65, 0x100
	s_addc_u32 s79, s79, 0
	s_add_u32 s56, s56, 0x100
	s_addc_u32 s57, s57, 0
	s_cmp_ge_i32 s80, s0
	s_mov_b32 s58, s80
	s_cbranch_scc0 .LBB0_549
	v_readlane_b32 s79, v255, 13
	s_and_b64 vcc, exec, s[38:39]
	s_cbranch_vccz .LBB0_552

; __device__ __forceinline__ int lane_id() { int l; asm volatile("v_mbcnt_lo_u32_b32 %0, -1, 0\n\tv_mbcnt_hi_u32_b32 %0, -1, %0" : "=v"(l)); return l; }
; #define G_STAGE(bufoff, gbase, voff) do { _Pragma("unroll") for (int _i = 0; _i < 2; ++_i) \
;         __builtin_amdgcn_global_load_lds((const unsigned*)((const char*)(gbase) + (voff)[_i]), (LAS unsigned*)(lds + (bufoff) + ldsw + _i * 8192), 16, 0, 0); } while (0)
; #define G_LDA(dst, b, h) do { _Pragma("unroll") for (int m = 0; m < 4; ++m) G_LD8(dst[m], lds + G_SA(b, h) + aoff + m * 2048); } while (0)
; #define G_BAR __builtin_amdgcn_s_barrier()
;     ...
;         for (int t = 0; t < nt; t += 2) {
;             const bool last = (t == nt - 2);
;             { const int tz_ = wid * 64 + lane_id();
; #pragma unroll
;               for (int i = 0; i < 2; ++i) { int R, C; stage_rc(tz_ * 16 + i * 8192, R, C); const int Rb = Epi::PERM ? ((R & ~31) + perm32(R & 31)) : R;
;                   voffA[i] = (unsigned)(R * S.multA * S.pitchA + C) * 2u; voffB[i] = (unsigned)(Rb * S.multB * S.pitchB + C) * 2u; } }
;             if constexpr (GATHER) asm volatile("" : "+v"(gc0[0]), "+v"(gc0[1]), "+v"(gc1[0]), "+v"(gc1[1]));
;             if constexpr (PREF) { if (t == nt - 4) S.prefetch(nxt, lds); }
;             const char* a11 = cur.a1 + (size_t)(t + 1) * kstep;
;             const char* a02 = last ? nxt.a0 : cur.a0 + (size_t)(t + 2) * kstep; const char* a12 = last ? nxt.a1 : cur.a1 + (size_t)(t + 2) * kstep;
;             const char* b02 = last ? nxt.b0 : cur.b0 + (size_t)(t + 2) * kstep; const char* b12 = last ? nxt.b1 : cur.b1 + (size_t)(t + 2) * kstep;
;             G_LDB(B0, 0, 0); G_LDB(B1, 0, 1); G_SCHED; G_LDA(At, 0, 0); G_STAGE(G_SA(1, 1), a11, vA1);
;             if constexpr (GATHER) { if (last) { int tz = tid; asm volatile("" : "+v"(tz));
; #pragma unroll
;                 for (int i = 0; i < 2; ++i) { int R, C; stage_rc(tz * 16 + i * 8192, R, C); gc0[i] = S.row_off(nxt, R, lds) + (unsigned)C * 2u; gc1[i] = S.row_off(nxt, 128 + R, lds) + (unsigned)C * 2u; } } }
;             G_WAIT_L(0); G_BAR; G_MMA(0, 0, At, B0); G_MMA(0, 1, At, B1); G_WAIT_V(8); G_BAR; G_SCHED;
;             G_LDA(At, 0, 1); G_STAGE(G_SB(0, 0), b02, voffB); G_STAGE(G_SB(0, 1), b12, voffB); G_STAGE(G_SA(0, 0), a02, vA0);
;             G_WAIT_L(0); G_BAR; G_MMA(1, 0, At, B0); G_MMA(1, 1, At, B1); G_WAIT_V(8); G_BAR; G_SCHED;
.LBB0_576:
	s_add_i32 s71, s52, 2
	ds_read_b128 v[138:141], v134
	ds_read_b128 v[142:145], v134 offset:1024
	ds_read_b128 v[146:149], v134 offset:2048
	ds_read_b128 v[150:153], v134 offset:3072
	ds_read_b128 v[154:157], v135
	ds_read_b128 v[158:161], v135 offset:1024
	ds_read_b128 v[162:165], v135 offset:2048
	ds_read_b128 v[166:169], v135 offset:3072
	s_add_u32 s72, s50, 0x80
	s_addc_u32 s53, s51, 0
	s_add_i32 s75, s22, s20
	s_add_i32 m0, s62, 0xc000
	s_add_i32 s74, s62, 0xe000
	s_add_i32 s76, s75, 0x2000
	s_cmp_eq_u32 s23, s52
	s_cselect_b32 s52, s38, s72
	s_cselect_b32 s55, s37, s70
	s_cselect_b32 s54, s36, s59
	s_cselect_b32 s57, s41, s45
	s_cselect_b32 s56, s40, s35
	s_cselect_b32 s53, s39, s53
	ds_read_b128 v[170:173], v136
	ds_read_b128 v[174:177], v136 offset:1024
	ds_read_b128 v[178:181], v136 offset:2048
	ds_read_b128 v[182:185], v136 offset:3072
	ds_read_b128 v[186:189], v136 offset:4096
	ds_read_b128 v[190:193], v136 offset:5120
	ds_read_b128 v[194:197], v136 offset:6144
	ds_read_b128 v[198:201], v136 offset:7168
	global_load_lds_dwordx4 v240, s[50:51]
	s_mov_b32 m0, s74
	v_mov_b32_e32 v205, v129
	global_load_lds_dwordx4 v242, s[50:51]
	s_waitcnt lgkmcnt(0)
	s_barrier
	s_setprio 1
	s_waitcnt lgkmcnt(0)
	v_mfma_f32_16x16x32_bf16 v[124:127], v[138:141], v[170:173], v[124:127]
	v_mfma_f32_16x16x32_bf16 v[120:123], v[146:149], v[170:173], v[120:123]
	v_mfma_f32_16x16x32_bf16 v[108:111], v[138:141], v[178:181], v[108:111]
	v_mfma_f32_16x16x32_bf16 v[104:107], v[146:149], v[178:181], v[104:107]
	v_mfma_f32_16x16x32_bf16 v[92:95], v[138:141], v[186:189], v[92:95]
	v_mfma_f32_16x16x32_bf16 v[88:91], v[146:149], v[186:189], v[88:91]
	v_mfma_f32_16x16x32_bf16 v[76:79], v[138:141], v[194:197], v[76:79]
	v_mfma_f32_16x16x32_bf16 v[72:75], v[146:149], v[194:197], v[72:75]
	v_mfma_f32_16x16x32_bf16 v[124:127], v[142:145], v[174:177], v[124:127]
	v_mfma_f32_16x16x32_bf16 v[120:123], v[150:153], v[174:177], v[120:123]
	v_mfma_f32_16x16x32_bf16 v[108:111], v[142:145], v[182:185], v[108:111]
	v_mfma_f32_16x16x32_bf16 v[104:107], v[150:153], v[182:185], v[104:107]
	v_mfma_f32_16x16x32_bf16 v[92:95], v[142:145], v[190:193], v[92:95]
	v_mfma_f32_16x16x32_bf16 v[88:91], v[150:153], v[190:193], v[88:91]
	v_mfma_f32_16x16x32_bf16 v[76:79], v[142:145], v[198:201], v[76:79]
	v_mfma_f32_16x16x32_bf16 v[72:75], v[150:153], v[198:201], v[72:75]
	v_mfma_f32_16x16x32_bf16 v[116:119], v[154:157], v[170:173], v[116:119]
	v_mfma_f32_16x16x32_bf16 v[112:115], v[162:165], v[170:173], v[112:115]
	v_mfma_f32_16x16x32_bf16 v[100:103], v[154:157], v[178:181], v[100:103]
	v_mfma_f32_16x16x32_bf16 v[96:99], v[162:165], v[178:181], v[96:99]
	v_mfma_f32_16x16x32_bf16 v[84:87], v[154:157], v[186:189], v[84:87]
	v_mfma_f32_16x16x32_bf16 v[80:83], v[162:165], v[186:189], v[80:83]
	v_mfma_f32_16x16x32_bf16 v[68:71], v[154:157], v[194:197], v[68:71]
	v_mfma_f32_16x16x32_bf16 v[64:67], v[162:165], v[194:197], v[64:67]
	v_mfma_f32_16x16x32_bf16 v[116:119], v[158:161], v[174:177], v[116:119]
	v_mfma_f32_16x16x32_bf16 v[112:115], v[166:169], v[174:177], v[112:115]
	v_mfma_f32_16x16x32_bf16 v[100:103], v[158:161], v[182:185], v[100:103]
	v_mfma_f32_16x16x32_bf16 v[96:99], v[166:169], v[182:185], v[96:99]
	v_mfma_f32_16x16x32_bf16 v[84:87], v[158:161], v[190:193], v[84:87]
	v_mfma_f32_16x16x32_bf16 v[80:83], v[166:169], v[190:193], v[80:83]
	v_mfma_f32_16x16x32_bf16 v[68:71], v[158:161], v[198:201], v[68:71]
	v_mfma_f32_16x16x32_bf16 v[64:67], v[166:169], v[198:201], v[64:67]
	s_setprio 0
	s_waitcnt vmcnt(8)
	s_barrier
	s_mov_b32 m0, s75
	ds_read_b128 v[170:173], v136 offset:16384
	ds_read_b128 v[174:177], v136 offset:17408
	ds_read_b128 v[178:181], v136 offset:18432
	ds_read_b128 v[182:185], v136 offset:19456
	ds_read_b128 v[186:189], v136 offset:20480
	ds_read_b128 v[190:193], v136 offset:21504
	ds_read_b128 v[194:197], v136 offset:22528
	ds_read_b128 v[198:201], v136 offset:23552
	global_load_lds_dwordx4 v244, s[56:57]
	s_mov_b32 m0, s76
	s_cselect_b32 s73, s43, s58
	s_cselect_b32 s72, s42, s49
	s_add_i32 s74, s24, s20
	global_load_lds_dwordx4 v246, s[56:57]
	s_mov_b32 m0, s74
	v_mov_b32_e32 v203, v129
	global_load_lds_dwordx4 v244, s[72:73]
	s_add_i32 m0, s74, 0x2000
	v_mov_b32_e32 v207, v129
	global_load_lds_dwordx4 v246, s[72:73]
	s_mov_b32 m0, s62
	v_lshl_add_u64 v[208:209], s[56:57], 0, v[244:245]
	global_load_lds_dwordx4 v240, s[54:55]
	s_mov_b32 m0, s63
	v_lshl_add_u64 v[210:211], s[56:57], 0, v[246:247]
	global_load_lds_dwordx4 v242, s[54:55]
	s_waitcnt lgkmcnt(0)
	v_lshl_add_u64 v[202:203], s[72:73], 0, v[244:245]
	v_lshl_add_u64 v[206:207], s[72:73], 0, v[246:247]
	v_lshl_add_u64 v[212:213], s[54:55], 0, v[240:241]
	v_lshl_add_u64 v[214:215], s[54:55], 0, v[242:243]
	s_barrier
; #define G_STAGE(bufoff, gbase, voff) do { _Pragma("unroll") for (int _i = 0; _i < 2; ++_i) \
;         __builtin_amdgcn_global_load_lds((const unsigned*)((const char*)(gbase) + (voff)[_i]), (LAS unsigned*)(lds + (bufoff) + ldsw + _i * 8192), 16, 0, 0); } while (0)
; #define G_LDA(dst, b, h) do { _Pragma("unroll") for (int m = 0; m < 4; ++m) G_LD8(dst[m], lds + G_SA(b, h) + aoff + m * 2048); } while (0)
; #define G_LDB(dst, b, h) do { _Pragma("unroll") for (int n = 0; n < 2; ++n) G_LD8(dst[n], lds + G_SB(b, h) + boff + n * 2048); } while (0)
; #define G_WAIT_V(n) asm volatile("s_waitcnt vmcnt(" #n ")" ::: "memory")
; #define G_WAIT_L(n) asm volatile("s_waitcnt lgkmcnt(" #n ")" ::: "memory")
; #define G_BAR __builtin_amdgcn_s_barrier()
; #define G_SCHED __builtin_amdgcn_sched_barrier(0)
;     ...
;             G_WAIT_L(0); G_BAR; G_MMA(1, 0, At, B0); G_MMA(1, 1, At, B1); G_WAIT_V(8); G_BAR; G_SCHED;
;             G_LDB(B0, 1, 0); G_LDB(B1, 1, 1); G_SCHED; G_LDA(At, 1, 0); G_STAGE(G_SA(0, 1), a12, vA1);
;             G_WAIT_L(0); G_BAR; G_MMA(0, 0, At, B0); G_MMA(0, 1, At, B1); G_WAIT_V(8); G_BAR; G_SCHED;
	s_setprio 1
	s_waitcnt lgkmcnt(0)
	v_mfma_f32_16x16x32_bf16 v[60:63], v[138:141], v[170:173], v[60:63]
	v_mfma_f32_16x16x32_bf16 v[56:59], v[146:149], v[170:173], v[56:59]
	v_mfma_f32_16x16x32_bf16 v[44:47], v[138:141], v[178:181], v[44:47]
	v_mfma_f32_16x16x32_bf16 v[40:43], v[146:149], v[178:181], v[40:43]
	v_mfma_f32_16x16x32_bf16 v[28:31], v[138:141], v[186:189], v[28:31]
	v_mfma_f32_16x16x32_bf16 v[24:27], v[146:149], v[186:189], v[24:27]
	v_mfma_f32_16x16x32_bf16 v[12:15], v[138:141], v[194:197], v[12:15]
	v_mfma_f32_16x16x32_bf16 v[8:11], v[146:149], v[194:197], v[8:11]
	v_mfma_f32_16x16x32_bf16 v[60:63], v[142:145], v[174:177], v[60:63]
	v_mfma_f32_16x16x32_bf16 v[56:59], v[150:153], v[174:177], v[56:59]
	v_mfma_f32_16x16x32_bf16 v[44:47], v[142:145], v[182:185], v[44:47]
	v_mfma_f32_16x16x32_bf16 v[40:43], v[150:153], v[182:185], v[40:43]
	v_mfma_f32_16x16x32_bf16 v[28:31], v[142:145], v[190:193], v[28:31]
	v_mfma_f32_16x16x32_bf16 v[24:27], v[150:153], v[190:193], v[24:27]
	v_mfma_f32_16x16x32_bf16 v[12:15], v[142:145], v[198:201], v[12:15]
	v_mfma_f32_16x16x32_bf16 v[8:11], v[150:153], v[198:201], v[8:11]
	v_mfma_f32_16x16x32_bf16 v[52:55], v[154:157], v[170:173], v[52:55]
	v_mfma_f32_16x16x32_bf16 v[48:51], v[162:165], v[170:173], v[48:51]
	v_mfma_f32_16x16x32_bf16 v[36:39], v[154:157], v[178:181], v[36:39]
	v_mfma_f32_16x16x32_bf16 v[32:35], v[162:165], v[178:181], v[32:35]
	v_mfma_f32_16x16x32_bf16 v[20:23], v[154:157], v[186:189], v[20:23]
	v_mfma_f32_16x16x32_bf16 v[16:19], v[162:165], v[186:189], v[16:19]
	v_mfma_f32_16x16x32_bf16 v[4:7], v[154:157], v[194:197], v[4:7]
	v_mfma_f32_16x16x32_bf16 v[0:3], v[162:165], v[194:197], v[0:3]
	v_mfma_f32_16x16x32_bf16 v[52:55], v[158:161], v[174:177], v[52:55]
	v_mfma_f32_16x16x32_bf16 v[48:51], v[166:169], v[174:177], v[48:51]
	v_mfma_f32_16x16x32_bf16 v[36:39], v[158:161], v[182:185], v[36:39]
	v_mfma_f32_16x16x32_bf16 v[32:35], v[166:169], v[182:185], v[32:35]
	v_mfma_f32_16x16x32_bf16 v[20:23], v[158:161], v[190:193], v[20:23]
	v_mfma_f32_16x16x32_bf16 v[16:19], v[166:169], v[190:193], v[16:19]
	v_mfma_f32_16x16x32_bf16 v[4:7], v[158:161], v[198:201], v[4:7]
	v_mfma_f32_16x16x32_bf16 v[0:3], v[166:169], v[198:201], v[0:3]
	s_setprio 0
	s_waitcnt vmcnt(8)
	s_barrier
	s_add_i32 s54, 0, 0x18000
	v_add_u32_e32 v137, s54, v133
	s_add_i32 s55, 0, 0x1c000
	ds_read_b128 v[138:141], v137
	ds_read_b128 v[142:145], v137 offset:1024
	ds_read_b128 v[146:149], v137 offset:2048
	ds_read_b128 v[150:153], v137 offset:3072
	v_add_u32_e32 v137, s55, v133
	ds_read_b128 v[154:157], v137
	ds_read_b128 v[158:161], v137 offset:1024
	ds_read_b128 v[162:165], v137 offset:2048
	ds_read_b128 v[166:169], v137 offset:3072
	s_mov_b32 m0, s64
	ds_read_b128 v[170:173], v136 offset:32768
	ds_read_b128 v[174:177], v136 offset:33792
	ds_read_b128 v[178:181], v136 offset:34816
	ds_read_b128 v[182:185], v136 offset:35840
	ds_read_b128 v[186:189], v136 offset:36864
	ds_read_b128 v[190:193], v136 offset:37888
	ds_read_b128 v[194:197], v136 offset:38912
	ds_read_b128 v[198:201], v136 offset:39936
	global_load_lds_dwordx4 v240, s[52:53]
	s_mov_b32 m0, s65
	s_nop 0
	global_load_lds_dwordx4 v242, s[52:53]
	s_waitcnt lgkmcnt(0)
	s_barrier
	s_setprio 1
	s_waitcnt lgkmcnt(0)
	v_mfma_f32_16x16x32_bf16 v[124:127], v[138:141], v[170:173], v[124:127]
	v_mfma_f32_16x16x32_bf16 v[120:123], v[146:149], v[170:173], v[120:123]
	v_mfma_f32_16x16x32_bf16 v[108:111], v[138:141], v[178:181], v[108:111]
	v_mfma_f32_16x16x32_bf16 v[104:107], v[146:149], v[178:181], v[104:107]
	v_mfma_f32_16x16x32_bf16 v[92:95], v[138:141], v[186:189], v[92:95]
	v_mfma_f32_16x16x32_bf16 v[88:91], v[146:149], v[186:189], v[88:91]
	v_mfma_f32_16x16x32_bf16 v[76:79], v[138:141], v[194:197], v[76:79]
	v_mfma_f32_16x16x32_bf16 v[72:75], v[146:149], v[194:197], v[72:75]
	v_mfma_f32_16x16x32_bf16 v[124:127], v[142:145], v[174:177], v[124:127]
	v_mfma_f32_16x16x32_bf16 v[120:123], v[150:153], v[174:177], v[120:123]
	v_mfma_f32_16x16x32_bf16 v[108:111], v[142:145], v[182:185], v[108:111]
	v_mfma_f32_16x16x32_bf16 v[104:107], v[150:153], v[182:185], v[104:107]
	v_mfma_f32_16x16x32_bf16 v[92:95], v[142:145], v[190:193], v[92:95]
	v_mfma_f32_16x16x32_bf16 v[88:91], v[150:153], v[190:193], v[88:91]
	v_mfma_f32_16x16x32_bf16 v[76:79], v[142:145], v[198:201], v[76:79]
	v_mfma_f32_16x16x32_bf16 v[72:75], v[150:153], v[198:201], v[72:75]
	v_mfma_f32_16x16x32_bf16 v[116:119], v[154:157], v[170:173], v[116:119]
	v_mfma_f32_16x16x32_bf16 v[112:115], v[162:165], v[170:173], v[112:115]
	v_mfma_f32_16x16x32_bf16 v[100:103], v[154:157], v[178:181], v[100:103]
	v_mfma_f32_16x16x32_bf16 v[96:99], v[162:165], v[178:181], v[96:99]
	v_mfma_f32_16x16x32_bf16 v[84:87], v[154:157], v[186:189], v[84:87]
	v_mfma_f32_16x16x32_bf16 v[80:83], v[162:165], v[186:189], v[80:83]
	v_mfma_f32_16x16x32_bf16 v[68:71], v[154:157], v[194:197], v[68:71]
	v_mfma_f32_16x16x32_bf16 v[64:67], v[162:165], v[194:197], v[64:67]
	v_mfma_f32_16x16x32_bf16 v[116:119], v[158:161], v[174:177], v[116:119]
	v_mfma_f32_16x16x32_bf16 v[112:115], v[166:169], v[174:177], v[112:115]
	v_mfma_f32_16x16x32_bf16 v[100:103], v[158:161], v[182:185], v[100:103]
	v_mfma_f32_16x16x32_bf16 v[96:99], v[166:169], v[182:185], v[96:99]
	v_mfma_f32_16x16x32_bf16 v[84:87], v[158:161], v[190:193], v[84:87]
	v_mfma_f32_16x16x32_bf16 v[80:83], v[166:169], v[190:193], v[80:83]
	v_mfma_f32_16x16x32_bf16 v[68:71], v[158:161], v[198:201], v[68:71]
	v_mfma_f32_16x16x32_bf16 v[64:67], v[166:169], v[198:201], v[64:67]
	s_setprio 0
	s_waitcnt vmcnt(8)
	s_barrier
; #define G_STAGE(bufoff, gbase, voff) do { _Pragma("unroll") for (int _i = 0; _i < 2; ++_i) \
;         __builtin_amdgcn_global_load_lds((const unsigned*)((const char*)(gbase) + (voff)[_i]), (LAS unsigned*)(lds + (bufoff) + ldsw + _i * 8192), 16, 0, 0); } while (0)
; #define G_LDA(dst, b, h) do { _Pragma("unroll") for (int m = 0; m < 4; ++m) G_LD8(dst[m], lds + G_SA(b, h) + aoff + m * 2048); } while (0)
; #define G_WAIT_V(n) asm volatile("s_waitcnt vmcnt(" #n ")" ::: "memory")
; #define G_WAIT_L(n) asm volatile("s_waitcnt lgkmcnt(" #n ")" ::: "memory")
; #define G_BAR __builtin_amdgcn_s_barrier()
; #define G_SCHED __builtin_amdgcn_sched_barrier(0)
;     ...
;             G_LDA(At, 1, 1); G_STAGE(G_SB(1, 0), b02 + kstep, voffB); G_STAGE(G_SB(1, 1), b12 + kstep, voffB); G_STAGE(G_SA(1, 0), a02 + kstep, vA0);
;             G_WAIT_L(0); G_BAR; G_MMA(1, 0, At, B0); G_MMA(1, 1, At, B1); G_WAIT_V(8); G_BAR; G_SCHED;
;         }
	s_add_i32 s52, s54, s20
	v_lshl_add_u64 v[204:205], v[208:209], 0, s[6:7]
	s_mov_b32 m0, s52
	ds_read_b128 v[170:173], v136 offset:49152
	ds_read_b128 v[174:177], v136 offset:50176
	ds_read_b128 v[178:181], v136 offset:51200
	ds_read_b128 v[182:185], v136 offset:52224
	ds_read_b128 v[186:189], v136 offset:53248
	ds_read_b128 v[190:193], v136 offset:54272
	ds_read_b128 v[194:197], v136 offset:55296
	ds_read_b128 v[198:201], v136 offset:56320
	global_load_lds_dwordx4 v[204:205], off
	v_lshl_add_u64 v[204:205], v[210:211], 0, s[6:7]
	s_add_i32 m0, s52, 0x2000
	s_add_i32 s52, s55, s20
	global_load_lds_dwordx4 v[204:205], off
	v_lshl_add_u64 v[202:203], v[202:203], 0, s[6:7]
	s_mov_b32 m0, s52
	s_nop 0
	global_load_lds_dwordx4 v[202:203], off
	v_lshl_add_u64 v[202:203], v[206:207], 0, s[6:7]
	s_add_i32 m0, s52, 0x2000
	s_nop 0
	global_load_lds_dwordx4 v[202:203], off
	v_lshl_add_u64 v[202:203], v[212:213], 0, s[6:7]
	s_mov_b32 m0, s25
	s_nop 0
	global_load_lds_dwordx4 v[202:203], off
	v_lshl_add_u64 v[202:203], v[214:215], 0, s[6:7]
	s_mov_b32 m0, s67
	s_nop 0
	global_load_lds_dwordx4 v[202:203], off
	s_waitcnt lgkmcnt(0)
	s_barrier
	s_setprio 1
	s_waitcnt lgkmcnt(0)
	v_mfma_f32_16x16x32_bf16 v[60:63], v[138:141], v[170:173], v[60:63]
	v_mfma_f32_16x16x32_bf16 v[56:59], v[146:149], v[170:173], v[56:59]
	v_mfma_f32_16x16x32_bf16 v[44:47], v[138:141], v[178:181], v[44:47]
	v_mfma_f32_16x16x32_bf16 v[40:43], v[146:149], v[178:181], v[40:43]
	v_mfma_f32_16x16x32_bf16 v[28:31], v[138:141], v[186:189], v[28:31]
	v_mfma_f32_16x16x32_bf16 v[24:27], v[146:149], v[186:189], v[24:27]
	v_mfma_f32_16x16x32_bf16 v[12:15], v[138:141], v[194:197], v[12:15]
	v_mfma_f32_16x16x32_bf16 v[8:11], v[146:149], v[194:197], v[8:11]
	v_mfma_f32_16x16x32_bf16 v[60:63], v[142:145], v[174:177], v[60:63]
	v_mfma_f32_16x16x32_bf16 v[56:59], v[150:153], v[174:177], v[56:59]
	v_mfma_f32_16x16x32_bf16 v[44:47], v[142:145], v[182:185], v[44:47]
	v_mfma_f32_16x16x32_bf16 v[40:43], v[150:153], v[182:185], v[40:43]
	v_mfma_f32_16x16x32_bf16 v[28:31], v[142:145], v[190:193], v[28:31]
	v_mfma_f32_16x16x32_bf16 v[24:27], v[150:153], v[190:193], v[24:27]
	v_mfma_f32_16x16x32_bf16 v[12:15], v[142:145], v[198:201], v[12:15]
	v_mfma_f32_16x16x32_bf16 v[8:11], v[150:153], v[198:201], v[8:11]
	v_mfma_f32_16x16x32_bf16 v[52:55], v[154:157], v[170:173], v[52:55]
	v_mfma_f32_16x16x32_bf16 v[48:51], v[162:165], v[170:173], v[48:51]
	v_mfma_f32_16x16x32_bf16 v[36:39], v[154:157], v[178:181], v[36:39]
	v_mfma_f32_16x16x32_bf16 v[32:35], v[162:165], v[178:181], v[32:35]
	v_mfma_f32_16x16x32_bf16 v[20:23], v[154:157], v[186:189], v[20:23]
	v_mfma_f32_16x16x32_bf16 v[16:19], v[162:165], v[186:189], v[16:19]
	v_mfma_f32_16x16x32_bf16 v[4:7], v[154:157], v[194:197], v[4:7]
	v_mfma_f32_16x16x32_bf16 v[0:3], v[162:165], v[194:197], v[0:3]
	v_mfma_f32_16x16x32_bf16 v[52:55], v[158:161], v[174:177], v[52:55]
	v_mfma_f32_16x16x32_bf16 v[48:51], v[166:169], v[174:177], v[48:51]
	v_mfma_f32_16x16x32_bf16 v[36:39], v[158:161], v[182:185], v[36:39]
	v_mfma_f32_16x16x32_bf16 v[32:35], v[166:169], v[182:185], v[32:35]
	v_mfma_f32_16x16x32_bf16 v[20:23], v[158:161], v[190:193], v[20:23]
	v_mfma_f32_16x16x32_bf16 v[16:19], v[166:169], v[190:193], v[16:19]
	v_mfma_f32_16x16x32_bf16 v[4:7], v[158:161], v[198:201], v[4:7]
	v_mfma_f32_16x16x32_bf16 v[0:3], v[166:169], v[198:201], v[0:3]
	s_setprio 0
	s_waitcnt vmcnt(8)
	s_barrier
	s_add_u32 s35, s35, 0x100
	s_addc_u32 s45, s45, 0
	s_add_u32 s49, s49, 0x100
	s_addc_u32 s58, s58, 0
	s_add_u32 s59, s59, 0x100
	s_addc_u32 s70, s70, 0
	s_add_u32 s50, s50, 0x100
	s_addc_u32 s51, s51, 0
	s_cmp_ge_i32 s71, s2
	s_mov_b32 s52, s71
	s_cbranch_scc0 .LBB0_576
	s_and_b64 vcc, exec, s[14:15]
	s_cbranch_vccz .LBB0_579

; __device__ __forceinline__ int lane_id() { int l; asm volatile("v_mbcnt_lo_u32_b32 %0, -1, 0\n\tv_mbcnt_hi_u32_b32 %0, -1, %0" : "=v"(l)); return l; }
; #define G_STAGE(bufoff, gbase, voff) do { _Pragma("unroll") for (int _i = 0; _i < 2; ++_i) \
;         __builtin_amdgcn_global_load_lds((const unsigned*)((const char*)(gbase) + (voff)[_i]), (LAS unsigned*)(lds + (bufoff) + ldsw + _i * 8192), 16, 0, 0); } while (0)
; #define G_LDA(dst, b, h) do { _Pragma("unroll") for (int m = 0; m < 4; ++m) G_LD8(dst[m], lds + G_SA(b, h) + aoff + m * 2048); } while (0)
; #define G_BAR __builtin_amdgcn_s_barrier()
;     ...
;         for (int t = 0; t < nt; t += 2) {
;             const bool last = (t == nt - 2);
;             { const int tz_ = wid * 64 + lane_id();
; #pragma unroll
;               for (int i = 0; i < 2; ++i) { int R, C; stage_rc(tz_ * 16 + i * 8192, R, C); const int Rb = Epi::PERM ? ((R & ~31) + perm32(R & 31)) : R;
;                   voffA[i] = (unsigned)(R * S.multA * S.pitchA + C) * 2u; voffB[i] = (unsigned)(Rb * S.multB * S.pitchB + C) * 2u; } }
;             if constexpr (GATHER) asm volatile("" : "+v"(gc0[0]), "+v"(gc0[1]), "+v"(gc1[0]), "+v"(gc1[1]));
;             if constexpr (PREF) { if (t == nt - 4) S.prefetch(nxt, lds); }
;             const char* a11 = cur.a1 + (size_t)(t + 1) * kstep;
;             const char* a02 = last ? nxt.a0 : cur.a0 + (size_t)(t + 2) * kstep; const char* a12 = last ? nxt.a1 : cur.a1 + (size_t)(t + 2) * kstep;
;             const char* b02 = last ? nxt.b0 : cur.b0 + (size_t)(t + 2) * kstep; const char* b12 = last ? nxt.b1 : cur.b1 + (size_t)(t + 2) * kstep;
;             G_LDB(B0, 0, 0); G_LDB(B1, 0, 1); G_SCHED; G_LDA(At, 0, 0); G_STAGE(G_SA(1, 1), a11, vA1);
;             if constexpr (GATHER) { if (last) { int tz = tid; asm volatile("" : "+v"(tz));
; #pragma unroll
;                 for (int i = 0; i < 2; ++i) { int R, C; stage_rc(tz * 16 + i * 8192, R, C); gc0[i] = S.row_off(nxt, R, lds) + (unsigned)C * 2u; gc1[i] = S.row_off(nxt, 128 + R, lds) + (unsigned)C * 2u; } } }
;             G_WAIT_L(0); G_BAR; G_MMA(0, 0, At, B0); G_MMA(0, 1, At, B1); G_WAIT_V(8); G_BAR; G_SCHED;
;             G_LDA(At, 0, 1); G_STAGE(G_SB(0, 0), b02, voffB); G_STAGE(G_SB(0, 1), b12, voffB); G_STAGE(G_SA(0, 0), a02, vA0);
;             G_WAIT_L(0); G_BAR; G_MMA(1, 0, At, B0); G_MMA(1, 1, At, B1); G_WAIT_V(8); G_BAR; G_SCHED;
.LBB0_812:
	s_add_i32 s74, s54, 2
	ds_read_b128 v[138:141], v134
	ds_read_b128 v[142:145], v134 offset:1024
	ds_read_b128 v[146:149], v134 offset:2048
	ds_read_b128 v[150:153], v134 offset:3072
	ds_read_b128 v[154:157], v135
	ds_read_b128 v[158:161], v135 offset:1024
	ds_read_b128 v[162:165], v135 offset:2048
	ds_read_b128 v[166:169], v135 offset:3072
	s_add_u32 s75, s52, 0x80
	s_addc_u32 s55, s53, 0
	s_add_i32 s78, s68, s20
	s_add_i32 m0, s22, 0xc000
	s_add_i32 s77, s22, 0xe000
	s_add_i32 s79, s78, 0x2000
	s_cmp_eq_u32 s67, s54
	s_cselect_b32 s54, s46, s75
	s_cselect_b32 s57, s49, s73
	s_cselect_b32 s56, s48, s72
	s_cselect_b32 s59, s43, s61
	s_cselect_b32 s58, s42, s60
	s_cselect_b32 s55, s47, s55
	ds_read_b128 v[170:173], v136
	ds_read_b128 v[174:177], v136 offset:1024
	ds_read_b128 v[178:181], v136 offset:2048
	ds_read_b128 v[182:185], v136 offset:3072
	ds_read_b128 v[186:189], v136 offset:4096
	ds_read_b128 v[190:193], v136 offset:5120
	ds_read_b128 v[194:197], v136 offset:6144
	ds_read_b128 v[198:201], v136 offset:7168
	global_load_lds_dwordx4 v240, s[52:53]
	s_mov_b32 m0, s77
	v_mov_b32_e32 v205, v129
	global_load_lds_dwordx4 v242, s[52:53]
	s_waitcnt lgkmcnt(0)
	s_barrier
	s_setprio 1
	s_waitcnt lgkmcnt(0)
	v_mfma_f32_16x16x32_bf16 v[124:127], v[138:141], v[170:173], v[124:127]
	v_mfma_f32_16x16x32_bf16 v[120:123], v[146:149], v[170:173], v[120:123]
	v_mfma_f32_16x16x32_bf16 v[108:111], v[138:141], v[178:181], v[108:111]
	v_mfma_f32_16x16x32_bf16 v[104:107], v[146:149], v[178:181], v[104:107]
	v_mfma_f32_16x16x32_bf16 v[92:95], v[138:141], v[186:189], v[92:95]
	v_mfma_f32_16x16x32_bf16 v[88:91], v[146:149], v[186:189], v[88:91]
	v_mfma_f32_16x16x32_bf16 v[76:79], v[138:141], v[194:197], v[76:79]
	v_mfma_f32_16x16x32_bf16 v[72:75], v[146:149], v[194:197], v[72:75]
	v_mfma_f32_16x16x32_bf16 v[124:127], v[142:145], v[174:177], v[124:127]
	v_mfma_f32_16x16x32_bf16 v[120:123], v[150:153], v[174:177], v[120:123]
	v_mfma_f32_16x16x32_bf16 v[108:111], v[142:145], v[182:185], v[108:111]
	v_mfma_f32_16x16x32_bf16 v[104:107], v[150:153], v[182:185], v[104:107]
	v_mfma_f32_16x16x32_bf16 v[92:95], v[142:145], v[190:193], v[92:95]
	v_mfma_f32_16x16x32_bf16 v[88:91], v[150:153], v[190:193], v[88:91]
	v_mfma_f32_16x16x32_bf16 v[76:79], v[142:145], v[198:201], v[76:79]
	v_mfma_f32_16x16x32_bf16 v[72:75], v[150:153], v[198:201], v[72:75]
	v_mfma_f32_16x16x32_bf16 v[116:119], v[154:157], v[170:173], v[116:119]
	v_mfma_f32_16x16x32_bf16 v[112:115], v[162:165], v[170:173], v[112:115]
	v_mfma_f32_16x16x32_bf16 v[100:103], v[154:157], v[178:181], v[100:103]
	v_mfma_f32_16x16x32_bf16 v[96:99], v[162:165], v[178:181], v[96:99]
	v_mfma_f32_16x16x32_bf16 v[84:87], v[154:157], v[186:189], v[84:87]
	v_mfma_f32_16x16x32_bf16 v[80:83], v[162:165], v[186:189], v[80:83]
	v_mfma_f32_16x16x32_bf16 v[68:71], v[154:157], v[194:197], v[68:71]
	v_mfma_f32_16x16x32_bf16 v[64:67], v[162:165], v[194:197], v[64:67]
	v_mfma_f32_16x16x32_bf16 v[116:119], v[158:161], v[174:177], v[116:119]
	v_mfma_f32_16x16x32_bf16 v[112:115], v[166:169], v[174:177], v[112:115]
	v_mfma_f32_16x16x32_bf16 v[100:103], v[158:161], v[182:185], v[100:103]
	v_mfma_f32_16x16x32_bf16 v[96:99], v[166:169], v[182:185], v[96:99]
	v_mfma_f32_16x16x32_bf16 v[84:87], v[158:161], v[190:193], v[84:87]
	v_mfma_f32_16x16x32_bf16 v[80:83], v[166:169], v[190:193], v[80:83]
	v_mfma_f32_16x16x32_bf16 v[68:71], v[158:161], v[198:201], v[68:71]
	v_mfma_f32_16x16x32_bf16 v[64:67], v[166:169], v[198:201], v[64:67]
	s_setprio 0
	s_waitcnt vmcnt(8)
	s_barrier
	s_mov_b32 m0, s78
	ds_read_b128 v[170:173], v136 offset:16384
	ds_read_b128 v[174:177], v136 offset:17408
	ds_read_b128 v[178:181], v136 offset:18432
	ds_read_b128 v[182:185], v136 offset:19456
	ds_read_b128 v[186:189], v136 offset:20480
	ds_read_b128 v[190:193], v136 offset:21504
	ds_read_b128 v[194:197], v136 offset:22528
	ds_read_b128 v[198:201], v136 offset:23552
	global_load_lds_dwordx4 v244, s[58:59]
	s_mov_b32 m0, s79
	s_cselect_b32 s79, s45, s71
	s_cselect_b32 s78, s44, s62
	s_add_i32 s75, s69, s20
	global_load_lds_dwordx4 v246, s[58:59]
	s_mov_b32 m0, s75
	v_mov_b32_e32 v203, v129
	global_load_lds_dwordx4 v244, s[78:79]
	s_add_i32 m0, s75, 0x2000
	v_mov_b32_e32 v207, v129
	global_load_lds_dwordx4 v246, s[78:79]
	s_mov_b32 m0, s22
	v_lshl_add_u64 v[208:209], s[58:59], 0, v[244:245]
	global_load_lds_dwordx4 v240, s[56:57]
	s_mov_b32 m0, s23
	v_lshl_add_u64 v[210:211], s[58:59], 0, v[246:247]
	global_load_lds_dwordx4 v242, s[56:57]
	s_waitcnt lgkmcnt(0)
	v_lshl_add_u64 v[202:203], s[78:79], 0, v[244:245]
	v_lshl_add_u64 v[206:207], s[78:79], 0, v[246:247]
	v_lshl_add_u64 v[212:213], s[56:57], 0, v[240:241]
	v_lshl_add_u64 v[214:215], s[56:57], 0, v[242:243]
	s_barrier
; #define G_STAGE(bufoff, gbase, voff) do { _Pragma("unroll") for (int _i = 0; _i < 2; ++_i) \
;         __builtin_amdgcn_global_load_lds((const unsigned*)((const char*)(gbase) + (voff)[_i]), (LAS unsigned*)(lds + (bufoff) + ldsw + _i * 8192), 16, 0, 0); } while (0)
; #define G_LDA(dst, b, h) do { _Pragma("unroll") for (int m = 0; m < 4; ++m) G_LD8(dst[m], lds + G_SA(b, h) + aoff + m * 2048); } while (0)
; #define G_LDB(dst, b, h) do { _Pragma("unroll") for (int n = 0; n < 2; ++n) G_LD8(dst[n], lds + G_SB(b, h) + boff + n * 2048); } while (0)
; #define G_WAIT_V(n) asm volatile("s_waitcnt vmcnt(" #n ")" ::: "memory")
; #define G_WAIT_L(n) asm volatile("s_waitcnt lgkmcnt(" #n ")" ::: "memory")
; #define G_BAR __builtin_amdgcn_s_barrier()
; #define G_SCHED __builtin_amdgcn_sched_barrier(0)
;     ...
;             G_WAIT_L(0); G_BAR; G_MMA(1, 0, At, B0); G_MMA(1, 1, At, B1); G_WAIT_V(8); G_BAR; G_SCHED;
;             G_LDB(B0, 1, 0); G_LDB(B1, 1, 1); G_SCHED; G_LDA(At, 1, 0); G_STAGE(G_SA(0, 1), a12, vA1);
;             G_WAIT_L(0); G_BAR; G_MMA(0, 0, At, B0); G_MMA(0, 1, At, B1); G_WAIT_V(8); G_BAR; G_SCHED;
	s_setprio 1
	s_waitcnt lgkmcnt(0)
	v_mfma_f32_16x16x32_bf16 v[60:63], v[138:141], v[170:173], v[60:63]
	v_mfma_f32_16x16x32_bf16 v[56:59], v[146:149], v[170:173], v[56:59]
	v_mfma_f32_16x16x32_bf16 v[44:47], v[138:141], v[178:181], v[44:47]
	v_mfma_f32_16x16x32_bf16 v[40:43], v[146:149], v[178:181], v[40:43]
	v_mfma_f32_16x16x32_bf16 v[28:31], v[138:141], v[186:189], v[28:31]
	v_mfma_f32_16x16x32_bf16 v[24:27], v[146:149], v[186:189], v[24:27]
	v_mfma_f32_16x16x32_bf16 v[12:15], v[138:141], v[194:197], v[12:15]
	v_mfma_f32_16x16x32_bf16 v[8:11], v[146:149], v[194:197], v[8:11]
	v_mfma_f32_16x16x32_bf16 v[60:63], v[142:145], v[174:177], v[60:63]
	v_mfma_f32_16x16x32_bf16 v[56:59], v[150:153], v[174:177], v[56:59]
	v_mfma_f32_16x16x32_bf16 v[44:47], v[142:145], v[182:185], v[44:47]
	v_mfma_f32_16x16x32_bf16 v[40:43], v[150:153], v[182:185], v[40:43]
	v_mfma_f32_16x16x32_bf16 v[28:31], v[142:145], v[190:193], v[28:31]
	v_mfma_f32_16x16x32_bf16 v[24:27], v[150:153], v[190:193], v[24:27]
	v_mfma_f32_16x16x32_bf16 v[12:15], v[142:145], v[198:201], v[12:15]
	v_mfma_f32_16x16x32_bf16 v[8:11], v[150:153], v[198:201], v[8:11]
	v_mfma_f32_16x16x32_bf16 v[52:55], v[154:157], v[170:173], v[52:55]
	v_mfma_f32_16x16x32_bf16 v[48:51], v[162:165], v[170:173], v[48:51]
	v_mfma_f32_16x16x32_bf16 v[36:39], v[154:157], v[178:181], v[36:39]
	v_mfma_f32_16x16x32_bf16 v[32:35], v[162:165], v[178:181], v[32:35]
	v_mfma_f32_16x16x32_bf16 v[20:23], v[154:157], v[186:189], v[20:23]
	v_mfma_f32_16x16x32_bf16 v[16:19], v[162:165], v[186:189], v[16:19]
	v_mfma_f32_16x16x32_bf16 v[4:7], v[154:157], v[194:197], v[4:7]
	v_mfma_f32_16x16x32_bf16 v[0:3], v[162:165], v[194:197], v[0:3]
	v_mfma_f32_16x16x32_bf16 v[52:55], v[158:161], v[174:177], v[52:55]
	v_mfma_f32_16x16x32_bf16 v[48:51], v[166:169], v[174:177], v[48:51]
	v_mfma_f32_16x16x32_bf16 v[36:39], v[158:161], v[182:185], v[36:39]
	v_mfma_f32_16x16x32_bf16 v[32:35], v[166:169], v[182:185], v[32:35]
	v_mfma_f32_16x16x32_bf16 v[20:23], v[158:161], v[190:193], v[20:23]
	v_mfma_f32_16x16x32_bf16 v[16:19], v[166:169], v[190:193], v[16:19]
	v_mfma_f32_16x16x32_bf16 v[4:7], v[158:161], v[198:201], v[4:7]
	v_mfma_f32_16x16x32_bf16 v[0:3], v[166:169], v[198:201], v[0:3]
	s_setprio 0
	s_waitcnt vmcnt(8)
	s_barrier
	s_add_i32 s56, 0, 0x18000
	v_add_u32_e32 v137, s56, v133
	s_add_i32 s57, 0, 0x1c000
	ds_read_b128 v[138:141], v137
	ds_read_b128 v[142:145], v137 offset:1024
	ds_read_b128 v[146:149], v137 offset:2048
	ds_read_b128 v[150:153], v137 offset:3072
	v_add_u32_e32 v137, s57, v133
	ds_read_b128 v[154:157], v137
	ds_read_b128 v[158:161], v137 offset:1024
	ds_read_b128 v[162:165], v137 offset:2048
	ds_read_b128 v[166:169], v137 offset:3072
	s_mov_b32 m0, s24
	ds_read_b128 v[170:173], v136 offset:32768
	ds_read_b128 v[174:177], v136 offset:33792
	ds_read_b128 v[178:181], v136 offset:34816
	ds_read_b128 v[182:185], v136 offset:35840
	ds_read_b128 v[186:189], v136 offset:36864
	ds_read_b128 v[190:193], v136 offset:37888
	ds_read_b128 v[194:197], v136 offset:38912
	ds_read_b128 v[198:201], v136 offset:39936
	global_load_lds_dwordx4 v240, s[54:55]
	s_mov_b32 m0, s25
	s_nop 0
	global_load_lds_dwordx4 v242, s[54:55]
	s_waitcnt lgkmcnt(0)
	s_barrier
	s_setprio 1
	s_waitcnt lgkmcnt(0)
	v_mfma_f32_16x16x32_bf16 v[124:127], v[138:141], v[170:173], v[124:127]
	v_mfma_f32_16x16x32_bf16 v[120:123], v[146:149], v[170:173], v[120:123]
	v_mfma_f32_16x16x32_bf16 v[108:111], v[138:141], v[178:181], v[108:111]
	v_mfma_f32_16x16x32_bf16 v[104:107], v[146:149], v[178:181], v[104:107]
	v_mfma_f32_16x16x32_bf16 v[92:95], v[138:141], v[186:189], v[92:95]
	v_mfma_f32_16x16x32_bf16 v[88:91], v[146:149], v[186:189], v[88:91]
	v_mfma_f32_16x16x32_bf16 v[76:79], v[138:141], v[194:197], v[76:79]
	v_mfma_f32_16x16x32_bf16 v[72:75], v[146:149], v[194:197], v[72:75]
	v_mfma_f32_16x16x32_bf16 v[124:127], v[142:145], v[174:177], v[124:127]
	v_mfma_f32_16x16x32_bf16 v[120:123], v[150:153], v[174:177], v[120:123]
	v_mfma_f32_16x16x32_bf16 v[108:111], v[142:145], v[182:185], v[108:111]
	v_mfma_f32_16x16x32_bf16 v[104:107], v[150:153], v[182:185], v[104:107]
	v_mfma_f32_16x16x32_bf16 v[92:95], v[142:145], v[190:193], v[92:95]
	v_mfma_f32_16x16x32_bf16 v[88:91], v[150:153], v[190:193], v[88:91]
	v_mfma_f32_16x16x32_bf16 v[76:79], v[142:145], v[198:201], v[76:79]
	v_mfma_f32_16x16x32_bf16 v[72:75], v[150:153], v[198:201], v[72:75]
	v_mfma_f32_16x16x32_bf16 v[116:119], v[154:157], v[170:173], v[116:119]
	v_mfma_f32_16x16x32_bf16 v[112:115], v[162:165], v[170:173], v[112:115]
	v_mfma_f32_16x16x32_bf16 v[100:103], v[154:157], v[178:181], v[100:103]
	v_mfma_f32_16x16x32_bf16 v[96:99], v[162:165], v[178:181], v[96:99]
	v_mfma_f32_16x16x32_bf16 v[84:87], v[154:157], v[186:189], v[84:87]
	v_mfma_f32_16x16x32_bf16 v[80:83], v[162:165], v[186:189], v[80:83]
	v_mfma_f32_16x16x32_bf16 v[68:71], v[154:157], v[194:197], v[68:71]
	v_mfma_f32_16x16x32_bf16 v[64:67], v[162:165], v[194:197], v[64:67]
	v_mfma_f32_16x16x32_bf16 v[116:119], v[158:161], v[174:177], v[116:119]
	v_mfma_f32_16x16x32_bf16 v[112:115], v[166:169], v[174:177], v[112:115]
	v_mfma_f32_16x16x32_bf16 v[100:103], v[158:161], v[182:185], v[100:103]
	v_mfma_f32_16x16x32_bf16 v[96:99], v[166:169], v[182:185], v[96:99]
	v_mfma_f32_16x16x32_bf16 v[84:87], v[158:161], v[190:193], v[84:87]
	v_mfma_f32_16x16x32_bf16 v[80:83], v[166:169], v[190:193], v[80:83]
	v_mfma_f32_16x16x32_bf16 v[68:71], v[158:161], v[198:201], v[68:71]
	v_mfma_f32_16x16x32_bf16 v[64:67], v[166:169], v[198:201], v[64:67]
	s_setprio 0
	s_waitcnt vmcnt(8)
	s_barrier
; #define G_STAGE(bufoff, gbase, voff) do { _Pragma("unroll") for (int _i = 0; _i < 2; ++_i) \
;         __builtin_amdgcn_global_load_lds((const unsigned*)((const char*)(gbase) + (voff)[_i]), (LAS unsigned*)(lds + (bufoff) + ldsw + _i * 8192), 16, 0, 0); } while (0)
; #define G_LDA(dst, b, h) do { _Pragma("unroll") for (int m = 0; m < 4; ++m) G_LD8(dst[m], lds + G_SA(b, h) + aoff + m * 2048); } while (0)
; #define G_WAIT_V(n) asm volatile("s_waitcnt vmcnt(" #n ")" ::: "memory")
; #define G_WAIT_L(n) asm volatile("s_waitcnt lgkmcnt(" #n ")" ::: "memory")
; #define G_BAR __builtin_amdgcn_s_barrier()
; #define G_SCHED __builtin_amdgcn_sched_barrier(0)
;     ...
;             G_LDA(At, 1, 1); G_STAGE(G_SB(1, 0), b02 + kstep, voffB); G_STAGE(G_SB(1, 1), b12 + kstep, voffB); G_STAGE(G_SA(1, 0), a02 + kstep, vA0);
;             G_WAIT_L(0); G_BAR; G_MMA(1, 0, At, B0); G_MMA(1, 1, At, B1); G_WAIT_V(8); G_BAR; G_SCHED;
;         }
	s_add_i32 s54, s56, s20
	v_lshl_add_u64 v[204:205], v[208:209], 0, s[36:37]
	s_mov_b32 m0, s54
	ds_read_b128 v[170:173], v136 offset:49152
	ds_read_b128 v[174:177], v136 offset:50176
	ds_read_b128 v[178:181], v136 offset:51200
	ds_read_b128 v[182:185], v136 offset:52224
	ds_read_b128 v[186:189], v136 offset:53248
	ds_read_b128 v[190:193], v136 offset:54272
	ds_read_b128 v[194:197], v136 offset:55296
	ds_read_b128 v[198:201], v136 offset:56320
	global_load_lds_dwordx4 v[204:205], off
	v_lshl_add_u64 v[204:205], v[210:211], 0, s[36:37]
	s_add_i32 m0, s54, 0x2000
	s_add_i32 s54, s57, s20
	global_load_lds_dwordx4 v[204:205], off
	v_lshl_add_u64 v[202:203], v[202:203], 0, s[36:37]
	s_mov_b32 m0, s54
	s_nop 0
	global_load_lds_dwordx4 v[202:203], off
	v_lshl_add_u64 v[202:203], v[206:207], 0, s[36:37]
	s_add_i32 m0, s54, 0x2000
	s_nop 0
	global_load_lds_dwordx4 v[202:203], off
	v_lshl_add_u64 v[202:203], v[212:213], 0, s[36:37]
	s_mov_b32 m0, s65
	s_nop 0
	global_load_lds_dwordx4 v[202:203], off
	v_lshl_add_u64 v[202:203], v[214:215], 0, s[36:37]
	s_mov_b32 m0, s66
	s_nop 0
	global_load_lds_dwordx4 v[202:203], off
	s_waitcnt lgkmcnt(0)
	s_barrier
	s_setprio 1
	s_waitcnt lgkmcnt(0)
	v_mfma_f32_16x16x32_bf16 v[60:63], v[138:141], v[170:173], v[60:63]
	v_mfma_f32_16x16x32_bf16 v[56:59], v[146:149], v[170:173], v[56:59]
	v_mfma_f32_16x16x32_bf16 v[44:47], v[138:141], v[178:181], v[44:47]
	v_mfma_f32_16x16x32_bf16 v[40:43], v[146:149], v[178:181], v[40:43]
	v_mfma_f32_16x16x32_bf16 v[28:31], v[138:141], v[186:189], v[28:31]
	v_mfma_f32_16x16x32_bf16 v[24:27], v[146:149], v[186:189], v[24:27]
	v_mfma_f32_16x16x32_bf16 v[12:15], v[138:141], v[194:197], v[12:15]
	v_mfma_f32_16x16x32_bf16 v[8:11], v[146:149], v[194:197], v[8:11]
	v_mfma_f32_16x16x32_bf16 v[60:63], v[142:145], v[174:177], v[60:63]
	v_mfma_f32_16x16x32_bf16 v[56:59], v[150:153], v[174:177], v[56:59]
	v_mfma_f32_16x16x32_bf16 v[44:47], v[142:145], v[182:185], v[44:47]
	v_mfma_f32_16x16x32_bf16 v[40:43], v[150:153], v[182:185], v[40:43]
	v_mfma_f32_16x16x32_bf16 v[28:31], v[142:145], v[190:193], v[28:31]
	v_mfma_f32_16x16x32_bf16 v[24:27], v[150:153], v[190:193], v[24:27]
	v_mfma_f32_16x16x32_bf16 v[12:15], v[142:145], v[198:201], v[12:15]
	v_mfma_f32_16x16x32_bf16 v[8:11], v[150:153], v[198:201], v[8:11]
	v_mfma_f32_16x16x32_bf16 v[52:55], v[154:157], v[170:173], v[52:55]
	v_mfma_f32_16x16x32_bf16 v[48:51], v[162:165], v[170:173], v[48:51]
	v_mfma_f32_16x16x32_bf16 v[36:39], v[154:157], v[178:181], v[36:39]
	v_mfma_f32_16x16x32_bf16 v[32:35], v[162:165], v[178:181], v[32:35]
	v_mfma_f32_16x16x32_bf16 v[20:23], v[154:157], v[186:189], v[20:23]
	v_mfma_f32_16x16x32_bf16 v[16:19], v[162:165], v[186:189], v[16:19]
	v_mfma_f32_16x16x32_bf16 v[4:7], v[154:157], v[194:197], v[4:7]
	v_mfma_f32_16x16x32_bf16 v[0:3], v[162:165], v[194:197], v[0:3]
	v_mfma_f32_16x16x32_bf16 v[52:55], v[158:161], v[174:177], v[52:55]
	v_mfma_f32_16x16x32_bf16 v[48:51], v[166:169], v[174:177], v[48:51]
	v_mfma_f32_16x16x32_bf16 v[36:39], v[158:161], v[182:185], v[36:39]
	v_mfma_f32_16x16x32_bf16 v[32:35], v[166:169], v[182:185], v[32:35]
	v_mfma_f32_16x16x32_bf16 v[20:23], v[158:161], v[190:193], v[20:23]
	v_mfma_f32_16x16x32_bf16 v[16:19], v[166:169], v[190:193], v[16:19]
	v_mfma_f32_16x16x32_bf16 v[4:7], v[158:161], v[198:201], v[4:7]
	v_mfma_f32_16x16x32_bf16 v[0:3], v[166:169], v[198:201], v[0:3]
	s_setprio 0
	s_waitcnt vmcnt(8)
	s_barrier
	s_add_u32 s60, s60, 0x100
	s_addc_u32 s61, s61, 0
	s_add_u32 s62, s62, 0x100
	s_addc_u32 s71, s71, 0
	s_add_u32 s72, s72, 0x100
	s_addc_u32 s73, s73, 0
	s_add_u32 s52, s52, 0x100
	s_addc_u32 s53, s53, 0
	s_cmp_ge_i32 s74, s0
	s_mov_b32 s54, s74
	s_cbranch_scc0 .LBB0_812
	v_readlane_b32 s78, v255, 11
	v_readlane_b32 s79, v255, 13
	s_and_b64 vcc, exec, s[40:41]
	s_cbranch_vccz .LBB0_815

; #define G_STAGE(bufoff, gbase, voff) do { _Pragma("unroll") for (int _i = 0; _i < 2; ++_i) \
;         __builtin_amdgcn_global_load_lds((const unsigned*)((const char*)(gbase) + (voff)[_i]), (LAS unsigned*)(lds + (bufoff) + ldsw + _i * 8192), 16, 0, 0); } while (0)
; #define G_LDA(dst, b, h) do { _Pragma("unroll") for (int m = 0; m < 4; ++m) G_LD8(dst[m], lds + G_SA(b, h) + aoff + m * 2048); } while (0)
; #define G_LDB(dst, b, h) do { _Pragma("unroll") for (int n = 0; n < 2; ++n) G_LD8(dst[n], lds + G_SB(b, h) + boff + n * 2048); } while (0)
; #define G_WAIT_V(n) asm volatile("s_waitcnt vmcnt(" #n ")" ::: "memory")
; #define G_WAIT_L(n) asm volatile("s_waitcnt lgkmcnt(" #n ")" ::: "memory")
; #define G_BAR __builtin_amdgcn_s_barrier()
; #define G_SCHED __builtin_amdgcn_sched_barrier(0)
;     __device__ __forceinline__ unsigned row_off(const Unit& u, int r, LAS unsigned char* lds) const { return (unsigned)((const LAS int*)(lds + LDS_STAGE + u.q * 4096))[r] * (unsigned)rowbytes; }
;     ...
;             const char* a11 = cur.a1 + (size_t)(t + 1) * kstep;
;             const char* a02 = last ? nxt.a0 : cur.a0 + (size_t)(t + 2) * kstep; const char* a12 = last ? nxt.a1 : cur.a1 + (size_t)(t + 2) * kstep;
;             const char* b02 = last ? nxt.b0 : cur.b0 + (size_t)(t + 2) * kstep; const char* b12 = last ? nxt.b1 : cur.b1 + (size_t)(t + 2) * kstep;
;             G_LDB(B0, 0, 0); G_LDB(B1, 0, 1); G_SCHED; G_LDA(At, 0, 0); G_STAGE(G_SA(1, 1), a11, vA1);
;             if constexpr (GATHER) { if (last) { int tz = tid; asm volatile("" : "+v"(tz));
; #pragma unroll
;                 for (int i = 0; i < 2; ++i) { int R, C; stage_rc(tz * 16 + i * 8192, R, C); gc0[i] = S.row_off(nxt, R, lds) + (unsigned)C * 2u; gc1[i] = S.row_off(nxt, 128 + R, lds) + (unsigned)C * 2u; } } }
;             G_WAIT_L(0); G_BAR; G_MMA(0, 0, At, B0); G_MMA(0, 1, At, B1); G_WAIT_V(8); G_BAR; G_SCHED;
;             G_LDA(At, 0, 1); G_STAGE(G_SB(0, 0), b02, voffB); G_STAGE(G_SB(0, 1), b12, voffB); G_STAGE(G_SA(0, 0), a02, vA0);
;             G_WAIT_L(0); G_BAR; G_MMA(1, 0, At, B0); G_MMA(1, 1, At, B1); G_WAIT_V(8); G_BAR; G_SCHED;
;             G_LDB(B0, 1, 0); G_LDB(B1, 1, 1); G_SCHED; G_LDA(At, 1, 0); G_STAGE(G_SA(0, 1), a12, vA1);
;             G_WAIT_L(0); G_BAR; G_MMA(0, 0, At, B0); G_MMA(0, 1, At, B1); G_WAIT_V(8); G_BAR; G_SCHED;
.LBB0_1023:
	s_add_i32 s78, s54, 2
	ds_read_b128 v[72:75], v70
	ds_read_b128 v[76:79], v70 offset:1024
	ds_read_b128 v[80:83], v70 offset:2048
	ds_read_b128 v[84:87], v70 offset:3072
	s_add_u32 s79, s52, 0x80
	s_addc_u32 s55, s53, 0
	s_add_i32 s81, s73, s20
	s_add_i32 m0, s23, 0xc000
	s_add_i32 s80, s23, 0xe000
	s_add_i32 s82, s81, 0x2000
	s_cmp_eq_u32 s72, s54
	s_cselect_b32 s54, s44, s79
	s_cselect_b32 s57, s43, s77
	s_cselect_b32 s56, s42, s75
	s_cselect_b32 s59, s49, s61
	s_cselect_b32 s58, s48, s60
	s_cselect_b32 s55, s45, s55
	ds_read_b128 v[88:91], v71
	ds_read_b128 v[92:95], v71 offset:1024
	ds_read_b128 v[96:99], v71 offset:2048
	ds_read_b128 v[100:103], v71 offset:3072
	ds_read_b128 v[104:107], v71 offset:4096
	ds_read_b128 v[108:111], v71 offset:5120
	ds_read_b128 v[112:115], v71 offset:6144
	ds_read_b128 v[116:119], v71 offset:7168
	global_load_lds_dwordx4 v240, s[52:53]
	s_mov_b32 m0, s80
	v_mov_b32_e32 v123, v65
	global_load_lds_dwordx4 v242, s[52:53]
	s_waitcnt lgkmcnt(0)
	s_barrier
	s_setprio 1
	s_waitcnt lgkmcnt(0)
	v_mfma_f32_16x16x32_bf16 v[60:63], v[72:75], v[88:91], v[60:63]
	v_mfma_f32_16x16x32_bf16 v[56:59], v[80:83], v[88:91], v[56:59]
	v_mfma_f32_16x16x32_bf16 v[52:55], v[72:75], v[96:99], v[52:55]
	v_mfma_f32_16x16x32_bf16 v[48:51], v[80:83], v[96:99], v[48:51]
	v_mfma_f32_16x16x32_bf16 v[44:47], v[72:75], v[104:107], v[44:47]
	v_mfma_f32_16x16x32_bf16 v[40:43], v[80:83], v[104:107], v[40:43]
	v_mfma_f32_16x16x32_bf16 v[36:39], v[72:75], v[112:115], v[36:39]
	v_mfma_f32_16x16x32_bf16 v[32:35], v[80:83], v[112:115], v[32:35]
	v_mfma_f32_16x16x32_bf16 v[60:63], v[76:79], v[92:95], v[60:63]
	v_mfma_f32_16x16x32_bf16 v[56:59], v[84:87], v[92:95], v[56:59]
	v_mfma_f32_16x16x32_bf16 v[52:55], v[76:79], v[100:103], v[52:55]
	v_mfma_f32_16x16x32_bf16 v[48:51], v[84:87], v[100:103], v[48:51]
	v_mfma_f32_16x16x32_bf16 v[44:47], v[76:79], v[108:111], v[44:47]
	v_mfma_f32_16x16x32_bf16 v[40:43], v[84:87], v[108:111], v[40:43]
	v_mfma_f32_16x16x32_bf16 v[36:39], v[76:79], v[116:119], v[36:39]
	v_mfma_f32_16x16x32_bf16 v[32:35], v[84:87], v[116:119], v[32:35]
	s_setprio 0
	s_waitcnt vmcnt(8)
	s_barrier
	s_mov_b32 m0, s81
	ds_read_b128 v[88:91], v71 offset:16384
	ds_read_b128 v[92:95], v71 offset:17408
	ds_read_b128 v[96:99], v71 offset:18432
	ds_read_b128 v[100:103], v71 offset:19456
	ds_read_b128 v[104:107], v71 offset:20480
	ds_read_b128 v[108:111], v71 offset:21504
	ds_read_b128 v[112:115], v71 offset:22528
	ds_read_b128 v[116:119], v71 offset:23552
	global_load_lds_dwordx4 v244, s[58:59]
	s_mov_b32 m0, s82
	s_cselect_b32 s81, s47, s74
	global_load_lds_dwordx4 v246, s[58:59]
	s_cselect_b32 s80, s46, s62
	s_mov_b32 m0, s24
	v_mov_b32_e32 v121, v65
	global_load_lds_dwordx4 v244, s[80:81]
	s_mov_b32 m0, s25
	v_mov_b32_e32 v125, v65
	global_load_lds_dwordx4 v246, s[80:81]
	s_mov_b32 m0, s23
	v_lshl_add_u64 v[126:127], s[58:59], 0, v[244:245]
	global_load_lds_dwordx4 v240, s[56:57]
	s_mov_b32 m0, s27
	v_lshl_add_u64 v[128:129], s[58:59], 0, v[246:247]
	global_load_lds_dwordx4 v242, s[56:57]
	s_waitcnt lgkmcnt(0)
	v_lshl_add_u64 v[120:121], s[80:81], 0, v[244:245]
	v_lshl_add_u64 v[124:125], s[80:81], 0, v[246:247]
	v_lshl_add_u64 v[130:131], s[56:57], 0, v[240:241]
	v_lshl_add_u64 v[132:133], s[56:57], 0, v[242:243]
	s_barrier
	s_setprio 1
	s_waitcnt lgkmcnt(0)
	v_mfma_f32_16x16x32_bf16 v[28:31], v[72:75], v[88:91], v[28:31]
	v_mfma_f32_16x16x32_bf16 v[24:27], v[80:83], v[88:91], v[24:27]
	v_mfma_f32_16x16x32_bf16 v[20:23], v[72:75], v[96:99], v[20:23]
	v_mfma_f32_16x16x32_bf16 v[16:19], v[80:83], v[96:99], v[16:19]
	v_mfma_f32_16x16x32_bf16 v[12:15], v[72:75], v[104:107], v[12:15]
	v_mfma_f32_16x16x32_bf16 v[8:11], v[80:83], v[104:107], v[8:11]
	v_mfma_f32_16x16x32_bf16 v[4:7], v[72:75], v[112:115], v[4:7]
	v_mfma_f32_16x16x32_bf16 v[0:3], v[80:83], v[112:115], v[0:3]
	v_mfma_f32_16x16x32_bf16 v[28:31], v[76:79], v[92:95], v[28:31]
	v_mfma_f32_16x16x32_bf16 v[24:27], v[84:87], v[92:95], v[24:27]
	v_mfma_f32_16x16x32_bf16 v[20:23], v[76:79], v[100:103], v[20:23]
	v_mfma_f32_16x16x32_bf16 v[16:19], v[84:87], v[100:103], v[16:19]
	v_mfma_f32_16x16x32_bf16 v[12:15], v[76:79], v[108:111], v[12:15]
	v_mfma_f32_16x16x32_bf16 v[8:11], v[84:87], v[108:111], v[8:11]
	v_mfma_f32_16x16x32_bf16 v[4:7], v[76:79], v[116:119], v[4:7]
	v_mfma_f32_16x16x32_bf16 v[0:3], v[84:87], v[116:119], v[0:3]
	s_setprio 0
	s_waitcnt vmcnt(8)
	s_barrier
	s_add_i32 s56, 0, 0x18000
	v_add_u32_e32 v84, s56, v69
	ds_read_b128 v[72:75], v84
	ds_read_b128 v[76:79], v84 offset:1024
	ds_read_b128 v[80:83], v84 offset:2048
	ds_read_b128 v[84:87], v84 offset:3072
	s_mov_b32 m0, s33
	ds_read_b128 v[88:91], v71 offset:32768
	ds_read_b128 v[92:95], v71 offset:33792
	ds_read_b128 v[96:99], v71 offset:34816
	ds_read_b128 v[100:103], v71 offset:35840
	ds_read_b128 v[104:107], v71 offset:36864
	ds_read_b128 v[108:111], v71 offset:37888
	ds_read_b128 v[112:115], v71 offset:38912
	ds_read_b128 v[116:119], v71 offset:39936
	global_load_lds_dwordx4 v240, s[54:55]
	s_mov_b32 m0, s41
	s_nop 0
	global_load_lds_dwordx4 v242, s[54:55]
	s_waitcnt lgkmcnt(0)
	s_barrier
; #define GAS __attribute__((address_space(1)))
; __device__ __forceinline__ v4u pack8(const f32x4 a, const f32x4 b) { v4u w; w.x = cvt_pk_bf16(a[0], a[1]); w.y = cvt_pk_bf16(a[2], a[3]); w.z = cvt_pk_bf16(b[0], b[1]); w.w = cvt_pk_bf16(b[2], b[3]); return w; }
; #define G_STAGE(bufoff, gbase, voff) do { _Pragma("unroll") for (int _i = 0; _i < 2; ++_i) \
;         __builtin_amdgcn_global_load_lds((const unsigned*)((const char*)(gbase) + (voff)[_i]), (LAS unsigned*)(lds + (bufoff) + ldsw + _i * 8192), 16, 0, 0); } while (0)
; #define G_LDA(dst, b, h) do { _Pragma("unroll") for (int m = 0; m < 4; ++m) G_LD8(dst[m], lds + G_SA(b, h) + aoff + m * 2048); } while (0)
; #define G_WAIT_V(n) asm volatile("s_waitcnt vmcnt(" #n ")" ::: "memory")
; #define G_WAIT_L(n) asm volatile("s_waitcnt lgkmcnt(" #n ")" ::: "memory")
; #define G_BAR __builtin_amdgcn_s_barrier()
; #define G_SCHED __builtin_amdgcn_sched_barrier(0)
; #define EPI_LOOP_AM for (int ai = 0; ai < 2; ++ai) _Pragma("unroll") for (int m = 0; m < 4; ++m)
;     ...
;             G_WAIT_L(0); G_BAR; G_MMA(0, 0, At, B0); G_MMA(0, 1, At, B1); G_WAIT_V(8); G_BAR; G_SCHED;
;             G_LDA(At, 1, 1); G_STAGE(G_SB(1, 0), b02 + kstep, voffB); G_STAGE(G_SB(1, 1), b12 + kstep, voffB); G_STAGE(G_SA(1, 0), a02 + kstep, vA0);
;             G_WAIT_L(0); G_BAR; G_MMA(1, 0, At, B0); G_MMA(1, 1, At, B1); G_WAIT_V(8); G_BAR; G_SCHED;
;         }
;     __device__ __forceinline__ void operator()(Acc& acc, const Unit& u, LAS unsigned char*, int wr, int wc, int fr, int fq) const {
;         const int l0 = wc * 32 + 8 * fq; const float norm = 6.9053396600248786e-4f;
; #pragma unroll
;         EPI_LOOP_AM { const int R = u.p0 * 256 + 128 * ai + 64 * wr + 16 * m + fr, k = R >> 3, g = R & 7;
;             *(GAS v4u*)(y + (size_t)k * D + g * 128 + l0) = pack8(acc[ai][0][m][0] * norm, acc[ai][0][m][1] * norm); }
	s_setprio 1
	s_waitcnt lgkmcnt(0)
	v_mfma_f32_16x16x32_bf16 v[60:63], v[72:75], v[88:91], v[60:63]
	v_mfma_f32_16x16x32_bf16 v[56:59], v[80:83], v[88:91], v[56:59]
	v_mfma_f32_16x16x32_bf16 v[52:55], v[72:75], v[96:99], v[52:55]
	v_mfma_f32_16x16x32_bf16 v[48:51], v[80:83], v[96:99], v[48:51]
	v_mfma_f32_16x16x32_bf16 v[44:47], v[72:75], v[104:107], v[44:47]
	v_mfma_f32_16x16x32_bf16 v[40:43], v[80:83], v[104:107], v[40:43]
	v_mfma_f32_16x16x32_bf16 v[36:39], v[72:75], v[112:115], v[36:39]
	v_mfma_f32_16x16x32_bf16 v[32:35], v[80:83], v[112:115], v[32:35]
	v_mfma_f32_16x16x32_bf16 v[60:63], v[76:79], v[92:95], v[60:63]
	v_mfma_f32_16x16x32_bf16 v[56:59], v[84:87], v[92:95], v[56:59]
	v_mfma_f32_16x16x32_bf16 v[52:55], v[76:79], v[100:103], v[52:55]
	v_mfma_f32_16x16x32_bf16 v[48:51], v[84:87], v[100:103], v[48:51]
	v_mfma_f32_16x16x32_bf16 v[44:47], v[76:79], v[108:111], v[44:47]
	v_mfma_f32_16x16x32_bf16 v[40:43], v[84:87], v[108:111], v[40:43]
	v_mfma_f32_16x16x32_bf16 v[36:39], v[76:79], v[116:119], v[36:39]
	v_mfma_f32_16x16x32_bf16 v[32:35], v[84:87], v[116:119], v[32:35]
	s_setprio 0
	s_waitcnt vmcnt(8)
	s_barrier
	s_add_i32 s54, s56, s20
	v_lshl_add_u64 v[122:123], v[126:127], 0, s[36:37]
	s_mov_b32 m0, s54
	ds_read_b128 v[88:91], v71 offset:49152
	ds_read_b128 v[92:95], v71 offset:50176
	ds_read_b128 v[96:99], v71 offset:51200
	ds_read_b128 v[100:103], v71 offset:52224
	ds_read_b128 v[104:107], v71 offset:53248
	ds_read_b128 v[108:111], v71 offset:54272
	ds_read_b128 v[112:115], v71 offset:55296
	ds_read_b128 v[116:119], v71 offset:56320
	global_load_lds_dwordx4 v[122:123], off
	v_lshl_add_u64 v[122:123], v[128:129], 0, s[36:37]
	s_add_i32 m0, s54, 0x2000
	v_lshl_add_u64 v[120:121], v[120:121], 0, s[36:37]
	global_load_lds_dwordx4 v[122:123], off
	s_mov_b32 m0, s69
	s_nop 0
	global_load_lds_dwordx4 v[120:121], off
	v_lshl_add_u64 v[120:121], v[124:125], 0, s[36:37]
	s_mov_b32 m0, s71
	s_nop 0
	global_load_lds_dwordx4 v[120:121], off
	v_lshl_add_u64 v[120:121], v[130:131], 0, s[36:37]
	s_mov_b32 m0, s66
	s_nop 0
	global_load_lds_dwordx4 v[120:121], off
	v_lshl_add_u64 v[120:121], v[132:133], 0, s[36:37]
	s_mov_b32 m0, s67
	s_nop 0
	global_load_lds_dwordx4 v[120:121], off
	s_waitcnt lgkmcnt(0)
	s_barrier
	s_setprio 1
	s_waitcnt lgkmcnt(0)
	v_mfma_f32_16x16x32_bf16 v[28:31], v[72:75], v[88:91], v[28:31]
	v_mfma_f32_16x16x32_bf16 v[24:27], v[80:83], v[88:91], v[24:27]
	v_mfma_f32_16x16x32_bf16 v[20:23], v[72:75], v[96:99], v[20:23]
	v_mfma_f32_16x16x32_bf16 v[16:19], v[80:83], v[96:99], v[16:19]
	v_mfma_f32_16x16x32_bf16 v[12:15], v[72:75], v[104:107], v[12:15]
	v_mfma_f32_16x16x32_bf16 v[8:11], v[80:83], v[104:107], v[8:11]
	v_mfma_f32_16x16x32_bf16 v[4:7], v[72:75], v[112:115], v[4:7]
	v_mfma_f32_16x16x32_bf16 v[0:3], v[80:83], v[112:115], v[0:3]
	v_mfma_f32_16x16x32_bf16 v[28:31], v[76:79], v[92:95], v[28:31]
	v_mfma_f32_16x16x32_bf16 v[24:27], v[84:87], v[92:95], v[24:27]
	v_mfma_f32_16x16x32_bf16 v[20:23], v[76:79], v[100:103], v[20:23]
	v_mfma_f32_16x16x32_bf16 v[16:19], v[84:87], v[100:103], v[16:19]
	v_mfma_f32_16x16x32_bf16 v[12:15], v[76:79], v[108:111], v[12:15]
	v_mfma_f32_16x16x32_bf16 v[8:11], v[84:87], v[108:111], v[8:11]
	v_mfma_f32_16x16x32_bf16 v[4:7], v[76:79], v[116:119], v[4:7]
	v_mfma_f32_16x16x32_bf16 v[0:3], v[84:87], v[116:119], v[0:3]
	s_setprio 0
	s_waitcnt vmcnt(8)
	s_barrier
	s_add_u32 s60, s60, 0x100
	s_addc_u32 s61, s61, 0
	s_add_u32 s62, s62, 0x100
	s_addc_u32 s74, s74, 0
	s_add_u32 s75, s75, 0x100
	s_addc_u32 s77, s77, 0
	s_add_u32 s52, s52, 0x100
	s_addc_u32 s53, s53, 0
	s_cmp_ge_i32 s78, s0
	s_mov_b32 s54, s78
	s_cbranch_scc0 .LBB0_1023
	v_pk_mul_f32 v[62:63], v[62:63], s[40:41] op_sel_hi:[1,0]
	v_pk_mul_f32 v[60:61], v[60:61], s[40:41] op_sel_hi:[1,0]
	v_pk_mul_f32 v[58:59], v[58:59], s[40:41] op_sel_hi:[1,0]
	v_pk_mul_f32 v[56:57], v[56:57], s[40:41] op_sel_hi:[1,0]
	v_pk_mul_f32 v[54:55], v[54:55], s[40:41] op_sel_hi:[1,0]
	v_pk_mul_f32 v[52:53], v[52:53], s[40:41] op_sel_hi:[1,0]
	v_pk_mul_f32 v[50:51], v[50:51], s[40:41] op_sel_hi:[1,0]
	v_pk_mul_f32 v[48:49], v[48:49], s[40:41] op_sel_hi:[1,0]
	v_pk_mul_f32 v[46:47], v[46:47], s[40:41] op_sel_hi:[1,0]
	v_pk_mul_f32 v[44:45], v[44:45], s[40:41] op_sel_hi:[1,0]
	v_pk_mul_f32 v[42:43], v[42:43], s[40:41] op_sel_hi:[1,0]
	v_pk_mul_f32 v[40:41], v[40:41], s[40:41] op_sel_hi:[1,0]
	v_pk_mul_f32 v[38:39], v[38:39], s[40:41] op_sel_hi:[1,0]
	v_pk_mul_f32 v[36:37], v[36:37], s[40:41] op_sel_hi:[1,0]
	v_pk_mul_f32 v[34:35], v[34:35], s[40:41] op_sel_hi:[1,0]
	v_pk_mul_f32 v[32:33], v[32:33], s[40:41] op_sel_hi:[1,0]
	v_pk_mul_f32 v[30:31], v[30:31], s[40:41] op_sel_hi:[1,0]
	v_pk_mul_f32 v[28:29], v[28:29], s[40:41] op_sel_hi:[1,0]
	v_pk_mul_f32 v[26:27], v[26:27], s[40:41] op_sel_hi:[1,0]
	v_pk_mul_f32 v[24:25], v[24:25], s[40:41] op_sel_hi:[1,0]
	v_pk_mul_f32 v[22:23], v[22:23], s[40:41] op_sel_hi:[1,0]
	v_pk_mul_f32 v[20:21], v[20:21], s[40:41] op_sel_hi:[1,0]
	v_pk_mul_f32 v[18:19], v[18:19], s[40:41] op_sel_hi:[1,0]
	v_pk_mul_f32 v[16:17], v[16:17], s[40:41] op_sel_hi:[1,0]
	v_pk_mul_f32 v[14:15], v[14:15], s[40:41] op_sel_hi:[1,0]
	v_pk_mul_f32 v[12:13], v[12:13], s[40:41] op_sel_hi:[1,0]
	v_pk_mul_f32 v[10:11], v[10:11], s[40:41] op_sel_hi:[1,0]
	v_pk_mul_f32 v[8:9], v[8:9], s[40:41] op_sel_hi:[1,0]
	v_pk_mul_f32 v[6:7], v[6:7], s[40:41] op_sel_hi:[1,0]
	v_pk_mul_f32 v[4:5], v[4:5], s[40:41] op_sel_hi:[1,0]
	v_pk_mul_f32 v[2:3], v[2:3], s[40:41] op_sel_hi:[1,0]
	v_pk_mul_f32 v[0:1], v[0:1], s[40:41] op_sel_hi:[1,0]
	v_readlane_b32 s78, v255, 11
	v_readlane_b32 s79, v255, 13
	s_and_b64 vcc, exec, s[38:39]
	s_cbranch_vccz .LBB0_1026

; __device__ __forceinline__ int lane_id() { int l; asm volatile("v_mbcnt_lo_u32_b32 %0, -1, 0\n\tv_mbcnt_hi_u32_b32 %0, -1, %0" : "=v"(l)); return l; }
; #define G_STAGE(bufoff, gbase, voff) do { _Pragma("unroll") for (int _i = 0; _i < 2; ++_i) \
;         __builtin_amdgcn_global_load_lds((const unsigned*)((const char*)(gbase) + (voff)[_i]), (LAS unsigned*)(lds + (bufoff) + ldsw + _i * 8192), 16, 0, 0); } while (0)
; #define G_LDA(dst, b, h) do { _Pragma("unroll") for (int m = 0; m < 4; ++m) G_LD8(dst[m], lds + G_SA(b, h) + aoff + m * 2048); } while (0)
; #define G_BAR __builtin_amdgcn_s_barrier()
;     ...
;         for (int t = 0; t < nt; t += 2) {
;             const bool last = (t == nt - 2);
;             { const int tz_ = wid * 64 + lane_id();
; #pragma unroll
;               for (int i = 0; i < 2; ++i) { int R, C; stage_rc(tz_ * 16 + i * 8192, R, C); const int Rb = Epi::PERM ? ((R & ~31) + perm32(R & 31)) : R;
;                   voffA[i] = (unsigned)(R * S.multA * S.pitchA + C) * 2u; voffB[i] = (unsigned)(Rb * S.multB * S.pitchB + C) * 2u; } }
;             if constexpr (GATHER) asm volatile("" : "+v"(gc0[0]), "+v"(gc0[1]), "+v"(gc1[0]), "+v"(gc1[1]));
;             if constexpr (PREF) { if (t == nt - 4) S.prefetch(nxt, lds); }
;             const char* a11 = cur.a1 + (size_t)(t + 1) * kstep;
;             const char* a02 = last ? nxt.a0 : cur.a0 + (size_t)(t + 2) * kstep; const char* a12 = last ? nxt.a1 : cur.a1 + (size_t)(t + 2) * kstep;
;             const char* b02 = last ? nxt.b0 : cur.b0 + (size_t)(t + 2) * kstep; const char* b12 = last ? nxt.b1 : cur.b1 + (size_t)(t + 2) * kstep;
;             G_LDB(B0, 0, 0); G_LDB(B1, 0, 1); G_SCHED; G_LDA(At, 0, 0); G_STAGE(G_SA(1, 1), a11, vA1);
;             if constexpr (GATHER) { if (last) { int tz = tid; asm volatile("" : "+v"(tz));
; #pragma unroll
;                 for (int i = 0; i < 2; ++i) { int R, C; stage_rc(tz * 16 + i * 8192, R, C); gc0[i] = S.row_off(nxt, R, lds) + (unsigned)C * 2u; gc1[i] = S.row_off(nxt, 128 + R, lds) + (unsigned)C * 2u; } } }
;             G_WAIT_L(0); G_BAR; G_MMA(0, 0, At, B0); G_MMA(0, 1, At, B1); G_WAIT_V(8); G_BAR; G_SCHED;
;             G_LDA(At, 0, 1); G_STAGE(G_SB(0, 0), b02, voffB); G_STAGE(G_SB(0, 1), b12, voffB); G_STAGE(G_SA(0, 0), a02, vA0);
;             G_WAIT_L(0); G_BAR; G_MMA(1, 0, At, B0); G_MMA(1, 1, At, B1); G_WAIT_V(8); G_BAR; G_SCHED;
.LBB0_1058:
	s_add_i32 s79, s54, 2
	ds_read_b128 v[130:133], v138
	ds_read_b128 v[144:147], v138 offset:1024
	ds_read_b128 v[148:151], v138 offset:2048
	ds_read_b128 v[152:155], v138 offset:3072
	ds_read_b128 v[156:159], v139
	ds_read_b128 v[160:163], v139 offset:1024
	ds_read_b128 v[164:167], v139 offset:2048
	ds_read_b128 v[168:171], v139 offset:3072
	s_add_u32 s80, s52, 0x80
	s_addc_u32 s55, s53, 0
	s_add_i32 s83, s71, s20
	s_add_i32 m0, s33, 0xc000
	s_add_i32 s82, s33, 0xe000
	s_add_i32 s84, s83, 0x2000
	s_cmp_eq_u32 s69, s54
	s_cselect_b32 s54, s44, s80
	s_cselect_b32 s57, s43, s78
	s_cselect_b32 s56, s42, s77
	s_cselect_b32 s59, s47, s41
	s_cselect_b32 s58, s46, s5
	s_cselect_b32 s55, s45, s55
	ds_read_b128 v[172:175], v140
	ds_read_b128 v[176:179], v140 offset:1024
	ds_read_b128 v[180:183], v140 offset:2048
	ds_read_b128 v[184:187], v140 offset:3072
	ds_read_b128 v[188:191], v140 offset:4096
	ds_read_b128 v[192:195], v140 offset:5120
	ds_read_b128 v[196:199], v140 offset:6144
	ds_read_b128 v[200:203], v140 offset:7168
	global_load_lds_dwordx4 v240, s[52:53]
	s_mov_b32 m0, s82
	v_mov_b32_e32 v207, v129
	global_load_lds_dwordx4 v242, s[52:53]
	s_waitcnt lgkmcnt(0)
	s_barrier
	s_setprio 1
	s_waitcnt lgkmcnt(0)
	v_mfma_f32_16x16x32_bf16 v[124:127], v[130:133], v[172:175], v[124:127]
	v_mfma_f32_16x16x32_bf16 v[120:123], v[148:151], v[172:175], v[120:123]
	v_mfma_f32_16x16x32_bf16 v[108:111], v[130:133], v[180:183], v[108:111]
	v_mfma_f32_16x16x32_bf16 v[104:107], v[148:151], v[180:183], v[104:107]
	v_mfma_f32_16x16x32_bf16 v[92:95], v[130:133], v[188:191], v[92:95]
	v_mfma_f32_16x16x32_bf16 v[88:91], v[148:151], v[188:191], v[88:91]
	v_mfma_f32_16x16x32_bf16 v[76:79], v[130:133], v[196:199], v[76:79]
	v_mfma_f32_16x16x32_bf16 v[72:75], v[148:151], v[196:199], v[72:75]
	v_mfma_f32_16x16x32_bf16 v[124:127], v[144:147], v[176:179], v[124:127]
	v_mfma_f32_16x16x32_bf16 v[120:123], v[152:155], v[176:179], v[120:123]
	v_mfma_f32_16x16x32_bf16 v[108:111], v[144:147], v[184:187], v[108:111]
	v_mfma_f32_16x16x32_bf16 v[104:107], v[152:155], v[184:187], v[104:107]
	v_mfma_f32_16x16x32_bf16 v[92:95], v[144:147], v[192:195], v[92:95]
	v_mfma_f32_16x16x32_bf16 v[88:91], v[152:155], v[192:195], v[88:91]
	v_mfma_f32_16x16x32_bf16 v[76:79], v[144:147], v[200:203], v[76:79]
	v_mfma_f32_16x16x32_bf16 v[72:75], v[152:155], v[200:203], v[72:75]
	v_mfma_f32_16x16x32_bf16 v[116:119], v[156:159], v[172:175], v[116:119]
	v_mfma_f32_16x16x32_bf16 v[112:115], v[164:167], v[172:175], v[112:115]
	v_mfma_f32_16x16x32_bf16 v[100:103], v[156:159], v[180:183], v[100:103]
	v_mfma_f32_16x16x32_bf16 v[96:99], v[164:167], v[180:183], v[96:99]
	v_mfma_f32_16x16x32_bf16 v[84:87], v[156:159], v[188:191], v[84:87]
	v_mfma_f32_16x16x32_bf16 v[80:83], v[164:167], v[188:191], v[80:83]
	v_mfma_f32_16x16x32_bf16 v[68:71], v[156:159], v[196:199], v[68:71]
	v_mfma_f32_16x16x32_bf16 v[64:67], v[164:167], v[196:199], v[64:67]
	v_mfma_f32_16x16x32_bf16 v[116:119], v[160:163], v[176:179], v[116:119]
	v_mfma_f32_16x16x32_bf16 v[112:115], v[168:171], v[176:179], v[112:115]
	v_mfma_f32_16x16x32_bf16 v[100:103], v[160:163], v[184:187], v[100:103]
	v_mfma_f32_16x16x32_bf16 v[96:99], v[168:171], v[184:187], v[96:99]
	v_mfma_f32_16x16x32_bf16 v[84:87], v[160:163], v[192:195], v[84:87]
	v_mfma_f32_16x16x32_bf16 v[80:83], v[168:171], v[192:195], v[80:83]
	v_mfma_f32_16x16x32_bf16 v[68:71], v[160:163], v[200:203], v[68:71]
	v_mfma_f32_16x16x32_bf16 v[64:67], v[168:171], v[200:203], v[64:67]
	s_setprio 0
	s_waitcnt vmcnt(8)
	s_barrier
	s_mov_b32 m0, s83
	ds_read_b128 v[172:175], v140 offset:16384
	ds_read_b128 v[176:179], v140 offset:17408
	ds_read_b128 v[180:183], v140 offset:18432
	ds_read_b128 v[184:187], v140 offset:19456
	ds_read_b128 v[188:191], v140 offset:20480
	ds_read_b128 v[192:195], v140 offset:21504
	ds_read_b128 v[196:199], v140 offset:22528
	ds_read_b128 v[200:203], v140 offset:23552
	global_load_lds_dwordx4 v244, s[58:59]
	s_mov_b32 m0, s84
	s_cselect_b32 s81, s49, s61
	s_cselect_b32 s80, s48, s60
	s_add_i32 s82, s72, s20
	global_load_lds_dwordx4 v246, s[58:59]
	s_mov_b32 m0, s82
	v_mov_b32_e32 v205, v129
	global_load_lds_dwordx4 v244, s[80:81]
	s_add_i32 m0, s82, 0x2000
	v_mov_b32_e32 v209, v129
	global_load_lds_dwordx4 v246, s[80:81]
	s_mov_b32 m0, s33
	v_lshl_add_u64 v[210:211], s[58:59], 0, v[244:245]
	global_load_lds_dwordx4 v240, s[56:57]
	s_mov_b32 m0, s62
	v_lshl_add_u64 v[212:213], s[58:59], 0, v[246:247]
	global_load_lds_dwordx4 v242, s[56:57]
	s_waitcnt lgkmcnt(0)
	v_lshl_add_u64 v[204:205], s[80:81], 0, v[244:245]
	v_lshl_add_u64 v[208:209], s[80:81], 0, v[246:247]
	v_lshl_add_u64 v[214:215], s[56:57], 0, v[240:241]
	v_lshl_add_u64 v[216:217], s[56:57], 0, v[242:243]
	s_barrier
; #define G_STAGE(bufoff, gbase, voff) do { _Pragma("unroll") for (int _i = 0; _i < 2; ++_i) \
;         __builtin_amdgcn_global_load_lds((const unsigned*)((const char*)(gbase) + (voff)[_i]), (LAS unsigned*)(lds + (bufoff) + ldsw + _i * 8192), 16, 0, 0); } while (0)
; #define G_LDA(dst, b, h) do { _Pragma("unroll") for (int m = 0; m < 4; ++m) G_LD8(dst[m], lds + G_SA(b, h) + aoff + m * 2048); } while (0)
; #define G_LDB(dst, b, h) do { _Pragma("unroll") for (int n = 0; n < 2; ++n) G_LD8(dst[n], lds + G_SB(b, h) + boff + n * 2048); } while (0)
; #define G_WAIT_V(n) asm volatile("s_waitcnt vmcnt(" #n ")" ::: "memory")
; #define G_WAIT_L(n) asm volatile("s_waitcnt lgkmcnt(" #n ")" ::: "memory")
; #define G_BAR __builtin_amdgcn_s_barrier()
; #define G_SCHED __builtin_amdgcn_sched_barrier(0)
;     ...
;             G_WAIT_L(0); G_BAR; G_MMA(1, 0, At, B0); G_MMA(1, 1, At, B1); G_WAIT_V(8); G_BAR; G_SCHED;
;             G_LDB(B0, 1, 0); G_LDB(B1, 1, 1); G_SCHED; G_LDA(At, 1, 0); G_STAGE(G_SA(0, 1), a12, vA1);
;             G_WAIT_L(0); G_BAR; G_MMA(0, 0, At, B0); G_MMA(0, 1, At, B1); G_WAIT_V(8); G_BAR; G_SCHED;
	s_setprio 1
	s_waitcnt lgkmcnt(0)
	v_mfma_f32_16x16x32_bf16 v[60:63], v[130:133], v[172:175], v[60:63]
	v_mfma_f32_16x16x32_bf16 v[56:59], v[148:151], v[172:175], v[56:59]
	v_mfma_f32_16x16x32_bf16 v[44:47], v[130:133], v[180:183], v[44:47]
	v_mfma_f32_16x16x32_bf16 v[40:43], v[148:151], v[180:183], v[40:43]
	v_mfma_f32_16x16x32_bf16 v[28:31], v[130:133], v[188:191], v[28:31]
	v_mfma_f32_16x16x32_bf16 v[24:27], v[148:151], v[188:191], v[24:27]
	v_mfma_f32_16x16x32_bf16 v[12:15], v[130:133], v[196:199], v[12:15]
	v_mfma_f32_16x16x32_bf16 v[8:11], v[148:151], v[196:199], v[8:11]
	v_mfma_f32_16x16x32_bf16 v[60:63], v[144:147], v[176:179], v[60:63]
	v_mfma_f32_16x16x32_bf16 v[56:59], v[152:155], v[176:179], v[56:59]
	v_mfma_f32_16x16x32_bf16 v[44:47], v[144:147], v[184:187], v[44:47]
	v_mfma_f32_16x16x32_bf16 v[40:43], v[152:155], v[184:187], v[40:43]
	v_mfma_f32_16x16x32_bf16 v[28:31], v[144:147], v[192:195], v[28:31]
	v_mfma_f32_16x16x32_bf16 v[24:27], v[152:155], v[192:195], v[24:27]
	v_mfma_f32_16x16x32_bf16 v[12:15], v[144:147], v[200:203], v[12:15]
	v_mfma_f32_16x16x32_bf16 v[8:11], v[152:155], v[200:203], v[8:11]
	v_mfma_f32_16x16x32_bf16 v[52:55], v[156:159], v[172:175], v[52:55]
	v_mfma_f32_16x16x32_bf16 v[48:51], v[164:167], v[172:175], v[48:51]
	v_mfma_f32_16x16x32_bf16 v[36:39], v[156:159], v[180:183], v[36:39]
	v_mfma_f32_16x16x32_bf16 v[32:35], v[164:167], v[180:183], v[32:35]
	v_mfma_f32_16x16x32_bf16 v[20:23], v[156:159], v[188:191], v[20:23]
	v_mfma_f32_16x16x32_bf16 v[16:19], v[164:167], v[188:191], v[16:19]
	v_mfma_f32_16x16x32_bf16 v[4:7], v[156:159], v[196:199], v[4:7]
	v_mfma_f32_16x16x32_bf16 v[0:3], v[164:167], v[196:199], v[0:3]
	v_mfma_f32_16x16x32_bf16 v[52:55], v[160:163], v[176:179], v[52:55]
	v_mfma_f32_16x16x32_bf16 v[48:51], v[168:171], v[176:179], v[48:51]
	v_mfma_f32_16x16x32_bf16 v[36:39], v[160:163], v[184:187], v[36:39]
	v_mfma_f32_16x16x32_bf16 v[32:35], v[168:171], v[184:187], v[32:35]
	v_mfma_f32_16x16x32_bf16 v[20:23], v[160:163], v[192:195], v[20:23]
	v_mfma_f32_16x16x32_bf16 v[16:19], v[168:171], v[192:195], v[16:19]
	v_mfma_f32_16x16x32_bf16 v[4:7], v[160:163], v[200:203], v[4:7]
	v_mfma_f32_16x16x32_bf16 v[0:3], v[168:171], v[200:203], v[0:3]
	s_setprio 0
	s_waitcnt vmcnt(8)
	s_barrier
	s_add_i32 s56, 0, 0x18000
	s_add_i32 s57, 0, 0x1c000
	v_add_u32_e32 v152, s56, v137
	v_add_u32_e32 v168, s57, v137
	ds_read_b128 v[130:133], v152
	ds_read_b128 v[144:147], v152 offset:1024
	ds_read_b128 v[148:151], v152 offset:2048
	ds_read_b128 v[152:155], v152 offset:3072
	ds_read_b128 v[156:159], v168
	ds_read_b128 v[160:163], v168 offset:1024
	ds_read_b128 v[164:167], v168 offset:2048
	ds_read_b128 v[168:171], v168 offset:3072
	s_mov_b32 m0, s63
	ds_read_b128 v[172:175], v140 offset:32768
	ds_read_b128 v[176:179], v140 offset:33792
	ds_read_b128 v[180:183], v140 offset:34816
	ds_read_b128 v[184:187], v140 offset:35840
	ds_read_b128 v[188:191], v140 offset:36864
	ds_read_b128 v[192:195], v140 offset:37888
	ds_read_b128 v[196:199], v140 offset:38912
	ds_read_b128 v[200:203], v140 offset:39936
	global_load_lds_dwordx4 v240, s[54:55]
	s_mov_b32 m0, s64
	s_nop 0
	global_load_lds_dwordx4 v242, s[54:55]
	s_waitcnt lgkmcnt(0)
	s_barrier
	s_setprio 1
	s_waitcnt lgkmcnt(0)
	v_mfma_f32_16x16x32_bf16 v[124:127], v[130:133], v[172:175], v[124:127]
	v_mfma_f32_16x16x32_bf16 v[120:123], v[148:151], v[172:175], v[120:123]
	v_mfma_f32_16x16x32_bf16 v[108:111], v[130:133], v[180:183], v[108:111]
	v_mfma_f32_16x16x32_bf16 v[104:107], v[148:151], v[180:183], v[104:107]
	v_mfma_f32_16x16x32_bf16 v[92:95], v[130:133], v[188:191], v[92:95]
	v_mfma_f32_16x16x32_bf16 v[88:91], v[148:151], v[188:191], v[88:91]
	v_mfma_f32_16x16x32_bf16 v[76:79], v[130:133], v[196:199], v[76:79]
	v_mfma_f32_16x16x32_bf16 v[72:75], v[148:151], v[196:199], v[72:75]
	v_mfma_f32_16x16x32_bf16 v[124:127], v[144:147], v[176:179], v[124:127]
	v_mfma_f32_16x16x32_bf16 v[120:123], v[152:155], v[176:179], v[120:123]
	v_mfma_f32_16x16x32_bf16 v[108:111], v[144:147], v[184:187], v[108:111]
	v_mfma_f32_16x16x32_bf16 v[104:107], v[152:155], v[184:187], v[104:107]
	v_mfma_f32_16x16x32_bf16 v[92:95], v[144:147], v[192:195], v[92:95]
	v_mfma_f32_16x16x32_bf16 v[88:91], v[152:155], v[192:195], v[88:91]
	v_mfma_f32_16x16x32_bf16 v[76:79], v[144:147], v[200:203], v[76:79]
	v_mfma_f32_16x16x32_bf16 v[72:75], v[152:155], v[200:203], v[72:75]
	v_mfma_f32_16x16x32_bf16 v[116:119], v[156:159], v[172:175], v[116:119]
	v_mfma_f32_16x16x32_bf16 v[112:115], v[164:167], v[172:175], v[112:115]
	v_mfma_f32_16x16x32_bf16 v[100:103], v[156:159], v[180:183], v[100:103]
	v_mfma_f32_16x16x32_bf16 v[96:99], v[164:167], v[180:183], v[96:99]
	v_mfma_f32_16x16x32_bf16 v[84:87], v[156:159], v[188:191], v[84:87]
	v_mfma_f32_16x16x32_bf16 v[80:83], v[164:167], v[188:191], v[80:83]
	v_mfma_f32_16x16x32_bf16 v[68:71], v[156:159], v[196:199], v[68:71]
	v_mfma_f32_16x16x32_bf16 v[64:67], v[164:167], v[196:199], v[64:67]
	v_mfma_f32_16x16x32_bf16 v[116:119], v[160:163], v[176:179], v[116:119]
	v_mfma_f32_16x16x32_bf16 v[112:115], v[168:171], v[176:179], v[112:115]
	v_mfma_f32_16x16x32_bf16 v[100:103], v[160:163], v[184:187], v[100:103]
	v_mfma_f32_16x16x32_bf16 v[96:99], v[168:171], v[184:187], v[96:99]
	v_mfma_f32_16x16x32_bf16 v[84:87], v[160:163], v[192:195], v[84:87]
	v_mfma_f32_16x16x32_bf16 v[80:83], v[168:171], v[192:195], v[80:83]
	v_mfma_f32_16x16x32_bf16 v[68:71], v[160:163], v[200:203], v[68:71]
	v_mfma_f32_16x16x32_bf16 v[64:67], v[168:171], v[200:203], v[64:67]
	s_setprio 0
	s_waitcnt vmcnt(8)
	s_barrier
; #define G_STAGE(bufoff, gbase, voff) do { _Pragma("unroll") for (int _i = 0; _i < 2; ++_i) \
;         __builtin_amdgcn_global_load_lds((const unsigned*)((const char*)(gbase) + (voff)[_i]), (LAS unsigned*)(lds + (bufoff) + ldsw + _i * 8192), 16, 0, 0); } while (0)
; #define G_LDA(dst, b, h) do { _Pragma("unroll") for (int m = 0; m < 4; ++m) G_LD8(dst[m], lds + G_SA(b, h) + aoff + m * 2048); } while (0)
; #define G_WAIT_V(n) asm volatile("s_waitcnt vmcnt(" #n ")" ::: "memory")
; #define G_WAIT_L(n) asm volatile("s_waitcnt lgkmcnt(" #n ")" ::: "memory")
; #define G_BAR __builtin_amdgcn_s_barrier()
; #define G_SCHED __builtin_amdgcn_sched_barrier(0)
;     ...
;             G_LDA(At, 1, 1); G_STAGE(G_SB(1, 0), b02 + kstep, voffB); G_STAGE(G_SB(1, 1), b12 + kstep, voffB); G_STAGE(G_SA(1, 0), a02 + kstep, vA0);
;             G_WAIT_L(0); G_BAR; G_MMA(1, 0, At, B0); G_MMA(1, 1, At, B1); G_WAIT_V(8); G_BAR; G_SCHED;
;         }
	s_add_i32 s54, s56, s20
	v_lshl_add_u64 v[206:207], v[210:211], 0, s[34:35]
	s_mov_b32 m0, s54
	ds_read_b128 v[172:175], v140 offset:49152
	ds_read_b128 v[176:179], v140 offset:50176
	ds_read_b128 v[180:183], v140 offset:51200
	ds_read_b128 v[184:187], v140 offset:52224
	ds_read_b128 v[188:191], v140 offset:53248
	ds_read_b128 v[192:195], v140 offset:54272
	ds_read_b128 v[196:199], v140 offset:55296
	ds_read_b128 v[200:203], v140 offset:56320
	global_load_lds_dwordx4 v[206:207], off
	v_lshl_add_u64 v[206:207], v[212:213], 0, s[34:35]
	s_add_i32 m0, s54, 0x2000
	s_add_i32 s54, s57, s20
	global_load_lds_dwordx4 v[206:207], off
	v_lshl_add_u64 v[204:205], v[204:205], 0, s[34:35]
	s_mov_b32 m0, s54
	s_nop 0
	global_load_lds_dwordx4 v[204:205], off
	v_lshl_add_u64 v[204:205], v[208:209], 0, s[34:35]
	s_add_i32 m0, s54, 0x2000
	s_nop 0
	global_load_lds_dwordx4 v[204:205], off
	v_lshl_add_u64 v[204:205], v[214:215], 0, s[34:35]
	s_mov_b32 m0, s66
	s_nop 0
	global_load_lds_dwordx4 v[204:205], off
	v_lshl_add_u64 v[204:205], v[216:217], 0, s[34:35]
	s_mov_b32 m0, s67
	s_nop 0
	global_load_lds_dwordx4 v[204:205], off
	s_waitcnt lgkmcnt(0)
	s_barrier
	s_setprio 1
	s_waitcnt lgkmcnt(0)
	v_mfma_f32_16x16x32_bf16 v[60:63], v[130:133], v[172:175], v[60:63]
	v_mfma_f32_16x16x32_bf16 v[56:59], v[148:151], v[172:175], v[56:59]
	v_mfma_f32_16x16x32_bf16 v[44:47], v[130:133], v[180:183], v[44:47]
	v_mfma_f32_16x16x32_bf16 v[40:43], v[148:151], v[180:183], v[40:43]
	v_mfma_f32_16x16x32_bf16 v[28:31], v[130:133], v[188:191], v[28:31]
	v_mfma_f32_16x16x32_bf16 v[24:27], v[148:151], v[188:191], v[24:27]
	v_mfma_f32_16x16x32_bf16 v[12:15], v[130:133], v[196:199], v[12:15]
	v_mfma_f32_16x16x32_bf16 v[8:11], v[148:151], v[196:199], v[8:11]
	v_mfma_f32_16x16x32_bf16 v[60:63], v[144:147], v[176:179], v[60:63]
	v_mfma_f32_16x16x32_bf16 v[56:59], v[152:155], v[176:179], v[56:59]
	v_mfma_f32_16x16x32_bf16 v[44:47], v[144:147], v[184:187], v[44:47]
	v_mfma_f32_16x16x32_bf16 v[40:43], v[152:155], v[184:187], v[40:43]
	v_mfma_f32_16x16x32_bf16 v[28:31], v[144:147], v[192:195], v[28:31]
	v_mfma_f32_16x16x32_bf16 v[24:27], v[152:155], v[192:195], v[24:27]
	v_mfma_f32_16x16x32_bf16 v[12:15], v[144:147], v[200:203], v[12:15]
	v_mfma_f32_16x16x32_bf16 v[8:11], v[152:155], v[200:203], v[8:11]
	v_mfma_f32_16x16x32_bf16 v[52:55], v[156:159], v[172:175], v[52:55]
	v_mfma_f32_16x16x32_bf16 v[48:51], v[164:167], v[172:175], v[48:51]
	v_mfma_f32_16x16x32_bf16 v[36:39], v[156:159], v[180:183], v[36:39]
	v_mfma_f32_16x16x32_bf16 v[32:35], v[164:167], v[180:183], v[32:35]
	v_mfma_f32_16x16x32_bf16 v[20:23], v[156:159], v[188:191], v[20:23]
	v_mfma_f32_16x16x32_bf16 v[16:19], v[164:167], v[188:191], v[16:19]
	v_mfma_f32_16x16x32_bf16 v[4:7], v[156:159], v[196:199], v[4:7]
	v_mfma_f32_16x16x32_bf16 v[0:3], v[164:167], v[196:199], v[0:3]
	v_mfma_f32_16x16x32_bf16 v[52:55], v[160:163], v[176:179], v[52:55]
	v_mfma_f32_16x16x32_bf16 v[48:51], v[168:171], v[176:179], v[48:51]
	v_mfma_f32_16x16x32_bf16 v[36:39], v[160:163], v[184:187], v[36:39]
	v_mfma_f32_16x16x32_bf16 v[32:35], v[168:171], v[184:187], v[32:35]
	v_mfma_f32_16x16x32_bf16 v[20:23], v[160:163], v[192:195], v[20:23]
	v_mfma_f32_16x16x32_bf16 v[16:19], v[168:171], v[192:195], v[16:19]
	v_mfma_f32_16x16x32_bf16 v[4:7], v[160:163], v[200:203], v[4:7]
	v_mfma_f32_16x16x32_bf16 v[0:3], v[168:171], v[200:203], v[0:3]
	s_setprio 0
	s_waitcnt vmcnt(8)
	s_barrier
	s_add_u32 s5, s5, 0x100
	s_addc_u32 s41, s41, 0
	s_add_u32 s60, s60, 0x100
	s_addc_u32 s61, s61, 0
	s_add_u32 s77, s77, 0x100
	s_addc_u32 s78, s78, 0
	s_add_u32 s52, s52, 0x100
	s_addc_u32 s53, s53, 0
	s_cmp_ge_i32 s79, s24
	s_mov_b32 s54, s79
	s_cbranch_scc0 .LBB0_1058
	v_readlane_b32 s78, v255, 11
	v_readlane_b32 s79, v255, 13
	s_and_b64 vcc, exec, s[38:39]
	s_cbranch_vccz .LBB0_1061

; #define G_STAGE(bufoff, gbase, voff) do { _Pragma("unroll") for (int _i = 0; _i < 2; ++_i) \
;         __builtin_amdgcn_global_load_lds((const unsigned*)((const char*)(gbase) + (voff)[_i]), (LAS unsigned*)(lds + (bufoff) + ldsw + _i * 8192), 16, 0, 0); } while (0)
; #define G_LDA(dst, b, h) do { _Pragma("unroll") for (int m = 0; m < 4; ++m) G_LD8(dst[m], lds + G_SA(b, h) + aoff + m * 2048); } while (0)
; #define G_LDB(dst, b, h) do { _Pragma("unroll") for (int n = 0; n < 2; ++n) G_LD8(dst[n], lds + G_SB(b, h) + boff + n * 2048); } while (0)
; #define G_WAIT_V(n) asm volatile("s_waitcnt vmcnt(" #n ")" ::: "memory")
; #define G_WAIT_L(n) asm volatile("s_waitcnt lgkmcnt(" #n ")" ::: "memory")
; #define G_BAR __builtin_amdgcn_s_barrier()
; #define G_SCHED __builtin_amdgcn_sched_barrier(0)
;     __device__ __forceinline__ unsigned row_off(const Unit& u, int r, LAS unsigned char* lds) const { return (unsigned)((const LAS int*)(lds + LDS_STAGE + u.q * 4096))[r] * (unsigned)rowbytes; }
;     ...
;             const char* a11 = cur.a1 + (size_t)(t + 1) * kstep;
;             const char* a02 = last ? nxt.a0 : cur.a0 + (size_t)(t + 2) * kstep; const char* a12 = last ? nxt.a1 : cur.a1 + (size_t)(t + 2) * kstep;
;             const char* b02 = last ? nxt.b0 : cur.b0 + (size_t)(t + 2) * kstep; const char* b12 = last ? nxt.b1 : cur.b1 + (size_t)(t + 2) * kstep;
;             G_LDB(B0, 0, 0); G_LDB(B1, 0, 1); G_SCHED; G_LDA(At, 0, 0); G_STAGE(G_SA(1, 1), a11, vA1);
;             if constexpr (GATHER) { if (last) { int tz = tid; asm volatile("" : "+v"(tz));
; #pragma unroll
;                 for (int i = 0; i < 2; ++i) { int R, C; stage_rc(tz * 16 + i * 8192, R, C); gc0[i] = S.row_off(nxt, R, lds) + (unsigned)C * 2u; gc1[i] = S.row_off(nxt, 128 + R, lds) + (unsigned)C * 2u; } } }
;             G_WAIT_L(0); G_BAR; G_MMA(0, 0, At, B0); G_MMA(0, 1, At, B1); G_WAIT_V(8); G_BAR; G_SCHED;
;             G_LDA(At, 0, 1); G_STAGE(G_SB(0, 0), b02, voffB); G_STAGE(G_SB(0, 1), b12, voffB); G_STAGE(G_SA(0, 0), a02, vA0);
;             G_WAIT_L(0); G_BAR; G_MMA(1, 0, At, B0); G_MMA(1, 1, At, B1); G_WAIT_V(8); G_BAR; G_SCHED;
.LBB0_1322:
	s_add_i32 vcc_lo, s66, 2
	s_add_u32 vcc_hi, s64, 0x80
	s_addc_u32 s67, s65, 0
	s_add_i32 s68, 0, 0x10000
	s_add_i32 s1, 0, 0x14000
	v_add_u32_e32 v146, s68, v172
	v_add_u32_e32 v162, s1, v172
	ds_read_b128 v[130:133], v146
	ds_read_b128 v[134:137], v146 offset:1024
	ds_read_b128 v[138:141], v146 offset:2048
	ds_read_b128 v[146:149], v146 offset:3072
	ds_read_b128 v[150:153], v162
	ds_read_b128 v[154:157], v162 offset:1024
	ds_read_b128 v[158:161], v162 offset:2048
	ds_read_b128 v[162:165], v162 offset:3072
	s_add_i32 s11, s68, s77
	s_add_i32 m0, s10, 0xc000
	s_add_i32 s33, s10, 0xe000
	s_add_i32 s21, s11, 0x2000
	s_cmp_eq_u32 s89, s66
	s_cselect_b32 s66, s54, vcc_hi
	s_cselect_b32 s69, s53, s97
	s_cselect_b32 s68, s52, s96
	s_cselect_b32 s71, s57, s93
	s_cselect_b32 s70, s56, s9
	s_cselect_b32 s67, s55, s67
	ds_read_b128 v[174:177], v173
	ds_read_b128 v[178:181], v173 offset:1024
	ds_read_b128 v[182:185], v173 offset:2048
	ds_read_b128 v[186:189], v173 offset:3072
	ds_read_b128 v[190:193], v173 offset:4096
	ds_read_b128 v[194:197], v173 offset:5120
	ds_read_b128 v[198:201], v173 offset:6144
	ds_read_b128 v[202:205], v173 offset:7168
	global_load_lds_dwordx4 v240, s[64:65]
	s_mov_b32 m0, s33
	s_nop 0
	global_load_lds_dwordx4 v242, s[64:65]
	s_waitcnt lgkmcnt(0)
	v_mov_b32_e32 v129, v145
	s_barrier
	s_setprio 1
	s_waitcnt lgkmcnt(0)
	v_mfma_f32_16x16x32_bf16 v[124:127], v[130:133], v[174:177], v[124:127]
	v_mfma_f32_16x16x32_bf16 v[120:123], v[138:141], v[174:177], v[120:123]
	v_mfma_f32_16x16x32_bf16 v[116:119], v[130:133], v[182:185], v[116:119]
	v_mfma_f32_16x16x32_bf16 v[112:115], v[138:141], v[182:185], v[112:115]
	v_mfma_f32_16x16x32_bf16 v[108:111], v[130:133], v[190:193], v[108:111]
	v_mfma_f32_16x16x32_bf16 v[104:107], v[138:141], v[190:193], v[104:107]
	v_mfma_f32_16x16x32_bf16 v[100:103], v[130:133], v[198:201], v[100:103]
	v_mfma_f32_16x16x32_bf16 v[96:99], v[138:141], v[198:201], v[96:99]
	v_mfma_f32_16x16x32_bf16 v[124:127], v[134:137], v[178:181], v[124:127]
	v_mfma_f32_16x16x32_bf16 v[120:123], v[146:149], v[178:181], v[120:123]
	v_mfma_f32_16x16x32_bf16 v[116:119], v[134:137], v[186:189], v[116:119]
	v_mfma_f32_16x16x32_bf16 v[112:115], v[146:149], v[186:189], v[112:115]
	v_mfma_f32_16x16x32_bf16 v[108:111], v[134:137], v[194:197], v[108:111]
	v_mfma_f32_16x16x32_bf16 v[104:107], v[146:149], v[194:197], v[104:107]
	v_mfma_f32_16x16x32_bf16 v[100:103], v[134:137], v[202:205], v[100:103]
	v_mfma_f32_16x16x32_bf16 v[96:99], v[146:149], v[202:205], v[96:99]
	v_mfma_f32_16x16x32_bf16 v[68:71], v[150:153], v[174:177], v[68:71]
	v_mfma_f32_16x16x32_bf16 v[60:63], v[158:161], v[174:177], v[60:63]
	v_mfma_f32_16x16x32_bf16 v[52:55], v[150:153], v[182:185], v[52:55]
	v_mfma_f32_16x16x32_bf16 v[48:51], v[158:161], v[182:185], v[48:51]
	v_mfma_f32_16x16x32_bf16 v[44:47], v[150:153], v[190:193], v[44:47]
	v_mfma_f32_16x16x32_bf16 v[40:43], v[158:161], v[190:193], v[40:43]
	v_mfma_f32_16x16x32_bf16 v[36:39], v[150:153], v[198:201], v[36:39]
	v_mfma_f32_16x16x32_bf16 v[32:35], v[158:161], v[198:201], v[32:35]
	v_mfma_f32_16x16x32_bf16 v[68:71], v[154:157], v[178:181], v[68:71]
	v_mfma_f32_16x16x32_bf16 v[60:63], v[162:165], v[178:181], v[60:63]
	v_mfma_f32_16x16x32_bf16 v[52:55], v[154:157], v[186:189], v[52:55]
	v_mfma_f32_16x16x32_bf16 v[48:51], v[162:165], v[186:189], v[48:51]
	v_mfma_f32_16x16x32_bf16 v[44:47], v[154:157], v[194:197], v[44:47]
	v_mfma_f32_16x16x32_bf16 v[40:43], v[162:165], v[194:197], v[40:43]
	v_mfma_f32_16x16x32_bf16 v[36:39], v[154:157], v[202:205], v[36:39]
	v_mfma_f32_16x16x32_bf16 v[32:35], v[162:165], v[202:205], v[32:35]
	s_setprio 0
	s_waitcnt vmcnt(8)
	s_barrier
	s_mov_b32 m0, s11
	ds_read_b128 v[174:177], v173 offset:16384
	ds_read_b128 v[178:181], v173 offset:17408
	ds_read_b128 v[182:185], v173 offset:18432
	ds_read_b128 v[186:189], v173 offset:19456
	ds_read_b128 v[190:193], v173 offset:20480
	ds_read_b128 v[194:197], v173 offset:21504
	ds_read_b128 v[198:201], v173 offset:22528
	ds_read_b128 v[202:205], v173 offset:23552
	v_mov_b32_e32 v143, v145
	global_load_lds_dwordx4 v244, s[70:71]
	v_mov_b32_e32 v207, v145
	s_mov_b32 m0, s21
	v_lshl_add_u64 v[208:209], s[70:71], 0, v[244:245]
	v_lshl_add_u64 v[210:211], s[70:71], 0, v[246:247]
	global_load_lds_dwordx4 v246, s[70:71]
	s_cselect_b32 s71, s59, s95
	s_cselect_b32 s70, s58, s94
	s_add_i32 s1, s1, s77
	s_mov_b32 m0, s1
	v_lshl_add_u64 v[212:213], s[70:71], 0, v[244:245]
	global_load_lds_dwordx4 v244, s[70:71]
	s_add_i32 m0, s1, 0x2000
	v_lshl_add_u64 v[142:143], s[70:71], 0, v[246:247]
	global_load_lds_dwordx4 v246, s[70:71]
	s_mov_b32 m0, s10
	v_lshl_add_u64 v[206:207], s[68:69], 0, v[240:241]
	global_load_lds_dwordx4 v240, s[68:69]
	s_mov_b32 m0, s63
	v_lshl_add_u64 v[214:215], s[68:69], 0, v[242:243]
	global_load_lds_dwordx4 v242, s[68:69]
	s_waitcnt lgkmcnt(0)
	s_barrier
; #define G_STAGE(bufoff, gbase, voff) do { _Pragma("unroll") for (int _i = 0; _i < 2; ++_i) \
;         __builtin_amdgcn_global_load_lds((const unsigned*)((const char*)(gbase) + (voff)[_i]), (LAS unsigned*)(lds + (bufoff) + ldsw + _i * 8192), 16, 0, 0); } while (0)
; #define G_LDA(dst, b, h) do { _Pragma("unroll") for (int m = 0; m < 4; ++m) G_LD8(dst[m], lds + G_SA(b, h) + aoff + m * 2048); } while (0)
; #define G_LDB(dst, b, h) do { _Pragma("unroll") for (int n = 0; n < 2; ++n) G_LD8(dst[n], lds + G_SB(b, h) + boff + n * 2048); } while (0)
; #define G_WAIT_V(n) asm volatile("s_waitcnt vmcnt(" #n ")" ::: "memory")
; #define G_WAIT_L(n) asm volatile("s_waitcnt lgkmcnt(" #n ")" ::: "memory")
; #define G_BAR __builtin_amdgcn_s_barrier()
; #define G_SCHED __builtin_amdgcn_sched_barrier(0)
;     ...
;             G_WAIT_L(0); G_BAR; G_MMA(1, 0, At, B0); G_MMA(1, 1, At, B1); G_WAIT_V(8); G_BAR; G_SCHED;
;             G_LDB(B0, 1, 0); G_LDB(B1, 1, 1); G_SCHED; G_LDA(At, 1, 0); G_STAGE(G_SA(0, 1), a12, vA1);
;             G_WAIT_L(0); G_BAR; G_MMA(0, 0, At, B0); G_MMA(0, 1, At, B1); G_WAIT_V(8); G_BAR; G_SCHED;
	s_setprio 1
	s_waitcnt lgkmcnt(0)
	v_mfma_f32_16x16x32_bf16 v[92:95], v[130:133], v[174:177], v[92:95]
	v_mfma_f32_16x16x32_bf16 v[88:91], v[138:141], v[174:177], v[88:91]
	v_mfma_f32_16x16x32_bf16 v[84:87], v[130:133], v[182:185], v[84:87]
	v_mfma_f32_16x16x32_bf16 v[80:83], v[138:141], v[182:185], v[80:83]
	v_mfma_f32_16x16x32_bf16 v[76:79], v[130:133], v[190:193], v[76:79]
	v_mfma_f32_16x16x32_bf16 v[72:75], v[138:141], v[190:193], v[72:75]
	v_mfma_f32_16x16x32_bf16 v[64:67], v[130:133], v[198:201], v[64:67]
	v_mfma_f32_16x16x32_bf16 v[56:59], v[138:141], v[198:201], v[56:59]
	v_mfma_f32_16x16x32_bf16 v[92:95], v[134:137], v[178:181], v[92:95]
	v_mfma_f32_16x16x32_bf16 v[88:91], v[146:149], v[178:181], v[88:91]
	v_mfma_f32_16x16x32_bf16 v[84:87], v[134:137], v[186:189], v[84:87]
	v_mfma_f32_16x16x32_bf16 v[80:83], v[146:149], v[186:189], v[80:83]
	v_mfma_f32_16x16x32_bf16 v[76:79], v[134:137], v[194:197], v[76:79]
	v_mfma_f32_16x16x32_bf16 v[72:75], v[146:149], v[194:197], v[72:75]
	v_mfma_f32_16x16x32_bf16 v[64:67], v[134:137], v[202:205], v[64:67]
	v_mfma_f32_16x16x32_bf16 v[56:59], v[146:149], v[202:205], v[56:59]
	v_mfma_f32_16x16x32_bf16 v[28:31], v[150:153], v[174:177], v[28:31]
	v_mfma_f32_16x16x32_bf16 v[24:27], v[158:161], v[174:177], v[24:27]
	v_mfma_f32_16x16x32_bf16 v[20:23], v[150:153], v[182:185], v[20:23]
	v_mfma_f32_16x16x32_bf16 v[16:19], v[158:161], v[182:185], v[16:19]
	v_mfma_f32_16x16x32_bf16 v[12:15], v[150:153], v[190:193], v[12:15]
	v_mfma_f32_16x16x32_bf16 v[8:11], v[158:161], v[190:193], v[8:11]
	v_mfma_f32_16x16x32_bf16 v[4:7], v[150:153], v[198:201], v[4:7]
	v_mfma_f32_16x16x32_bf16 v[0:3], v[158:161], v[198:201], v[0:3]
	v_mfma_f32_16x16x32_bf16 v[28:31], v[154:157], v[178:181], v[28:31]
	v_mfma_f32_16x16x32_bf16 v[24:27], v[162:165], v[178:181], v[24:27]
	v_mfma_f32_16x16x32_bf16 v[20:23], v[154:157], v[186:189], v[20:23]
	v_mfma_f32_16x16x32_bf16 v[16:19], v[162:165], v[186:189], v[16:19]
	v_mfma_f32_16x16x32_bf16 v[12:15], v[154:157], v[194:197], v[12:15]
	v_mfma_f32_16x16x32_bf16 v[8:11], v[162:165], v[194:197], v[8:11]
	v_mfma_f32_16x16x32_bf16 v[4:7], v[154:157], v[202:205], v[4:7]
	v_mfma_f32_16x16x32_bf16 v[0:3], v[162:165], v[202:205], v[0:3]
	s_setprio 0
	s_waitcnt vmcnt(8)
	s_barrier
	s_add_i32 s1, 0, 0x18000
	v_add_u32_e32 v129, s1, v172
	s_add_i32 s11, 0, 0x1c000
	ds_read_b128 v[130:133], v129
	ds_read_b128 v[134:137], v129 offset:1024
	ds_read_b128 v[138:141], v129 offset:2048
	ds_read_b128 v[146:149], v129 offset:3072
	v_add_u32_e32 v129, s11, v172
	ds_read_b128 v[150:153], v129
	ds_read_b128 v[154:157], v129 offset:1024
	ds_read_b128 v[158:161], v129 offset:2048
	ds_read_b128 v[162:165], v129 offset:3072
	s_mov_b32 m0, s72
	ds_read_b128 v[174:177], v173 offset:32768
	ds_read_b128 v[178:181], v173 offset:33792
	ds_read_b128 v[182:185], v173 offset:34816
	ds_read_b128 v[186:189], v173 offset:35840
	ds_read_b128 v[190:193], v173 offset:36864
	ds_read_b128 v[194:197], v173 offset:37888
	ds_read_b128 v[198:201], v173 offset:38912
	ds_read_b128 v[202:205], v173 offset:39936
	global_load_lds_dwordx4 v240, s[66:67]
	s_mov_b32 m0, s73
	s_nop 0
	global_load_lds_dwordx4 v242, s[66:67]
	s_waitcnt lgkmcnt(0)
	s_barrier
	s_setprio 1
	s_waitcnt lgkmcnt(0)
	v_mfma_f32_16x16x32_bf16 v[124:127], v[130:133], v[174:177], v[124:127]
	v_mfma_f32_16x16x32_bf16 v[120:123], v[138:141], v[174:177], v[120:123]
	v_mfma_f32_16x16x32_bf16 v[116:119], v[130:133], v[182:185], v[116:119]
	v_mfma_f32_16x16x32_bf16 v[112:115], v[138:141], v[182:185], v[112:115]
	v_mfma_f32_16x16x32_bf16 v[108:111], v[130:133], v[190:193], v[108:111]
	v_mfma_f32_16x16x32_bf16 v[104:107], v[138:141], v[190:193], v[104:107]
	v_mfma_f32_16x16x32_bf16 v[100:103], v[130:133], v[198:201], v[100:103]
	v_mfma_f32_16x16x32_bf16 v[96:99], v[138:141], v[198:201], v[96:99]
	v_mfma_f32_16x16x32_bf16 v[124:127], v[134:137], v[178:181], v[124:127]
	v_mfma_f32_16x16x32_bf16 v[120:123], v[146:149], v[178:181], v[120:123]
	v_mfma_f32_16x16x32_bf16 v[116:119], v[134:137], v[186:189], v[116:119]
	v_mfma_f32_16x16x32_bf16 v[112:115], v[146:149], v[186:189], v[112:115]
	v_mfma_f32_16x16x32_bf16 v[108:111], v[134:137], v[194:197], v[108:111]
	v_mfma_f32_16x16x32_bf16 v[104:107], v[146:149], v[194:197], v[104:107]
	v_mfma_f32_16x16x32_bf16 v[100:103], v[134:137], v[202:205], v[100:103]
	v_mfma_f32_16x16x32_bf16 v[96:99], v[146:149], v[202:205], v[96:99]
	v_mfma_f32_16x16x32_bf16 v[68:71], v[150:153], v[174:177], v[68:71]
	v_mfma_f32_16x16x32_bf16 v[60:63], v[158:161], v[174:177], v[60:63]
	v_mfma_f32_16x16x32_bf16 v[52:55], v[150:153], v[182:185], v[52:55]
	v_mfma_f32_16x16x32_bf16 v[48:51], v[158:161], v[182:185], v[48:51]
	v_mfma_f32_16x16x32_bf16 v[44:47], v[150:153], v[190:193], v[44:47]
	v_mfma_f32_16x16x32_bf16 v[40:43], v[158:161], v[190:193], v[40:43]
	v_mfma_f32_16x16x32_bf16 v[36:39], v[150:153], v[198:201], v[36:39]
	v_mfma_f32_16x16x32_bf16 v[32:35], v[158:161], v[198:201], v[32:35]
	v_mfma_f32_16x16x32_bf16 v[68:71], v[154:157], v[178:181], v[68:71]
	v_mfma_f32_16x16x32_bf16 v[60:63], v[162:165], v[178:181], v[60:63]
	v_mfma_f32_16x16x32_bf16 v[52:55], v[154:157], v[186:189], v[52:55]
	v_mfma_f32_16x16x32_bf16 v[48:51], v[162:165], v[186:189], v[48:51]
	v_mfma_f32_16x16x32_bf16 v[44:47], v[154:157], v[194:197], v[44:47]
	v_mfma_f32_16x16x32_bf16 v[40:43], v[162:165], v[194:197], v[40:43]
	v_mfma_f32_16x16x32_bf16 v[36:39], v[154:157], v[202:205], v[36:39]
	v_mfma_f32_16x16x32_bf16 v[32:35], v[162:165], v[202:205], v[32:35]
	s_setprio 0
	s_waitcnt vmcnt(8)
	s_barrier
; #define G_STAGE(bufoff, gbase, voff) do { _Pragma("unroll") for (int _i = 0; _i < 2; ++_i) \
;         __builtin_amdgcn_global_load_lds((const unsigned*)((const char*)(gbase) + (voff)[_i]), (LAS unsigned*)(lds + (bufoff) + ldsw + _i * 8192), 16, 0, 0); } while (0)
; #define G_LDA(dst, b, h) do { _Pragma("unroll") for (int m = 0; m < 4; ++m) G_LD8(dst[m], lds + G_SA(b, h) + aoff + m * 2048); } while (0)
; #define G_WAIT_V(n) asm volatile("s_waitcnt vmcnt(" #n ")" ::: "memory")
; #define G_WAIT_L(n) asm volatile("s_waitcnt lgkmcnt(" #n ")" ::: "memory")
; #define G_BAR __builtin_amdgcn_s_barrier()
; #define G_SCHED __builtin_amdgcn_sched_barrier(0)
;     ...
;             G_LDA(At, 1, 1); G_STAGE(G_SB(1, 0), b02 + kstep, voffB); G_STAGE(G_SB(1, 1), b12 + kstep, voffB); G_STAGE(G_SA(1, 0), a02 + kstep, vA0);
;             G_WAIT_L(0); G_BAR; G_MMA(1, 0, At, B0); G_MMA(1, 1, At, B1); G_WAIT_V(8); G_BAR; G_SCHED;
;         }
	s_add_i32 s1, s1, s77
	v_lshl_add_u64 v[128:129], v[208:209], 0, s[48:49]
	s_mov_b32 m0, s1
	ds_read_b128 v[174:177], v173 offset:49152
	ds_read_b128 v[178:181], v173 offset:50176
	ds_read_b128 v[182:185], v173 offset:51200
	ds_read_b128 v[186:189], v173 offset:52224
	ds_read_b128 v[190:193], v173 offset:53248
	ds_read_b128 v[194:197], v173 offset:54272
	ds_read_b128 v[198:201], v173 offset:55296
	ds_read_b128 v[202:205], v173 offset:56320
	global_load_lds_dwordx4 v[128:129], off
	v_lshl_add_u64 v[128:129], v[210:211], 0, s[48:49]
	s_add_i32 m0, s1, 0x2000
	s_add_i32 s1, s11, s77
	global_load_lds_dwordx4 v[128:129], off
	v_lshl_add_u64 v[128:129], v[212:213], 0, s[48:49]
	s_mov_b32 m0, s1
	s_nop 0
	global_load_lds_dwordx4 v[128:129], off
	v_lshl_add_u64 v[128:129], v[142:143], 0, s[48:49]
	s_add_i32 m0, s1, 0x2000
	s_nop 0
	global_load_lds_dwordx4 v[128:129], off
	v_lshl_add_u64 v[128:129], v[206:207], 0, s[48:49]
	s_mov_b32 m0, s75
	s_nop 0
	global_load_lds_dwordx4 v[128:129], off
	v_lshl_add_u64 v[128:129], v[214:215], 0, s[48:49]
	s_mov_b32 m0, s76
	s_nop 0
	global_load_lds_dwordx4 v[128:129], off
	s_waitcnt lgkmcnt(0)
	s_barrier
	s_setprio 1
	s_waitcnt lgkmcnt(0)
	v_mfma_f32_16x16x32_bf16 v[92:95], v[130:133], v[174:177], v[92:95]
	v_mfma_f32_16x16x32_bf16 v[88:91], v[138:141], v[174:177], v[88:91]
	v_mfma_f32_16x16x32_bf16 v[84:87], v[130:133], v[182:185], v[84:87]
	v_mfma_f32_16x16x32_bf16 v[80:83], v[138:141], v[182:185], v[80:83]
	v_mfma_f32_16x16x32_bf16 v[76:79], v[130:133], v[190:193], v[76:79]
	v_mfma_f32_16x16x32_bf16 v[72:75], v[138:141], v[190:193], v[72:75]
	v_mfma_f32_16x16x32_bf16 v[64:67], v[130:133], v[198:201], v[64:67]
	v_mfma_f32_16x16x32_bf16 v[56:59], v[138:141], v[198:201], v[56:59]
	v_mfma_f32_16x16x32_bf16 v[92:95], v[134:137], v[178:181], v[92:95]
	v_mfma_f32_16x16x32_bf16 v[88:91], v[146:149], v[178:181], v[88:91]
	v_mfma_f32_16x16x32_bf16 v[84:87], v[134:137], v[186:189], v[84:87]
	v_mfma_f32_16x16x32_bf16 v[80:83], v[146:149], v[186:189], v[80:83]
	v_mfma_f32_16x16x32_bf16 v[76:79], v[134:137], v[194:197], v[76:79]
	v_mfma_f32_16x16x32_bf16 v[72:75], v[146:149], v[194:197], v[72:75]
	v_mfma_f32_16x16x32_bf16 v[64:67], v[134:137], v[202:205], v[64:67]
	v_mfma_f32_16x16x32_bf16 v[56:59], v[146:149], v[202:205], v[56:59]
	v_mfma_f32_16x16x32_bf16 v[28:31], v[150:153], v[174:177], v[28:31]
	v_mfma_f32_16x16x32_bf16 v[24:27], v[158:161], v[174:177], v[24:27]
	v_mfma_f32_16x16x32_bf16 v[20:23], v[150:153], v[182:185], v[20:23]
	v_mfma_f32_16x16x32_bf16 v[16:19], v[158:161], v[182:185], v[16:19]
	v_mfma_f32_16x16x32_bf16 v[12:15], v[150:153], v[190:193], v[12:15]
	v_mfma_f32_16x16x32_bf16 v[8:11], v[158:161], v[190:193], v[8:11]
	v_mfma_f32_16x16x32_bf16 v[4:7], v[150:153], v[198:201], v[4:7]
	v_mfma_f32_16x16x32_bf16 v[0:3], v[158:161], v[198:201], v[0:3]
	v_mfma_f32_16x16x32_bf16 v[28:31], v[154:157], v[178:181], v[28:31]
	v_mfma_f32_16x16x32_bf16 v[24:27], v[162:165], v[178:181], v[24:27]
	v_mfma_f32_16x16x32_bf16 v[20:23], v[154:157], v[186:189], v[20:23]
	v_mfma_f32_16x16x32_bf16 v[16:19], v[162:165], v[186:189], v[16:19]
	v_mfma_f32_16x16x32_bf16 v[12:15], v[154:157], v[194:197], v[12:15]
	v_mfma_f32_16x16x32_bf16 v[8:11], v[162:165], v[194:197], v[8:11]
	v_mfma_f32_16x16x32_bf16 v[4:7], v[154:157], v[202:205], v[4:7]
	v_mfma_f32_16x16x32_bf16 v[0:3], v[162:165], v[202:205], v[0:3]
	s_setprio 0
	s_waitcnt vmcnt(8)
	s_barrier
	s_add_u32 s9, s9, 0x100
	s_addc_u32 s93, s93, 0
	s_add_u32 s94, s94, 0x100
	s_addc_u32 s95, s95, 0
	s_add_u32 s96, s96, 0x100
	s_addc_u32 s97, s97, 0
	s_add_u32 s64, s64, 0x100
	s_addc_u32 s65, s65, 0
	s_cmp_ge_i32 vcc_lo, s2
	s_mov_b32 s66, vcc_lo
	s_cbranch_scc0 .LBB0_1322
	v_readlane_b32 s64, v255, 9
	v_readlane_b32 s65, v255, 10
	s_load_dword s97, s[64:65], 0xa8
	s_and_b64 vcc, exec, s[46:47]
	s_cbranch_vccz .LBB0_1325

; #define G_STAGE(bufoff, gbase, voff) do { _Pragma("unroll") for (int _i = 0; _i < 2; ++_i) \
;         __builtin_amdgcn_global_load_lds((const unsigned*)((const char*)(gbase) + (voff)[_i]), (LAS unsigned*)(lds + (bufoff) + ldsw + _i * 8192), 16, 0, 0); } while (0)
; #define G_LDA(dst, b, h) do { _Pragma("unroll") for (int m = 0; m < 4; ++m) G_LD8(dst[m], lds + G_SA(b, h) + aoff + m * 2048); } while (0)
; #define G_LDB(dst, b, h) do { _Pragma("unroll") for (int n = 0; n < 2; ++n) G_LD8(dst[n], lds + G_SB(b, h) + boff + n * 2048); } while (0)
; #define G_WAIT_V(n) asm volatile("s_waitcnt vmcnt(" #n ")" ::: "memory")
; #define G_WAIT_L(n) asm volatile("s_waitcnt lgkmcnt(" #n ")" ::: "memory")
; #define G_BAR __builtin_amdgcn_s_barrier()
; #define G_SCHED __builtin_amdgcn_sched_barrier(0)
;     __device__ __forceinline__ unsigned row_off(const Unit& u, int r, LAS unsigned char* lds) const { return (unsigned)((const LAS int*)(lds + LDS_STAGE + u.q * 4096))[r] * (unsigned)rowbytes; }
;     ...
;             const char* a11 = cur.a1 + (size_t)(t + 1) * kstep;
;             const char* a02 = last ? nxt.a0 : cur.a0 + (size_t)(t + 2) * kstep; const char* a12 = last ? nxt.a1 : cur.a1 + (size_t)(t + 2) * kstep;
;             const char* b02 = last ? nxt.b0 : cur.b0 + (size_t)(t + 2) * kstep; const char* b12 = last ? nxt.b1 : cur.b1 + (size_t)(t + 2) * kstep;
;             G_LDB(B0, 0, 0); G_LDB(B1, 0, 1); G_SCHED; G_LDA(At, 0, 0); G_STAGE(G_SA(1, 1), a11, vA1);
;             if constexpr (GATHER) { if (last) { int tz = tid; asm volatile("" : "+v"(tz));
; #pragma unroll
;                 for (int i = 0; i < 2; ++i) { int R, C; stage_rc(tz * 16 + i * 8192, R, C); gc0[i] = S.row_off(nxt, R, lds) + (unsigned)C * 2u; gc1[i] = S.row_off(nxt, 128 + R, lds) + (unsigned)C * 2u; } } }
;             G_WAIT_L(0); G_BAR; G_MMA(0, 0, At, B0); G_MMA(0, 1, At, B1); G_WAIT_V(8); G_BAR; G_SCHED;
;             G_LDA(At, 0, 1); G_STAGE(G_SB(0, 0), b02, voffB); G_STAGE(G_SB(0, 1), b12, voffB); G_STAGE(G_SA(0, 0), a02, vA0);
;             G_WAIT_L(0); G_BAR; G_MMA(1, 0, At, B0); G_MMA(1, 1, At, B1); G_WAIT_V(8); G_BAR; G_SCHED;
.LBB0_1626:
	s_add_i32 s31, s31, 2
	s_add_u32 s78, s26, s74
	s_addc_u32 s79, s27, s75
	s_add_u32 s80, s62, s74
	s_addc_u32 s81, s63, s75
	s_add_u32 s82, s80, 0x100
	s_addc_u32 s83, s81, 0
	s_add_u32 s80, s36, s74
	s_addc_u32 s81, s37, s75
	s_add_u32 vcc_lo, s87, s74
	s_waitcnt lgkmcnt(0)
	s_addc_u32 vcc_hi, s90, s75
	s_and_b64 s[76:77], s[76:77], exec
	s_cselect_b32 s79, s57, s79
	s_cselect_b32 s78, s56, s78
	s_cselect_b32 s81, s51, s81
	s_cselect_b32 s80, s50, s80
	s_cselect_b32 s77, s55, s83
	s_cselect_b32 s76, s54, s82
	s_cselect_b32 s83, s53, vcc_hi
	s_cselect_b32 s82, s52, vcc_lo
	s_barrier
	s_setprio 1
	s_waitcnt lgkmcnt(0)
	v_mfma_i32_16x16x64_i8 v[156:159], v[88:91], v[184:187], v[156:159]
	v_mfma_i32_16x16x64_i8 v[148:151], v[96:99], v[184:187], v[148:151]
	v_mfma_i32_16x16x64_i8 v[140:143], v[88:91], v[176:179], v[140:143]
	v_mfma_i32_16x16x64_i8 v[132:135], v[96:99], v[176:179], v[132:135]
	v_mfma_i32_16x16x64_i8 v[124:127], v[88:91], v[168:171], v[124:127]
	v_mfma_i32_16x16x64_i8 v[116:119], v[96:99], v[168:171], v[116:119]
	v_mfma_i32_16x16x64_i8 v[108:111], v[88:91], v[160:163], v[108:111]
	v_mfma_i32_16x16x64_i8 v[84:87], v[96:99], v[160:163], v[84:87]
	v_mfma_i32_16x16x64_i8 v[156:159], v[92:95], v[188:191], v[156:159]
	v_mfma_i32_16x16x64_i8 v[148:151], v[100:103], v[188:191], v[148:151]
	v_mfma_i32_16x16x64_i8 v[140:143], v[92:95], v[180:183], v[140:143]
	v_mfma_i32_16x16x64_i8 v[132:135], v[100:103], v[180:183], v[132:135]
	v_mfma_i32_16x16x64_i8 v[124:127], v[92:95], v[172:175], v[124:127]
	v_mfma_i32_16x16x64_i8 v[116:119], v[100:103], v[172:175], v[116:119]
	v_mfma_i32_16x16x64_i8 v[108:111], v[92:95], v[164:167], v[108:111]
	v_mfma_i32_16x16x64_i8 v[84:87], v[100:103], v[164:167], v[84:87]
	v_mfma_i32_16x16x64_i8 v[152:155], v[64:67], v[184:187], v[152:155]
	v_mfma_i32_16x16x64_i8 v[144:147], v[72:75], v[184:187], v[144:147]
	v_mfma_i32_16x16x64_i8 v[136:139], v[64:67], v[176:179], v[136:139]
	v_mfma_i32_16x16x64_i8 v[128:131], v[72:75], v[176:179], v[128:131]
	v_mfma_i32_16x16x64_i8 v[120:123], v[64:67], v[168:171], v[120:123]
	v_mfma_i32_16x16x64_i8 v[112:115], v[72:75], v[168:171], v[112:115]
	v_mfma_i32_16x16x64_i8 v[104:107], v[64:67], v[160:163], v[104:107]
	v_mfma_i32_16x16x64_i8 v[80:83], v[72:75], v[160:163], v[80:83]
	v_mfma_i32_16x16x64_i8 v[152:155], v[68:71], v[188:191], v[152:155]
	v_mfma_i32_16x16x64_i8 v[144:147], v[76:79], v[188:191], v[144:147]
	v_mfma_i32_16x16x64_i8 v[136:139], v[68:71], v[180:183], v[136:139]
	v_mfma_i32_16x16x64_i8 v[128:131], v[76:79], v[180:183], v[128:131]
	v_mfma_i32_16x16x64_i8 v[120:123], v[68:71], v[172:175], v[120:123]
	v_mfma_i32_16x16x64_i8 v[112:115], v[76:79], v[172:175], v[112:115]
	v_mfma_i32_16x16x64_i8 v[104:107], v[68:71], v[164:167], v[104:107]
	v_mfma_i32_16x16x64_i8 v[80:83], v[76:79], v[164:167], v[80:83]
	s_setprio 0
	s_waitcnt vmcnt(8)
	s_barrier
	s_mov_b32 m0, s34
	ds_read_b128 v[160:163], v208 offset:16384
	ds_read_b128 v[164:167], v208 offset:17408
	ds_read_b128 v[168:171], v208 offset:18432
	ds_read_b128 v[172:175], v208 offset:19456
	ds_read_b128 v[176:179], v208 offset:20480
	ds_read_b128 v[180:183], v208 offset:21504
	ds_read_b128 v[184:187], v208 offset:22528
	ds_read_b128 v[188:191], v208 offset:23552
	global_load_lds_dwordx4 v244, s[80:81]
	s_mov_b32 m0, s35
	v_mov_b32_e32 v211, v193
	global_load_lds_dwordx4 v246, s[80:81]
	s_mov_b32 m0, s30
	v_mov_b32_e32 v213, v193
	global_load_lds_dwordx4 v244, s[82:83]
	s_mov_b32 m0, s0
	v_mov_b32_e32 v195, v193
	global_load_lds_dwordx4 v246, s[82:83]
	s_mov_b32 m0, s3
	v_mov_b32_e32 v197, v193
	global_load_lds_dwordx4 v194, s[78:79]
	s_mov_b32 m0, s40
	v_lshl_add_u64 v[214:215], s[80:81], 0, v[244:245]
	global_load_lds_dwordx4 v196, s[78:79]
	s_waitcnt lgkmcnt(0)
	v_lshl_add_u64 v[216:217], s[80:81], 0, v[246:247]
	v_lshl_add_u64 v[210:211], s[82:83], 0, v[244:245]
	v_lshl_add_u64 v[212:213], s[82:83], 0, v[246:247]
	v_lshl_add_u64 v[218:219], s[78:79], 0, v[194:195]
	v_lshl_add_u64 v[220:221], s[78:79], 0, v[196:197]
	s_barrier
	s_setprio 1
	s_waitcnt lgkmcnt(0)
	v_mfma_i32_16x16x64_i8 v[60:63], v[88:91], v[160:163], v[60:63]
	v_mfma_i32_16x16x64_i8 v[52:55], v[96:99], v[160:163], v[52:55]
	v_mfma_i32_16x16x64_i8 v[44:47], v[88:91], v[168:171], v[44:47]
	v_mfma_i32_16x16x64_i8 v[36:39], v[96:99], v[168:171], v[36:39]
	v_mfma_i32_16x16x64_i8 v[28:31], v[88:91], v[176:179], v[28:31]
	v_mfma_i32_16x16x64_i8 v[20:23], v[96:99], v[176:179], v[20:23]
	v_mfma_i32_16x16x64_i8 v[12:15], v[88:91], v[184:187], v[12:15]
	v_mfma_i32_16x16x64_i8 v[4:7], v[96:99], v[184:187], v[4:7]
	v_mfma_i32_16x16x64_i8 v[60:63], v[92:95], v[164:167], v[60:63]
	v_mfma_i32_16x16x64_i8 v[52:55], v[100:103], v[164:167], v[52:55]
	v_mfma_i32_16x16x64_i8 v[44:47], v[92:95], v[172:175], v[44:47]
	v_mfma_i32_16x16x64_i8 v[36:39], v[100:103], v[172:175], v[36:39]
	v_mfma_i32_16x16x64_i8 v[28:31], v[92:95], v[180:183], v[28:31]
	v_mfma_i32_16x16x64_i8 v[20:23], v[100:103], v[180:183], v[20:23]
	v_mfma_i32_16x16x64_i8 v[12:15], v[92:95], v[188:191], v[12:15]
	v_mfma_i32_16x16x64_i8 v[4:7], v[100:103], v[188:191], v[4:7]
	v_mfma_i32_16x16x64_i8 v[56:59], v[64:67], v[160:163], v[56:59]
	v_mfma_i32_16x16x64_i8 v[48:51], v[72:75], v[160:163], v[48:51]
	v_mfma_i32_16x16x64_i8 v[40:43], v[64:67], v[168:171], v[40:43]
	v_mfma_i32_16x16x64_i8 v[32:35], v[72:75], v[168:171], v[32:35]
	v_mfma_i32_16x16x64_i8 v[24:27], v[64:67], v[176:179], v[24:27]
	v_mfma_i32_16x16x64_i8 v[16:19], v[72:75], v[176:179], v[16:19]
	v_mfma_i32_16x16x64_i8 v[8:11], v[64:67], v[184:187], v[8:11]
	v_mfma_i32_16x16x64_i8 v[0:3], v[72:75], v[184:187], v[0:3]
	v_mfma_i32_16x16x64_i8 v[56:59], v[68:71], v[164:167], v[56:59]
	v_mfma_i32_16x16x64_i8 v[48:51], v[76:79], v[164:167], v[48:51]
	v_mfma_i32_16x16x64_i8 v[40:43], v[68:71], v[172:175], v[40:43]
	v_mfma_i32_16x16x64_i8 v[32:35], v[76:79], v[172:175], v[32:35]
	v_mfma_i32_16x16x64_i8 v[24:27], v[68:71], v[180:183], v[24:27]
	v_mfma_i32_16x16x64_i8 v[16:19], v[76:79], v[180:183], v[16:19]
	v_mfma_i32_16x16x64_i8 v[8:11], v[68:71], v[188:191], v[8:11]
	v_mfma_i32_16x16x64_i8 v[0:3], v[76:79], v[188:191], v[0:3]
	s_setprio 0
	s_waitcnt vmcnt(8)
	s_barrier
; #define G_STAGE(bufoff, gbase, voff) do { _Pragma("unroll") for (int _i = 0; _i < 2; ++_i) \
;         __builtin_amdgcn_global_load_lds((const unsigned*)((const char*)(gbase) + (voff)[_i]), (LAS unsigned*)(lds + (bufoff) + ldsw + _i * 8192), 16, 0, 0); } while (0)
; #define G_LDA(dst, b, h) do { _Pragma("unroll") for (int m = 0; m < 4; ++m) G_LD8(dst[m], lds + G_SA(b, h) + aoff + m * 2048); } while (0)
; #define G_LDB(dst, b, h) do { _Pragma("unroll") for (int n = 0; n < 2; ++n) G_LD8(dst[n], lds + G_SB(b, h) + boff + n * 2048); } while (0)
; #define G_WAIT_V(n) asm volatile("s_waitcnt vmcnt(" #n ")" ::: "memory")
; #define G_WAIT_L(n) asm volatile("s_waitcnt lgkmcnt(" #n ")" ::: "memory")
; #define G_BAR __builtin_amdgcn_s_barrier()
; #define G_SCHED __builtin_amdgcn_sched_barrier(0)
;     ...
;             G_LDB(B0, 1, 0); G_LDB(B1, 1, 1); G_SCHED; G_LDA(At, 1, 0); G_STAGE(G_SA(0, 1), a12, vA1);
;             G_WAIT_L(0); G_BAR; G_MMA(0, 0, At, B0); G_MMA(0, 1, At, B1); G_WAIT_V(8); G_BAR; G_SCHED;
;             G_LDA(At, 1, 1); G_STAGE(G_SB(1, 0), b02 + kstep, voffB); G_STAGE(G_SB(1, 1), b12 + kstep, voffB); G_STAGE(G_SA(1, 0), a02 + kstep, vA0);
;             G_WAIT_L(0); G_BAR; G_MMA(1, 0, At, B0); G_MMA(1, 1, At, B1); G_WAIT_V(8); G_BAR; G_SCHED;
;         }
	s_add_i32 s78, 0, 0x18000
	s_add_i32 s79, 0, 0x1c000
	v_add_u32_e32 v76, s78, v203
	v_add_u32_e32 v100, s79, v203
	ds_read_b128 v[64:67], v76
	ds_read_b128 v[68:71], v76 offset:1024
	ds_read_b128 v[72:75], v76 offset:2048
	ds_read_b128 v[76:79], v76 offset:3072
	ds_read_b128 v[88:91], v100
	ds_read_b128 v[92:95], v100 offset:1024
	ds_read_b128 v[96:99], v100 offset:2048
	ds_read_b128 v[100:103], v100 offset:3072
	s_mov_b32 m0, s41
	v_lshl_add_u64 v[222:223], s[76:77], 0, v[192:193]
	ds_read_b128 v[160:163], v208 offset:32768
	ds_read_b128 v[164:167], v208 offset:33792
	ds_read_b128 v[168:171], v208 offset:34816
	ds_read_b128 v[172:175], v208 offset:35840
	ds_read_b128 v[176:179], v208 offset:36864
	ds_read_b128 v[180:183], v208 offset:37888
	ds_read_b128 v[184:187], v208 offset:38912
	ds_read_b128 v[188:191], v208 offset:39936
	global_load_lds_dwordx4 v[222:223], off
	v_lshl_add_u64 v[222:223], s[76:77], 0, v[198:199]
	s_mov_b32 m0, s18
	s_nop 0
	global_load_lds_dwordx4 v[222:223], off
	s_waitcnt lgkmcnt(0)
	s_barrier
	s_setprio 1
	s_waitcnt lgkmcnt(0)
	v_mfma_i32_16x16x64_i8 v[156:159], v[64:67], v[160:163], v[156:159]
	v_mfma_i32_16x16x64_i8 v[148:151], v[72:75], v[160:163], v[148:151]
	v_mfma_i32_16x16x64_i8 v[140:143], v[64:67], v[168:171], v[140:143]
	v_mfma_i32_16x16x64_i8 v[132:135], v[72:75], v[168:171], v[132:135]
	v_mfma_i32_16x16x64_i8 v[124:127], v[64:67], v[176:179], v[124:127]
	v_mfma_i32_16x16x64_i8 v[116:119], v[72:75], v[176:179], v[116:119]
	v_mfma_i32_16x16x64_i8 v[108:111], v[64:67], v[184:187], v[108:111]
	v_mfma_i32_16x16x64_i8 v[84:87], v[72:75], v[184:187], v[84:87]
	v_mfma_i32_16x16x64_i8 v[156:159], v[68:71], v[164:167], v[156:159]
	v_mfma_i32_16x16x64_i8 v[148:151], v[76:79], v[164:167], v[148:151]
	v_mfma_i32_16x16x64_i8 v[140:143], v[68:71], v[172:175], v[140:143]
	v_mfma_i32_16x16x64_i8 v[132:135], v[76:79], v[172:175], v[132:135]
	v_mfma_i32_16x16x64_i8 v[124:127], v[68:71], v[180:183], v[124:127]
	v_mfma_i32_16x16x64_i8 v[116:119], v[76:79], v[180:183], v[116:119]
	v_mfma_i32_16x16x64_i8 v[108:111], v[68:71], v[188:191], v[108:111]
	v_mfma_i32_16x16x64_i8 v[84:87], v[76:79], v[188:191], v[84:87]
	v_mfma_i32_16x16x64_i8 v[152:155], v[88:91], v[160:163], v[152:155]
	v_mfma_i32_16x16x64_i8 v[144:147], v[96:99], v[160:163], v[144:147]
	v_mfma_i32_16x16x64_i8 v[136:139], v[88:91], v[168:171], v[136:139]
	v_mfma_i32_16x16x64_i8 v[128:131], v[96:99], v[168:171], v[128:131]
	v_mfma_i32_16x16x64_i8 v[120:123], v[88:91], v[176:179], v[120:123]
	v_mfma_i32_16x16x64_i8 v[112:115], v[96:99], v[176:179], v[112:115]
	v_mfma_i32_16x16x64_i8 v[104:107], v[88:91], v[184:187], v[104:107]
	v_mfma_i32_16x16x64_i8 v[80:83], v[96:99], v[184:187], v[80:83]
	v_mfma_i32_16x16x64_i8 v[152:155], v[92:95], v[164:167], v[152:155]
	v_mfma_i32_16x16x64_i8 v[144:147], v[100:103], v[164:167], v[144:147]
	v_mfma_i32_16x16x64_i8 v[136:139], v[92:95], v[172:175], v[136:139]
	v_mfma_i32_16x16x64_i8 v[128:131], v[100:103], v[172:175], v[128:131]
	v_mfma_i32_16x16x64_i8 v[120:123], v[92:95], v[180:183], v[120:123]
	v_mfma_i32_16x16x64_i8 v[112:115], v[100:103], v[180:183], v[112:115]
	v_mfma_i32_16x16x64_i8 v[104:107], v[92:95], v[188:191], v[104:107]
	v_mfma_i32_16x16x64_i8 v[80:83], v[100:103], v[188:191], v[80:83]
	s_setprio 0
	s_waitcnt vmcnt(8)
	s_barrier
	s_add_i32 s76, s78, s93
	v_lshl_add_u64 v[214:215], v[214:215], 0, s[44:45]
	s_mov_b32 m0, s76
	ds_read_b128 v[160:163], v208 offset:49152
	ds_read_b128 v[164:167], v208 offset:50176
	ds_read_b128 v[168:171], v208 offset:51200
	ds_read_b128 v[172:175], v208 offset:52224
	ds_read_b128 v[176:179], v208 offset:53248
	ds_read_b128 v[180:183], v208 offset:54272
	ds_read_b128 v[184:187], v208 offset:55296
	ds_read_b128 v[188:191], v208 offset:56320
	global_load_lds_dwordx4 v[214:215], off
	v_lshl_add_u64 v[214:215], v[216:217], 0, s[44:45]
	s_add_i32 m0, s76, 0x2000
	s_add_i32 s76, s79, s93
	global_load_lds_dwordx4 v[214:215], off
	v_lshl_add_u64 v[210:211], v[210:211], 0, s[44:45]
	s_mov_b32 m0, s76
	s_nop 0
	global_load_lds_dwordx4 v[210:211], off
	v_lshl_add_u64 v[210:211], v[212:213], 0, s[44:45]
	s_add_i32 m0, s76, 0x2000
	s_nop 0
	global_load_lds_dwordx4 v[210:211], off
	v_lshl_add_u64 v[210:211], v[218:219], 0, s[44:45]
	s_mov_b32 m0, s19
	s_nop 0
	global_load_lds_dwordx4 v[210:211], off
	v_lshl_add_u64 v[210:211], v[220:221], 0, s[44:45]
	s_mov_b32 m0, s89
	s_nop 0
	global_load_lds_dwordx4 v[210:211], off
	s_waitcnt lgkmcnt(0)
	s_barrier
	s_setprio 1
	s_waitcnt lgkmcnt(0)
	v_mfma_i32_16x16x64_i8 v[60:63], v[64:67], v[160:163], v[60:63]
	v_mfma_i32_16x16x64_i8 v[52:55], v[72:75], v[160:163], v[52:55]
	v_mfma_i32_16x16x64_i8 v[44:47], v[64:67], v[168:171], v[44:47]
	v_mfma_i32_16x16x64_i8 v[36:39], v[72:75], v[168:171], v[36:39]
	v_mfma_i32_16x16x64_i8 v[28:31], v[64:67], v[176:179], v[28:31]
	v_mfma_i32_16x16x64_i8 v[20:23], v[72:75], v[176:179], v[20:23]
	v_mfma_i32_16x16x64_i8 v[12:15], v[64:67], v[184:187], v[12:15]
	v_mfma_i32_16x16x64_i8 v[4:7], v[72:75], v[184:187], v[4:7]
	v_mfma_i32_16x16x64_i8 v[60:63], v[68:71], v[164:167], v[60:63]
	v_mfma_i32_16x16x64_i8 v[52:55], v[76:79], v[164:167], v[52:55]
	v_mfma_i32_16x16x64_i8 v[44:47], v[68:71], v[172:175], v[44:47]
	v_mfma_i32_16x16x64_i8 v[36:39], v[76:79], v[172:175], v[36:39]
	v_mfma_i32_16x16x64_i8 v[28:31], v[68:71], v[180:183], v[28:31]
	v_mfma_i32_16x16x64_i8 v[20:23], v[76:79], v[180:183], v[20:23]
	v_mfma_i32_16x16x64_i8 v[12:15], v[68:71], v[188:191], v[12:15]
	v_mfma_i32_16x16x64_i8 v[4:7], v[76:79], v[188:191], v[4:7]
	v_mfma_i32_16x16x64_i8 v[56:59], v[88:91], v[160:163], v[56:59]
	v_mfma_i32_16x16x64_i8 v[48:51], v[96:99], v[160:163], v[48:51]
	v_mfma_i32_16x16x64_i8 v[40:43], v[88:91], v[168:171], v[40:43]
	v_mfma_i32_16x16x64_i8 v[32:35], v[96:99], v[168:171], v[32:35]
	v_mfma_i32_16x16x64_i8 v[24:27], v[88:91], v[176:179], v[24:27]
	v_mfma_i32_16x16x64_i8 v[16:19], v[96:99], v[176:179], v[16:19]
	v_mfma_i32_16x16x64_i8 v[8:11], v[88:91], v[184:187], v[8:11]
	v_mfma_i32_16x16x64_i8 v[0:3], v[96:99], v[184:187], v[0:3]
	v_mfma_i32_16x16x64_i8 v[56:59], v[92:95], v[164:167], v[56:59]
	v_mfma_i32_16x16x64_i8 v[48:51], v[100:103], v[164:167], v[48:51]
	v_mfma_i32_16x16x64_i8 v[40:43], v[92:95], v[172:175], v[40:43]
	v_mfma_i32_16x16x64_i8 v[32:35], v[100:103], v[172:175], v[32:35]
	v_mfma_i32_16x16x64_i8 v[24:27], v[92:95], v[180:183], v[24:27]
	v_mfma_i32_16x16x64_i8 v[16:19], v[100:103], v[180:183], v[16:19]
	v_mfma_i32_16x16x64_i8 v[8:11], v[92:95], v[188:191], v[8:11]
	v_mfma_i32_16x16x64_i8 v[0:3], v[100:103], v[188:191], v[0:3]
	s_setprio 0
	s_waitcnt vmcnt(8)
	s_barrier
	s_add_u32 s74, s74, 0x100
	s_addc_u32 s75, s75, 0
	s_cmp_ge_i32 s31, s33
	s_cbranch_scc1 .LBB0_1639

; #define G_STAGE(bufoff, gbase, voff) do { _Pragma("unroll") for (int _i = 0; _i < 2; ++_i) \
;         __builtin_amdgcn_global_load_lds((const unsigned*)((const char*)(gbase) + (voff)[_i]), (LAS unsigned*)(lds + (bufoff) + ldsw + _i * 8192), 16, 0, 0); } while (0)
; #define G_LDA(dst, b, h) do { _Pragma("unroll") for (int m = 0; m < 4; ++m) G_LD8(dst[m], lds + G_SA(b, h) + aoff + m * 2048); } while (0)
; #define G_LDB(dst, b, h) do { _Pragma("unroll") for (int n = 0; n < 2; ++n) G_LD8(dst[n], lds + G_SB(b, h) + boff + n * 2048); } while (0)
; #define G_WAIT_V(n) asm volatile("s_waitcnt vmcnt(" #n ")" ::: "memory")
; #define G_WAIT_L(n) asm volatile("s_waitcnt lgkmcnt(" #n ")" ::: "memory")
; #define G_BAR __builtin_amdgcn_s_barrier()
; #define G_SCHED __builtin_amdgcn_sched_barrier(0)
;     __device__ __forceinline__ unsigned row_off(const Unit& u, int r, LAS unsigned char* lds) const { return (unsigned)((const LAS int*)(lds + LDS_STAGE + u.q * 4096))[r] * (unsigned)rowbytes; }
;     ...
;             const char* a11 = cur.a1 + (size_t)(t + 1) * kstep;
;             const char* a02 = last ? nxt.a0 : cur.a0 + (size_t)(t + 2) * kstep; const char* a12 = last ? nxt.a1 : cur.a1 + (size_t)(t + 2) * kstep;
;             const char* b02 = last ? nxt.b0 : cur.b0 + (size_t)(t + 2) * kstep; const char* b12 = last ? nxt.b1 : cur.b1 + (size_t)(t + 2) * kstep;
;             G_LDB(B0, 0, 0); G_LDB(B1, 0, 1); G_SCHED; G_LDA(At, 0, 0); G_STAGE(G_SA(1, 1), a11, vA1);
;             if constexpr (GATHER) { if (last) { int tz = tid; asm volatile("" : "+v"(tz));
; #pragma unroll
;                 for (int i = 0; i < 2; ++i) { int R, C; stage_rc(tz * 16 + i * 8192, R, C); gc0[i] = S.row_off(nxt, R, lds) + (unsigned)C * 2u; gc1[i] = S.row_off(nxt, 128 + R, lds) + (unsigned)C * 2u; } } }
;             G_WAIT_L(0); G_BAR; G_MMA(0, 0, At, B0); G_MMA(0, 1, At, B1); G_WAIT_V(8); G_BAR; G_SCHED;
;             G_LDA(At, 0, 1); G_STAGE(G_SB(0, 0), b02, voffB); G_STAGE(G_SB(0, 1), b12, voffB); G_STAGE(G_SA(0, 0), a02, vA0);
.LBB0_1733:
	s_add_i32 s81, s80, 2
	s_add_u32 s52, s78, s48
	s_addc_u32 s53, s79, s49
	s_add_u32 s58, s44, s48
	s_addc_u32 s59, s45, s49
	s_add_u32 s86, s58, 0x100
	v_add_u32_e32 v154, s66, v137
	v_add_u32_e32 v170, s67, v137
	s_addc_u32 s87, s59, 0
	ds_read_b128 v[142:145], v154
	ds_read_b128 v[146:149], v154 offset:1024
	ds_read_b128 v[150:153], v154 offset:2048
	ds_read_b128 v[154:157], v154 offset:3072
	ds_read_b128 v[158:161], v170
	ds_read_b128 v[162:165], v170 offset:1024
	ds_read_b128 v[166:169], v170 offset:2048
	ds_read_b128 v[170:173], v170 offset:3072
	s_add_u32 s56, s29, s48
	s_addc_u32 s57, s75, s49
	s_add_u32 s82, s76, s48
	s_addc_u32 s83, s77, s49
	s_add_i32 s90, s66, s22
	s_add_i32 m0, s23, 0xc000
	s_add_i32 s89, s23, 0xe000
	s_add_i32 s84, s90, 0x2000
	s_cmp_eq_u32 s65, s80
	s_cselect_b32 s55, s37, s53
	s_cselect_b32 s54, s36, s52
	s_cselect_b32 s57, s31, s57
	s_cselect_b32 s56, s30, s56
	s_cselect_b32 s53, s39, s87
	s_cselect_b32 s52, s38, s86
	v_lshl_add_u64 v[206:207], s[58:59], 0, v[128:129]
	v_lshl_add_u64 v[206:207], v[206:207], 0, s[10:11]
	ds_read_b128 v[174:177], v138
	ds_read_b128 v[178:181], v138 offset:1024
	ds_read_b128 v[182:185], v138 offset:2048
	ds_read_b128 v[186:189], v138 offset:3072
	ds_read_b128 v[190:193], v138 offset:4096
	ds_read_b128 v[194:197], v138 offset:5120
	ds_read_b128 v[198:201], v138 offset:6144
	ds_read_b128 v[202:205], v138 offset:7168
	global_load_lds_dwordx4 v[206:207], off
	v_lshl_add_u64 v[206:207], s[58:59], 0, v[130:131]
	v_lshl_add_u64 v[206:207], v[206:207], 0, s[10:11]
	s_mov_b32 m0, s89
	v_mov_b32_e32 v131, v129
	global_load_lds_dwordx4 v[206:207], off
	s_waitcnt lgkmcnt(0)
	s_barrier
	s_setprio 1
	s_waitcnt lgkmcnt(0)
	v_mfma_scale_f32_16x16x128_f8f6f4 v[124:127], v[142:149], v[174:181], v[124:127], v139, v139 op_sel_hi:[0,0,0]
	v_mfma_scale_f32_16x16x128_f8f6f4 v[120:123], v[150:157], v[174:181], v[120:123], v139, v139 op_sel_hi:[0,0,0]
	v_mfma_scale_f32_16x16x128_f8f6f4 v[116:119], v[142:149], v[182:189], v[116:119], v139, v139 op_sel_hi:[0,0,0]
	v_mfma_scale_f32_16x16x128_f8f6f4 v[112:115], v[150:157], v[182:189], v[112:115], v139, v139 op_sel_hi:[0,0,0]
	v_mfma_scale_f32_16x16x128_f8f6f4 v[108:111], v[142:149], v[190:197], v[108:111], v139, v139 op_sel_hi:[0,0,0]
	v_mfma_scale_f32_16x16x128_f8f6f4 v[104:107], v[150:157], v[190:197], v[104:107], v139, v139 op_sel_hi:[0,0,0]
	v_mfma_scale_f32_16x16x128_f8f6f4 v[100:103], v[142:149], v[198:205], v[100:103], v139, v139 op_sel_hi:[0,0,0]
	v_mfma_scale_f32_16x16x128_f8f6f4 v[96:99], v[150:157], v[198:205], v[96:99], v139, v139 op_sel_hi:[0,0,0]
	v_mfma_scale_f32_16x16x128_f8f6f4 v[206:209], v[158:165], v[174:181], v[60:63], v139, v139 op_sel_hi:[0,0,0]
	v_mfma_scale_f32_16x16x128_f8f6f4 v[174:177], v[166:173], v[174:181], v[56:59], v139, v139 op_sel_hi:[0,0,0]
	v_mfma_scale_f32_16x16x128_f8f6f4 v[178:181], v[158:165], v[182:189], v[52:55], v139, v139 op_sel_hi:[0,0,0]
	v_mfma_scale_f32_16x16x128_f8f6f4 v[182:185], v[166:173], v[182:189], v[48:51], v139, v139 op_sel_hi:[0,0,0]
	v_mfma_scale_f32_16x16x128_f8f6f4 v[186:189], v[158:165], v[190:197], v[44:47], v139, v139 op_sel_hi:[0,0,0]
	v_mfma_scale_f32_16x16x128_f8f6f4 v[190:193], v[166:173], v[190:197], v[40:43], v139, v139 op_sel_hi:[0,0,0]
	v_mfma_scale_f32_16x16x128_f8f6f4 v[194:197], v[158:165], v[198:205], v[36:39], v139, v139 op_sel_hi:[0,0,0]
	v_mfma_scale_f32_16x16x128_f8f6f4 v[198:201], v[166:173], v[198:205], v[32:35], v139, v139 op_sel_hi:[0,0,0]
	s_setprio 0
	s_waitcnt vmcnt(8)
	s_barrier
	s_mov_b32 m0, s90
	s_nop 3
	ds_read_b128 v[32:35], v138 offset:16384
	ds_read_b128 v[36:39], v138 offset:17408
	ds_read_b128 v[40:43], v138 offset:18432
	ds_read_b128 v[44:47], v138 offset:19456
	ds_read_b128 v[48:51], v138 offset:20480
	ds_read_b128 v[52:55], v138 offset:21504
	ds_read_b128 v[56:59], v138 offset:22528
	ds_read_b128 v[60:63], v138 offset:23552
	global_load_lds_dwordx4 v132, s[56:57]
	s_mov_b32 m0, s84
	s_cselect_b32 s59, s35, s83
	s_cselect_b32 s58, s34, s82
	s_add_i32 s80, s67, s22
	s_add_u32 s98, s56, 0x20000
	s_addc_u32 s99, s57, 0
	global_load_lds_dwordx4 v132, s[98:99]
	s_mov_b32 m0, s80
	v_mov_b32_e32 v133, v129
	global_load_lds_dwordx4 v132, s[58:59]
	s_add_i32 m0, s80, 0x2000
	s_add_u32 s100, s58, 0x20000
	s_addc_u32 s101, s59, 0
	global_load_lds_dwordx4 v132, s[100:101]
	s_mov_b32 m0, s23
	v_lshl_add_u64 v[246:247], s[56:57], 0, v[132:133]
	global_load_lds_dwordx4 v128, s[54:55]
	s_mov_b32 m0, s24
	v_lshl_add_u64 v[248:249], s[98:99], 0, v[132:133]
	global_load_lds_dwordx4 v130, s[54:55]
	s_waitcnt lgkmcnt(0)
	v_lshl_add_u64 v[250:251], s[100:101], 0, v[132:133]
	v_lshl_add_u64 v[252:253], s[54:55], 0, v[128:129]
	v_lshl_add_u64 v[134:135], s[54:55], 0, v[130:131]
	s_barrier
; #define G_STAGE(bufoff, gbase, voff) do { _Pragma("unroll") for (int _i = 0; _i < 2; ++_i) \
;         __builtin_amdgcn_global_load_lds((const unsigned*)((const char*)(gbase) + (voff)[_i]), (LAS unsigned*)(lds + (bufoff) + ldsw + _i * 8192), 16, 0, 0); } while (0)
; #define G_LDA(dst, b, h) do { _Pragma("unroll") for (int m = 0; m < 4; ++m) G_LD8(dst[m], lds + G_SA(b, h) + aoff + m * 2048); } while (0)
; #define G_LDB(dst, b, h) do { _Pragma("unroll") for (int n = 0; n < 2; ++n) G_LD8(dst[n], lds + G_SB(b, h) + boff + n * 2048); } while (0)
; #define G_WAIT_V(n) asm volatile("s_waitcnt vmcnt(" #n ")" ::: "memory")
; #define G_WAIT_L(n) asm volatile("s_waitcnt lgkmcnt(" #n ")" ::: "memory")
; #define G_BAR __builtin_amdgcn_s_barrier()
; #define G_SCHED __builtin_amdgcn_sched_barrier(0)
;     ...
;             G_WAIT_L(0); G_BAR; G_MMA(1, 0, At, B0); G_MMA(1, 1, At, B1); G_WAIT_V(8); G_BAR; G_SCHED;
;             G_LDB(B0, 1, 0); G_LDB(B1, 1, 1); G_SCHED; G_LDA(At, 1, 0); G_STAGE(G_SA(0, 1), a12, vA1);
;             G_WAIT_L(0); G_BAR; G_MMA(0, 0, At, B0); G_MMA(0, 1, At, B1); G_WAIT_V(8); G_BAR; G_SCHED;
	s_setprio 1
	s_waitcnt lgkmcnt(0)
	v_mfma_scale_f32_16x16x128_f8f6f4 v[92:95], v[142:149], v[32:39], v[92:95], v139, v139 op_sel_hi:[0,0,0]
	v_mfma_scale_f32_16x16x128_f8f6f4 v[88:91], v[150:157], v[32:39], v[88:91], v139, v139 op_sel_hi:[0,0,0]
	v_mfma_scale_f32_16x16x128_f8f6f4 v[84:87], v[142:149], v[40:47], v[84:87], v139, v139 op_sel_hi:[0,0,0]
	v_mfma_scale_f32_16x16x128_f8f6f4 v[80:83], v[150:157], v[40:47], v[80:83], v139, v139 op_sel_hi:[0,0,0]
	v_mfma_scale_f32_16x16x128_f8f6f4 v[76:79], v[142:149], v[48:55], v[76:79], v139, v139 op_sel_hi:[0,0,0]
	v_mfma_scale_f32_16x16x128_f8f6f4 v[72:75], v[150:157], v[48:55], v[72:75], v139, v139 op_sel_hi:[0,0,0]
	v_mfma_scale_f32_16x16x128_f8f6f4 v[202:205], v[142:149], v[56:63], v[68:71], v139, v139 op_sel_hi:[0,0,0]
	v_mfma_scale_f32_16x16x128_f8f6f4 v[210:213], v[150:157], v[56:63], v[64:67], v139, v139 op_sel_hi:[0,0,0]
	v_mfma_scale_f32_16x16x128_f8f6f4 v[214:217], v[158:165], v[32:39], v[28:31], v139, v139 op_sel_hi:[0,0,0]
	v_mfma_scale_f32_16x16x128_f8f6f4 v[218:221], v[166:173], v[32:39], v[24:27], v139, v139 op_sel_hi:[0,0,0]
	v_mfma_scale_f32_16x16x128_f8f6f4 v[222:225], v[158:165], v[40:47], v[20:23], v139, v139 op_sel_hi:[0,0,0]
	v_mfma_scale_f32_16x16x128_f8f6f4 v[226:229], v[166:173], v[40:47], v[16:19], v139, v139 op_sel_hi:[0,0,0]
	v_mfma_scale_f32_16x16x128_f8f6f4 v[230:233], v[158:165], v[48:55], v[12:15], v139, v139 op_sel_hi:[0,0,0]
	v_mfma_scale_f32_16x16x128_f8f6f4 v[234:237], v[166:173], v[48:55], v[8:11], v139, v139 op_sel_hi:[0,0,0]
	v_mfma_scale_f32_16x16x128_f8f6f4 v[238:241], v[158:165], v[56:63], v[4:7], v139, v139 op_sel_hi:[0,0,0]
	v_mfma_scale_f32_16x16x128_f8f6f4 v[242:245], v[166:173], v[56:63], v[0:3], v139, v139 op_sel_hi:[0,0,0]
	s_setprio 0
	s_waitcnt vmcnt(8)
	s_barrier
	s_add_i32 s54, 0, 0x18000
	s_add_i32 s55, 0, 0x1c000
	v_add_u32_e32 v12, s54, v137
	v_add_u32_e32 v16, s55, v137
	s_nop 0
	ds_read_b128 v[0:3], v12
	ds_read_b128 v[4:7], v12 offset:1024
	ds_read_b128 v[8:11], v12 offset:2048
	ds_read_b128 v[12:15], v12 offset:3072
	ds_read_b128 v[142:145], v16
	ds_read_b128 v[146:149], v16 offset:1024
	ds_read_b128 v[150:153], v16 offset:2048
	ds_read_b128 v[154:157], v16 offset:3072
	s_mov_b32 m0, s25
	ds_read_b128 v[16:19], v138 offset:32768
	ds_read_b128 v[20:23], v138 offset:33792
	ds_read_b128 v[24:27], v138 offset:34816
	ds_read_b128 v[28:31], v138 offset:35840
	ds_read_b128 v[32:35], v138 offset:36864
	ds_read_b128 v[36:39], v138 offset:37888
	ds_read_b128 v[64:67], v138 offset:38912
	ds_read_b128 v[68:71], v138 offset:39936
	global_load_lds_dwordx4 v128, s[52:53]
	s_mov_b32 m0, s26
	s_nop 0
	global_load_lds_dwordx4 v130, s[52:53]
	s_waitcnt lgkmcnt(0)
	s_barrier
	s_setprio 1
	s_waitcnt lgkmcnt(0)
	v_mfma_scale_f32_16x16x128_f8f6f4 v[124:127], v[0:7], v[16:23], v[124:127], v139, v139 op_sel_hi:[0,0,0]
	v_mfma_scale_f32_16x16x128_f8f6f4 v[120:123], v[8:15], v[16:23], v[120:123], v139, v139 op_sel_hi:[0,0,0]
	v_mfma_scale_f32_16x16x128_f8f6f4 v[116:119], v[0:7], v[24:31], v[116:119], v139, v139 op_sel_hi:[0,0,0]
	v_mfma_scale_f32_16x16x128_f8f6f4 v[112:115], v[8:15], v[24:31], v[112:115], v139, v139 op_sel_hi:[0,0,0]
	v_mfma_scale_f32_16x16x128_f8f6f4 v[108:111], v[0:7], v[32:39], v[108:111], v139, v139 op_sel_hi:[0,0,0]
	v_mfma_scale_f32_16x16x128_f8f6f4 v[104:107], v[8:15], v[32:39], v[104:107], v139, v139 op_sel_hi:[0,0,0]
	v_mfma_scale_f32_16x16x128_f8f6f4 v[100:103], v[0:7], v[64:71], v[100:103], v139, v139 op_sel_hi:[0,0,0]
	v_mfma_scale_f32_16x16x128_f8f6f4 v[96:99], v[8:15], v[64:71], v[96:99], v139, v139 op_sel_hi:[0,0,0]
	v_mfma_scale_f32_16x16x128_f8f6f4 v[60:63], v[142:149], v[16:23], v[206:209], v139, v139 op_sel_hi:[0,0,0]
	v_mfma_scale_f32_16x16x128_f8f6f4 v[56:59], v[150:157], v[16:23], v[174:177], v139, v139 op_sel_hi:[0,0,0]
	v_mfma_scale_f32_16x16x128_f8f6f4 v[52:55], v[142:149], v[24:31], v[178:181], v139, v139 op_sel_hi:[0,0,0]
	v_mfma_scale_f32_16x16x128_f8f6f4 v[48:51], v[150:157], v[24:31], v[182:185], v139, v139 op_sel_hi:[0,0,0]
	v_mfma_scale_f32_16x16x128_f8f6f4 v[44:47], v[142:149], v[32:39], v[186:189], v139, v139 op_sel_hi:[0,0,0]
	v_mfma_scale_f32_16x16x128_f8f6f4 v[40:43], v[150:157], v[32:39], v[190:193], v139, v139 op_sel_hi:[0,0,0]
	v_mfma_scale_f32_16x16x128_f8f6f4 v[36:39], v[142:149], v[64:71], v[194:197], v139, v139 op_sel_hi:[0,0,0]
	v_mfma_scale_f32_16x16x128_f8f6f4 v[32:35], v[150:157], v[64:71], v[198:201], v139, v139 op_sel_hi:[0,0,0]
	s_setprio 0
	s_waitcnt vmcnt(8)
	s_barrier
; #define G_STAGE(bufoff, gbase, voff) do { _Pragma("unroll") for (int _i = 0; _i < 2; ++_i) \
;         __builtin_amdgcn_global_load_lds((const unsigned*)((const char*)(gbase) + (voff)[_i]), (LAS unsigned*)(lds + (bufoff) + ldsw + _i * 8192), 16, 0, 0); } while (0)
; #define G_LDA(dst, b, h) do { _Pragma("unroll") for (int m = 0; m < 4; ++m) G_LD8(dst[m], lds + G_SA(b, h) + aoff + m * 2048); } while (0)
; #define G_WAIT_V(n) asm volatile("s_waitcnt vmcnt(" #n ")" ::: "memory")
; #define G_WAIT_L(n) asm volatile("s_waitcnt lgkmcnt(" #n ")" ::: "memory")
; #define G_BAR __builtin_amdgcn_s_barrier()
; #define G_SCHED __builtin_amdgcn_sched_barrier(0)
;     ...
;             G_LDA(At, 1, 1); G_STAGE(G_SB(1, 0), b02 + kstep, voffB); G_STAGE(G_SB(1, 1), b12 + kstep, voffB); G_STAGE(G_SA(1, 0), a02 + kstep, vA0);
;             G_WAIT_L(0); G_BAR; G_MMA(1, 0, At, B0); G_MMA(1, 1, At, B1); G_WAIT_V(8); G_BAR; G_SCHED;
;         }
	s_add_i32 s52, s54, s22
	v_lshl_add_u64 v[24:25], v[246:247], 0, s[10:11]
	s_mov_b32 m0, s52
	ds_read_b128 v[16:19], v138 offset:49152
	ds_read_b128 v[20:23], v138 offset:50176
	ds_read_b128 v[158:161], v138 offset:51200
	ds_read_b128 v[162:165], v138 offset:52224
	ds_read_b128 v[166:169], v138 offset:53248
	ds_read_b128 v[170:173], v138 offset:54272
	ds_read_b128 v[174:177], v138 offset:55296
	ds_read_b128 v[178:181], v138 offset:56320
	global_load_lds_dwordx4 v[24:25], off
	v_lshl_add_u64 v[24:25], v[248:249], 0, s[10:11]
	s_add_i32 m0, s52, 0x2000
	s_add_i32 s52, s55, s22
	s_sub_u32 s98, s10, 0x20000
	s_subb_u32 s99, s11, 0
	global_load_lds_dwordx4 v[24:25], off
	v_lshl_add_u64 v[24:25], v[250:251], 0, s[98:99]
	s_mov_b32 m0, s52
	s_nop 0
	global_load_lds_dwordx4 v[24:25], off
	v_lshl_add_u64 v[24:25], v[250:251], 0, s[10:11]
	s_add_i32 m0, s52, 0x2000
	s_nop 0
	global_load_lds_dwordx4 v[24:25], off
	v_lshl_add_u64 v[24:25], v[252:253], 0, s[10:11]
	s_mov_b32 m0, s62
	s_nop 0
	global_load_lds_dwordx4 v[24:25], off
	v_lshl_add_u64 v[24:25], v[134:135], 0, s[10:11]
	s_mov_b32 m0, s63
	s_nop 0
	global_load_lds_dwordx4 v[24:25], off
	s_waitcnt lgkmcnt(0)
	s_barrier
	s_setprio 1
	s_waitcnt lgkmcnt(0)
	v_mfma_scale_f32_16x16x128_f8f6f4 v[92:95], v[0:7], v[16:23], v[92:95], v139, v139 op_sel_hi:[0,0,0]
	v_mfma_scale_f32_16x16x128_f8f6f4 v[88:91], v[8:15], v[16:23], v[88:91], v139, v139 op_sel_hi:[0,0,0]
	v_mfma_scale_f32_16x16x128_f8f6f4 v[84:87], v[0:7], v[158:165], v[84:87], v139, v139 op_sel_hi:[0,0,0]
	v_mfma_scale_f32_16x16x128_f8f6f4 v[80:83], v[8:15], v[158:165], v[80:83], v139, v139 op_sel_hi:[0,0,0]
	v_mfma_scale_f32_16x16x128_f8f6f4 v[76:79], v[0:7], v[166:173], v[76:79], v139, v139 op_sel_hi:[0,0,0]
	v_mfma_scale_f32_16x16x128_f8f6f4 v[72:75], v[8:15], v[166:173], v[72:75], v139, v139 op_sel_hi:[0,0,0]
	v_mfma_scale_f32_16x16x128_f8f6f4 v[68:71], v[0:7], v[174:181], v[202:205], v139, v139 op_sel_hi:[0,0,0]
	v_mfma_scale_f32_16x16x128_f8f6f4 v[64:67], v[8:15], v[174:181], v[210:213], v139, v139 op_sel_hi:[0,0,0]
	v_mfma_scale_f32_16x16x128_f8f6f4 v[28:31], v[142:149], v[16:23], v[214:217], v139, v139 op_sel_hi:[0,0,0]
	v_mfma_scale_f32_16x16x128_f8f6f4 v[24:27], v[150:157], v[16:23], v[218:221], v139, v139 op_sel_hi:[0,0,0]
	v_mfma_scale_f32_16x16x128_f8f6f4 v[20:23], v[142:149], v[158:165], v[222:225], v139, v139 op_sel_hi:[0,0,0]
	v_mfma_scale_f32_16x16x128_f8f6f4 v[16:19], v[150:157], v[158:165], v[226:229], v139, v139 op_sel_hi:[0,0,0]
	v_mfma_scale_f32_16x16x128_f8f6f4 v[12:15], v[142:149], v[166:173], v[230:233], v139, v139 op_sel_hi:[0,0,0]
	v_mfma_scale_f32_16x16x128_f8f6f4 v[8:11], v[150:157], v[166:173], v[234:237], v139, v139 op_sel_hi:[0,0,0]
	v_mfma_scale_f32_16x16x128_f8f6f4 v[4:7], v[142:149], v[174:181], v[238:241], v139, v139 op_sel_hi:[0,0,0]
	v_mfma_scale_f32_16x16x128_f8f6f4 v[0:3], v[150:157], v[174:181], v[242:245], v139, v139 op_sel_hi:[0,0,0]
	s_setprio 0
	s_waitcnt vmcnt(8)
	s_barrier
	s_add_u32 s48, s48, 0x100
	s_addc_u32 s49, s49, 0
	s_cmp_ge_i32 s81, s0
	s_cbranch_scc1 .LBB0_1735
	s_mov_b32 s80, s81
	s_branch .LBB0_1724
